# baseline (speedup 1.0000x reference)
_Z5gemm8ILi192ELi2ELi3ELi0ELi1ELi16EEvPKDF16_S1_iiiPDF16_PfPKf:
	v_readfirstlane_b32 s28, v0
	s_nop 3
	s_nop 0
	s_bitcmp1_b32 s28, 8
	s_cbranch_scc0 .Lprio_skip0
	s_setprio 1

.LBB4_4:
	s_load_dword s2, s[0:1], 0x18
	v_lshrrev_b32_e32 v6, 4, v0
	v_xor_b32_e32 v1, v6, v0
	v_lshlrev_b32_e32 v1, 3, v1
	v_and_b32_e32 v2, 56, v1
	v_lshrrev_b32_e32 v1, 3, v0
	s_waitcnt lgkmcnt(0)
	v_mad_u64_u32 v[4:5], s[0:1], v1, s2, v[2:3]
	v_or_b32_e32 v3, 0x200, v0
	v_lshrrev_b32_e32 v3, 3, v3
	s_lshl_b32 s10, s12, 7
	s_ashr_i32 s13, s2, 31
	v_mul_lo_u32 v3, v3, s2
	s_lshl_b32 s0, s2, 7
	v_add_lshl_u32 v2, v3, v2, 1
	v_add_lshl_u32 v3, v4, s0, 1
	s_mul_i32 s0, s10, s13
	s_mul_hi_u32 s1, s10, s2
	s_add_i32 s1, s1, s0
	s_mul_i32 s0, s10, s2
	s_mul_i32 s11, s3, 0xc0
	s_lshl_b64 s[0:1], s[0:1], 1
	v_lshlrev_b32_e32 v122, 4, v0
	v_lshlrev_b32_e32 v1, 1, v4
	s_add_u32 s0, s4, s0
	s_mul_i32 s3, s11, s13
	s_mul_hi_u32 s4, s11, s2
	v_add_u32_e32 v4, 0, v122
	s_addc_u32 s1, s5, s1
	s_add_i32 s3, s4, s3
	s_mul_i32 s2, s11, s2
	v_readfirstlane_b32 s13, v4
	v_add_u32_e32 v5, 0x2000, v4
	s_lshl_b64 s[2:3], s[2:3], 1
	s_mov_b32 m0, s13
	v_readfirstlane_b32 s4, v5
	v_add_u32_e32 v5, 0x4000, v4
	s_add_u32 s2, s6, s2
	global_load_lds_dwordx4 v1, s[0:1]
	s_mov_b32 m0, s4
	v_readfirstlane_b32 s5, v5
	v_add_u32_e32 v5, 0x6000, v4
	s_addc_u32 s3, s7, s3
	global_load_lds_dwordx4 v2, s[0:1]
	s_mov_b32 m0, s5
	v_readfirstlane_b32 s6, v5
	v_add_u32_e32 v5, 0x8000, v4
	global_load_lds_dwordx4 v1, s[2:3]
	s_mov_b32 m0, s6
	v_readfirstlane_b32 s7, v5
	v_add_u32_e32 v5, 0xa000, v4
	global_load_lds_dwordx4 v2, s[2:3]
	s_mov_b32 m0, s7
	s_add_u32 s16, s0, 0x80
	v_readfirstlane_b32 s18, v5
	v_add_u32_e32 v5, 0xc000, v4
	global_load_lds_dwordx4 v3, s[2:3]
	s_addc_u32 s17, s1, 0
	s_mov_b32 m0, s18
	v_readfirstlane_b32 s14, v5
	v_add_u32_e32 v5, 0xe000, v4
	s_add_u32 s20, s2, 0x80
	global_load_lds_dwordx4 v1, s[16:17]
	s_mov_b32 m0, s14
	v_readfirstlane_b32 s15, v5
	v_add_u32_e32 v5, 0x10000, v4
	s_addc_u32 s21, s3, 0
	global_load_lds_dwordx4 v2, s[16:17]
	s_mov_b32 m0, s15
	v_readfirstlane_b32 s16, v5
	v_add_u32_e32 v5, 0x12000, v4
	global_load_lds_dwordx4 v1, s[20:21]
	s_mov_b32 m0, s16
	v_readfirstlane_b32 s17, v5
	global_load_lds_dwordx4 v2, s[20:21]
	s_mov_b32 m0, s17
	v_add_u32_e32 v5, 0x14000, v4
	global_load_lds_dwordx4 v3, s[20:21]
	s_add_u32 s20, s0, 0x100
	v_readfirstlane_b32 s19, v5
	v_add_u32_e32 v5, 0x16000, v4
	s_addc_u32 s21, s1, 0
	s_mov_b32 m0, s19
	v_readfirstlane_b32 s19, v5
	v_add_u32_e32 v5, 0x18000, v4
	s_add_u32 s22, s2, 0x100
	global_load_lds_dwordx4 v1, s[20:21]
	s_mov_b32 m0, s19
	v_readfirstlane_b32 s19, v5
	v_add_u32_e32 v5, 0x1a000, v4
	s_addc_u32 s23, s3, 0
	global_load_lds_dwordx4 v2, s[20:21]
	s_mov_b32 m0, s19
	v_readfirstlane_b32 s19, v5
	v_add_u32_e32 v4, 0x1c000, v4
	global_load_lds_dwordx4 v1, s[22:23]
	s_mov_b32 m0, s19
	v_readfirstlane_b32 s19, v4
	global_load_lds_dwordx4 v2, s[22:23]
	s_mov_b32 m0, s19
	v_and_b32_e32 v8, 15, v0
	global_load_lds_dwordx4 v3, s[22:23]
	v_lshrrev_b32_e32 v11, 2, v0
	v_bfe_u32 v9, v0, 6, 2
	v_bfe_u32 v5, v0, 1, 3
	v_and_or_b32 v4, v11, 64, v8
	v_lshlrev_b32_e32 v123, 7, v4
	v_bitop3_b32 v4, v6, v5, 3 bitop3:0x6c
	v_mul_u32_u24_e32 v10, 48, v9
	v_lshlrev_b32_e32 v6, 4, v4
	v_or_b32_e32 v4, v10, v8
	v_lshlrev_b32_e32 v7, 7, v4
	v_add_u32_e32 v13, 0, v7
	s_waitcnt vmcnt(10)
	s_barrier
	v_add_u32_e32 v4, v13, v6
	ds_read_b128 v[14:17], v4 offset:16384
	v_add_u32_e32 v50, 0, v123
	v_add_u32_e32 v6, v50, v6
	ds_read_b128 v[18:21], v6
	ds_read_b128 v[22:25], v4 offset:18432
	ds_read_b128 v[26:29], v6 offset:2048
	ds_read_b128 v[30:33], v4 offset:20480
	ds_read_b128 v[42:45], v6 offset:4096
	ds_read_b128 v[46:49], v6 offset:6144
	v_bfe_u32 v12, v0, 4, 2
	v_bitop3_b32 v0, v12, v5, 4 bitop3:0x36
	v_lshlrev_b32_e32 v5, 4, v0
	s_add_i32 s19, 0, 0x14000
	v_add_u32_e32 v124, s19, v5
	s_waitcnt lgkmcnt(0)
	v_mfma_f32_16x16x32_f16 v[34:37], v[14:17], v[18:21], 0
	v_add_u32_e32 v7, v7, v124
	v_mfma_f32_16x16x32_f16 v[38:41], v[22:25], v[18:21], 0
	v_mfma_f32_16x16x32_f16 v[18:21], v[30:33], v[18:21], 0
	v_add_u32_e32 v0, v50, v5
	ds_read_b128 v[50:53], v0
	ds_read_b128 v[54:57], v0 offset:2048
	ds_read_b128 v[58:61], v0 offset:4096
	ds_read_b128 v[62:65], v0 offset:6144
	v_add_u32_e32 v5, v13, v5
	ds_read_b128 v[66:69], v5 offset:16384
	ds_read_b128 v[70:73], v5 offset:18432
	ds_read_b128 v[74:77], v5 offset:20480
	v_mfma_f32_16x16x32_f16 v[78:81], v[14:17], v[26:29], 0
	v_mfma_f32_16x16x32_f16 v[82:85], v[22:25], v[26:29], 0
	v_mfma_f32_16x16x32_f16 v[26:29], v[30:33], v[26:29], 0
	v_mfma_f32_16x16x32_f16 v[86:89], v[14:17], v[42:45], 0
	v_mfma_f32_16x16x32_f16 v[90:93], v[22:25], v[42:45], 0
	v_mfma_f32_16x16x32_f16 v[42:45], v[30:33], v[42:45], 0
	v_mfma_f32_16x16x32_f16 v[14:17], v[14:17], v[46:49], 0
	v_mfma_f32_16x16x32_f16 v[22:25], v[22:25], v[46:49], 0
	v_mfma_f32_16x16x32_f16 v[30:33], v[30:33], v[46:49], 0
	s_add_u32 s20, s0, 0x180
	s_mov_b32 m0, s13
	s_waitcnt vmcnt(5) lgkmcnt(0)
	s_barrier
	s_addc_u32 s21, s1, 0
	s_add_u32 s22, s2, 0x180
	global_load_lds_dwordx4 v1, s[20:21]
	s_mov_b32 m0, s4
	s_addc_u32 s23, s3, 0
	global_load_lds_dwordx4 v2, s[20:21]
	s_mov_b32 m0, s5
	s_nop 0
	global_load_lds_dwordx4 v1, s[22:23]
	s_mov_b32 m0, s6
	s_nop 0
	global_load_lds_dwordx4 v2, s[22:23]
	s_mov_b32 m0, s7
	s_nop 0
	global_load_lds_dwordx4 v3, s[22:23]
	s_waitcnt lgkmcnt(0)
	v_mfma_f32_16x16x32_f16 v[34:37], v[66:69], v[50:53], v[34:37]
	v_mfma_f32_16x16x32_f16 v[38:41], v[70:73], v[50:53], v[38:41]
	v_mfma_f32_16x16x32_f16 v[18:21], v[74:77], v[50:53], v[18:21]
	ds_read_b128 v[46:49], v6 offset:40960
	ds_read_b128 v[50:53], v6 offset:43008
	ds_read_b128 v[94:97], v6 offset:45056
	ds_read_b128 v[98:101], v6 offset:47104
	ds_read_b128 v[102:105], v4 offset:57344
	ds_read_b128 v[106:109], v4 offset:59392
	ds_read_b128 v[110:113], v4 offset:61440
	v_mfma_f32_16x16x32_f16 v[78:81], v[66:69], v[54:57], v[78:81]
	v_mfma_f32_16x16x32_f16 v[82:85], v[70:73], v[54:57], v[82:85]
	v_mfma_f32_16x16x32_f16 v[26:29], v[74:77], v[54:57], v[26:29]
	v_mfma_f32_16x16x32_f16 v[54:57], v[66:69], v[58:61], v[86:89]
	v_mfma_f32_16x16x32_f16 v[86:89], v[70:73], v[58:61], v[90:93]
	v_mfma_f32_16x16x32_f16 v[42:45], v[74:77], v[58:61], v[42:45]
	v_mfma_f32_16x16x32_f16 v[14:17], v[66:69], v[62:65], v[14:17]
	v_mfma_f32_16x16x32_f16 v[22:25], v[70:73], v[62:65], v[22:25]
	v_mfma_f32_16x16x32_f16 v[30:33], v[74:77], v[62:65], v[30:33]
	s_waitcnt lgkmcnt(0)
	v_mfma_f32_16x16x32_f16 v[34:37], v[102:105], v[46:49], v[34:37]
	v_mfma_f32_16x16x32_f16 v[38:41], v[106:109], v[46:49], v[38:41]
	v_mfma_f32_16x16x32_f16 v[18:21], v[110:113], v[46:49], v[18:21]
	ds_read_b128 v[46:49], v0 offset:40960
	ds_read_b128 v[58:61], v0 offset:43008
	ds_read_b128 v[62:65], v0 offset:45056
	ds_read_b128 v[66:69], v0 offset:47104
	ds_read_b128 v[70:73], v5 offset:57344
	ds_read_b128 v[74:77], v5 offset:59392
	ds_read_b128 v[90:93], v5 offset:61440
	v_mfma_f32_16x16x32_f16 v[78:81], v[102:105], v[50:53], v[78:81]
	v_mfma_f32_16x16x32_f16 v[82:85], v[106:109], v[50:53], v[82:85]
	v_mfma_f32_16x16x32_f16 v[26:29], v[110:113], v[50:53], v[26:29]
	v_mfma_f32_16x16x32_f16 v[50:53], v[102:105], v[94:97], v[54:57]
	v_mfma_f32_16x16x32_f16 v[54:57], v[106:109], v[94:97], v[86:89]
	v_mfma_f32_16x16x32_f16 v[42:45], v[110:113], v[94:97], v[42:45]
	v_mfma_f32_16x16x32_f16 v[86:89], v[102:105], v[98:101], v[14:17]
	v_mfma_f32_16x16x32_f16 v[22:25], v[106:109], v[98:101], v[22:25]
	v_mfma_f32_16x16x32_f16 v[30:33], v[110:113], v[98:101], v[30:33]
	s_add_u32 s20, s0, 0x200
	s_mov_b32 m0, s18
	s_waitcnt vmcnt(5) lgkmcnt(0)
	s_barrier
	s_addc_u32 s21, s1, 0
	s_add_u32 s22, s2, 0x200
	global_load_lds_dwordx4 v1, s[20:21]
	s_mov_b32 m0, s14
	s_addc_u32 s23, s3, 0
	global_load_lds_dwordx4 v2, s[20:21]
	s_mov_b32 m0, s15
	s_nop 0
	global_load_lds_dwordx4 v1, s[22:23]
	s_mov_b32 m0, s16
	s_nop 0
	global_load_lds_dwordx4 v2, s[22:23]
	s_mov_b32 m0, s17
	s_nop 0
	global_load_lds_dwordx4 v3, s[22:23]
	s_waitcnt lgkmcnt(0)
	v_mfma_f32_16x16x32_f16 v[34:37], v[70:73], v[46:49], v[34:37]
	v_mfma_f32_16x16x32_f16 v[38:41], v[74:77], v[46:49], v[38:41]
	v_mfma_f32_16x16x32_f16 v[46:49], v[90:93], v[46:49], v[18:21]
	v_add_u32_e32 v13, 0x14000, v6
	v_add_u32_e32 v15, 0x15000, v6
	s_nop 0
	v_add_u32_e32 v18, 0x18000, v4
	v_add_u32_e32 v14, 0x14800, v6
	ds_read_b128 v[94:97], v13
	ds_read_b128 v[98:101], v14
	v_add_u32_e32 v16, 0x15800, v6
	ds_read_b128 v[102:105], v15
	ds_read_b128 v[106:109], v16
	v_add_u32_e32 v19, 0x18800, v4
	ds_read_b128 v[110:113], v18
	ds_read_b128 v[114:117], v19
	v_add_u32_e32 v20, 0x19000, v4
	ds_read_b128 v[118:121], v20
	v_mfma_f32_16x16x32_f16 v[78:81], v[70:73], v[58:61], v[78:81]
	v_mfma_f32_16x16x32_f16 v[82:85], v[74:77], v[58:61], v[82:85]
	v_mfma_f32_16x16x32_f16 v[26:29], v[90:93], v[58:61], v[26:29]
	v_mfma_f32_16x16x32_f16 v[50:53], v[70:73], v[62:65], v[50:53]
	v_mfma_f32_16x16x32_f16 v[54:57], v[74:77], v[62:65], v[54:57]
	v_mfma_f32_16x16x32_f16 v[42:45], v[90:93], v[62:65], v[42:45]
	v_mfma_f32_16x16x32_f16 v[58:61], v[70:73], v[66:69], v[86:89]
	v_mfma_f32_16x16x32_f16 v[22:25], v[74:77], v[66:69], v[22:25]
	v_mfma_f32_16x16x32_f16 v[30:33], v[90:93], v[66:69], v[30:33]
	s_waitcnt lgkmcnt(0)
	v_mfma_f32_16x16x32_f16 v[34:37], v[110:113], v[94:97], v[34:37]
	v_mfma_f32_16x16x32_f16 v[38:41], v[114:117], v[94:97], v[38:41]
	v_mfma_f32_16x16x32_f16 v[46:49], v[118:121], v[94:97], v[46:49]
	v_add_u32_e32 v17, v124, v123
	ds_read_b128 v[62:65], v17 offset:2048
	ds_read_b128 v[66:69], v17 offset:4096
	ds_read_b128 v[70:73], v17 offset:6144
	ds_read_b128 v[74:77], v7 offset:16384
	ds_read_b128 v[86:89], v7 offset:18432
	ds_read_b128 v[90:93], v17
	ds_read_b128 v[94:97], v7 offset:20480
	v_mfma_f32_16x16x32_f16 v[78:81], v[110:113], v[98:101], v[78:81]
	v_mfma_f32_16x16x32_f16 v[82:85], v[114:117], v[98:101], v[82:85]
	v_mfma_f32_16x16x32_f16 v[26:29], v[118:121], v[98:101], v[26:29]
	v_mfma_f32_16x16x32_f16 v[50:53], v[110:113], v[102:105], v[50:53]
	v_mfma_f32_16x16x32_f16 v[54:57], v[114:117], v[102:105], v[54:57]
	v_mfma_f32_16x16x32_f16 v[42:45], v[118:121], v[102:105], v[42:45]
	v_mfma_f32_16x16x32_f16 v[58:61], v[110:113], v[106:109], v[58:61]
	v_mfma_f32_16x16x32_f16 v[22:25], v[114:117], v[106:109], v[22:25]
	v_mfma_f32_16x16x32_f16 v[30:33], v[118:121], v[106:109], v[30:33]
	v_add_u32_e32 v21, s19, v122
	s_add_u32 s20, s0, 0x280
	v_readfirstlane_b32 s23, v21
	v_add_u32_e32 v98, 0x2000, v21
	s_waitcnt vmcnt(5) lgkmcnt(0)
	s_barrier
	s_addc_u32 s21, s1, 0
	s_mov_b32 m0, s23
	v_readfirstlane_b32 s19, v98
	global_load_lds_dwordx4 v1, s[20:21]
	s_mov_b32 m0, s19
	v_add_u32_e32 v98, 0x4000, v21
	s_add_u32 s24, s2, 0x280
	global_load_lds_dwordx4 v2, s[20:21]
	v_readfirstlane_b32 s20, v98
	v_add_u32_e32 v98, 0x6000, v21
	s_addc_u32 s25, s3, 0
	s_mov_b32 m0, s20
	v_readfirstlane_b32 s21, v98
	v_add_u32_e32 v21, 0x8000, v21
	global_load_lds_dwordx4 v1, s[24:25]
	s_mov_b32 m0, s21
	v_readfirstlane_b32 s22, v21
	global_load_lds_dwordx4 v2, s[24:25]
	s_mov_b32 m0, s22
	s_nop 0
	global_load_lds_dwordx4 v3, s[24:25]
	s_waitcnt lgkmcnt(0)
	v_mfma_f32_16x16x32_f16 v[34:37], v[74:77], v[90:93], v[34:37]
	v_mfma_f32_16x16x32_f16 v[38:41], v[86:89], v[90:93], v[38:41]
	v_mfma_f32_16x16x32_f16 v[46:49], v[94:97], v[90:93], v[46:49]
	ds_read_b128 v[90:93], v6
	ds_read_b128 v[98:101], v6 offset:2048
	ds_read_b128 v[102:105], v6 offset:4096
	ds_read_b128 v[106:109], v6 offset:6144
	ds_read_b128 v[110:113], v4 offset:16384
	ds_read_b128 v[114:117], v4 offset:18432
	ds_read_b128 v[118:121], v4 offset:20480
	v_mfma_f32_16x16x32_f16 v[78:81], v[74:77], v[62:65], v[78:81]
	v_mfma_f32_16x16x32_f16 v[82:85], v[86:89], v[62:65], v[82:85]
	v_mfma_f32_16x16x32_f16 v[26:29], v[94:97], v[62:65], v[26:29]
	v_mfma_f32_16x16x32_f16 v[50:53], v[74:77], v[66:69], v[50:53]
	v_mfma_f32_16x16x32_f16 v[54:57], v[86:89], v[66:69], v[54:57]
	v_mfma_f32_16x16x32_f16 v[42:45], v[94:97], v[66:69], v[42:45]
	v_mfma_f32_16x16x32_f16 v[58:61], v[74:77], v[70:73], v[58:61]
	v_mfma_f32_16x16x32_f16 v[22:25], v[86:89], v[70:73], v[22:25]
	v_mfma_f32_16x16x32_f16 v[30:33], v[94:97], v[70:73], v[30:33]
	s_waitcnt lgkmcnt(0)
	v_mfma_f32_16x16x32_f16 v[34:37], v[110:113], v[90:93], v[34:37]
	v_mfma_f32_16x16x32_f16 v[38:41], v[114:117], v[90:93], v[38:41]
	v_mfma_f32_16x16x32_f16 v[46:49], v[118:121], v[90:93], v[46:49]
	ds_read_b128 v[62:65], v0
	ds_read_b128 v[66:69], v0 offset:2048
	ds_read_b128 v[70:73], v0 offset:4096
	ds_read_b128 v[74:77], v0 offset:6144
	ds_read_b128 v[86:89], v5 offset:16384
	ds_read_b128 v[90:93], v5 offset:18432
	ds_read_b128 v[94:97], v5 offset:20480
	v_mfma_f32_16x16x32_f16 v[78:81], v[110:113], v[98:101], v[78:81]
	v_mfma_f32_16x16x32_f16 v[82:85], v[114:117], v[98:101], v[82:85]
	v_mfma_f32_16x16x32_f16 v[26:29], v[118:121], v[98:101], v[26:29]
	v_mfma_f32_16x16x32_f16 v[50:53], v[110:113], v[102:105], v[50:53]
	v_mfma_f32_16x16x32_f16 v[54:57], v[114:117], v[102:105], v[54:57]
	v_mfma_f32_16x16x32_f16 v[42:45], v[118:121], v[102:105], v[42:45]
	v_mfma_f32_16x16x32_f16 v[58:61], v[110:113], v[106:109], v[58:61]
	v_mfma_f32_16x16x32_f16 v[22:25], v[114:117], v[106:109], v[22:25]
	v_mfma_f32_16x16x32_f16 v[30:33], v[118:121], v[106:109], v[30:33]
	s_add_u32 s24, s0, 0x300
	s_mov_b32 m0, s13
	s_waitcnt vmcnt(5) lgkmcnt(0)
	s_barrier
	s_addc_u32 s25, s1, 0
	s_add_u32 s26, s2, 0x300
	global_load_lds_dwordx4 v1, s[24:25]
	s_mov_b32 m0, s4
	s_addc_u32 s27, s3, 0
	global_load_lds_dwordx4 v2, s[24:25]
	s_mov_b32 m0, s5
	s_nop 0
	global_load_lds_dwordx4 v1, s[26:27]
	s_mov_b32 m0, s6
	s_nop 0
	global_load_lds_dwordx4 v2, s[26:27]
	s_mov_b32 m0, s7
	s_nop 0
	global_load_lds_dwordx4 v3, s[26:27]
	s_waitcnt lgkmcnt(0)
	v_mfma_f32_16x16x32_f16 v[34:37], v[86:89], v[62:65], v[34:37]
	v_mfma_f32_16x16x32_f16 v[38:41], v[90:93], v[62:65], v[38:41]
	v_mfma_f32_16x16x32_f16 v[46:49], v[94:97], v[62:65], v[46:49]
	ds_read_b128 v[62:65], v6 offset:40960
	ds_read_b128 v[98:101], v6 offset:43008
	ds_read_b128 v[102:105], v6 offset:45056
	ds_read_b128 v[106:109], v6 offset:47104
	ds_read_b128 v[110:113], v4 offset:57344
	ds_read_b128 v[114:117], v4 offset:59392
	ds_read_b128 v[118:121], v4 offset:61440
	v_mfma_f32_16x16x32_f16 v[78:81], v[86:89], v[66:69], v[78:81]
	v_mfma_f32_16x16x32_f16 v[82:85], v[90:93], v[66:69], v[82:85]
	v_mfma_f32_16x16x32_f16 v[26:29], v[94:97], v[66:69], v[26:29]
	v_mfma_f32_16x16x32_f16 v[50:53], v[86:89], v[70:73], v[50:53]
	v_mfma_f32_16x16x32_f16 v[54:57], v[90:93], v[70:73], v[54:57]
	v_mfma_f32_16x16x32_f16 v[42:45], v[94:97], v[70:73], v[42:45]
	v_mfma_f32_16x16x32_f16 v[58:61], v[86:89], v[74:77], v[58:61]
	v_mfma_f32_16x16x32_f16 v[22:25], v[90:93], v[74:77], v[22:25]
	v_mfma_f32_16x16x32_f16 v[30:33], v[94:97], v[74:77], v[30:33]
	s_waitcnt lgkmcnt(0)
	v_mfma_f32_16x16x32_f16 v[34:37], v[110:113], v[62:65], v[34:37]
	v_mfma_f32_16x16x32_f16 v[38:41], v[114:117], v[62:65], v[38:41]
	v_mfma_f32_16x16x32_f16 v[46:49], v[118:121], v[62:65], v[46:49]
	ds_read_b128 v[62:65], v0 offset:40960
	ds_read_b128 v[66:69], v0 offset:43008
	ds_read_b128 v[70:73], v0 offset:45056
	ds_read_b128 v[74:77], v0 offset:47104
	ds_read_b128 v[86:89], v5 offset:57344
	ds_read_b128 v[90:93], v5 offset:59392
	ds_read_b128 v[94:97], v5 offset:61440
	v_mfma_f32_16x16x32_f16 v[78:81], v[110:113], v[98:101], v[78:81]
	v_mfma_f32_16x16x32_f16 v[82:85], v[114:117], v[98:101], v[82:85]
	v_mfma_f32_16x16x32_f16 v[26:29], v[118:121], v[98:101], v[26:29]
	v_mfma_f32_16x16x32_f16 v[50:53], v[110:113], v[102:105], v[50:53]
	v_mfma_f32_16x16x32_f16 v[54:57], v[114:117], v[102:105], v[54:57]
	v_mfma_f32_16x16x32_f16 v[42:45], v[118:121], v[102:105], v[42:45]
	v_mfma_f32_16x16x32_f16 v[58:61], v[110:113], v[106:109], v[58:61]
	v_mfma_f32_16x16x32_f16 v[22:25], v[114:117], v[106:109], v[22:25]
	v_mfma_f32_16x16x32_f16 v[30:33], v[118:121], v[106:109], v[30:33]
	s_add_u32 s24, s0, 0x380
	s_mov_b32 m0, s18
	s_waitcnt vmcnt(5) lgkmcnt(0)
	s_barrier
	s_addc_u32 s25, s1, 0
	s_add_u32 s26, s2, 0x380
	global_load_lds_dwordx4 v1, s[24:25]
	s_mov_b32 m0, s14
	s_addc_u32 s27, s3, 0
	global_load_lds_dwordx4 v2, s[24:25]
	s_mov_b32 m0, s15
	s_nop 0
	global_load_lds_dwordx4 v1, s[26:27]
	s_mov_b32 m0, s16
	s_nop 0
	global_load_lds_dwordx4 v2, s[26:27]
	s_mov_b32 m0, s17
	s_nop 0
	global_load_lds_dwordx4 v3, s[26:27]
	s_waitcnt lgkmcnt(0)
	v_mfma_f32_16x16x32_f16 v[34:37], v[86:89], v[62:65], v[34:37]
	v_mfma_f32_16x16x32_f16 v[38:41], v[90:93], v[62:65], v[38:41]
	v_mfma_f32_16x16x32_f16 v[46:49], v[94:97], v[62:65], v[46:49]
	ds_read_b128 v[62:65], v13
	ds_read_b128 v[98:101], v14
	ds_read_b128 v[102:105], v15
	ds_read_b128 v[106:109], v16
	ds_read_b128 v[110:113], v18
	ds_read_b128 v[114:117], v19
	ds_read_b128 v[118:121], v20
	v_mfma_f32_16x16x32_f16 v[78:81], v[86:89], v[66:69], v[78:81]
	v_mfma_f32_16x16x32_f16 v[82:85], v[90:93], v[66:69], v[82:85]
	v_mfma_f32_16x16x32_f16 v[26:29], v[94:97], v[66:69], v[26:29]
	v_mfma_f32_16x16x32_f16 v[50:53], v[86:89], v[70:73], v[50:53]
	v_mfma_f32_16x16x32_f16 v[54:57], v[90:93], v[70:73], v[54:57]
	v_mfma_f32_16x16x32_f16 v[42:45], v[94:97], v[70:73], v[42:45]
	v_mfma_f32_16x16x32_f16 v[58:61], v[86:89], v[74:77], v[58:61]
	v_mfma_f32_16x16x32_f16 v[22:25], v[90:93], v[74:77], v[22:25]
	v_mfma_f32_16x16x32_f16 v[30:33], v[94:97], v[74:77], v[30:33]
	s_waitcnt lgkmcnt(0)
	v_mfma_f32_16x16x32_f16 v[34:37], v[110:113], v[62:65], v[34:37]
	v_mfma_f32_16x16x32_f16 v[38:41], v[114:117], v[62:65], v[38:41]
	v_mfma_f32_16x16x32_f16 v[46:49], v[118:121], v[62:65], v[46:49]
	ds_read_b128 v[62:65], v17 offset:2048
	ds_read_b128 v[66:69], v17 offset:4096
	ds_read_b128 v[70:73], v17 offset:6144
	ds_read_b128 v[74:77], v7 offset:16384
	ds_read_b128 v[86:89], v7 offset:18432
	ds_read_b128 v[90:93], v17
	ds_read_b128 v[94:97], v7 offset:20480
	v_mfma_f32_16x16x32_f16 v[78:81], v[110:113], v[98:101], v[78:81]
	v_mfma_f32_16x16x32_f16 v[82:85], v[114:117], v[98:101], v[82:85]
	v_mfma_f32_16x16x32_f16 v[26:29], v[118:121], v[98:101], v[26:29]
	v_mfma_f32_16x16x32_f16 v[50:53], v[110:113], v[102:105], v[50:53]
	v_mfma_f32_16x16x32_f16 v[54:57], v[114:117], v[102:105], v[54:57]
	v_mfma_f32_16x16x32_f16 v[42:45], v[118:121], v[102:105], v[42:45]
	v_mfma_f32_16x16x32_f16 v[58:61], v[110:113], v[106:109], v[58:61]
	v_mfma_f32_16x16x32_f16 v[22:25], v[114:117], v[106:109], v[22:25]
	v_mfma_f32_16x16x32_f16 v[30:33], v[118:121], v[106:109], v[30:33]
	s_add_u32 s24, s0, 0x400
	s_mov_b32 m0, s23
	s_waitcnt vmcnt(5) lgkmcnt(0)
	s_barrier
	s_addc_u32 s25, s1, 0
	s_add_u32 s26, s2, 0x400
	global_load_lds_dwordx4 v1, s[24:25]
	s_mov_b32 m0, s19
	s_addc_u32 s27, s3, 0
	global_load_lds_dwordx4 v2, s[24:25]
	s_mov_b32 m0, s20
	s_nop 0
	global_load_lds_dwordx4 v1, s[26:27]
	s_mov_b32 m0, s21
	s_nop 0
	global_load_lds_dwordx4 v2, s[26:27]
	s_mov_b32 m0, s22
	s_nop 0
	global_load_lds_dwordx4 v3, s[26:27]
	s_waitcnt lgkmcnt(0)
	v_mfma_f32_16x16x32_f16 v[34:37], v[74:77], v[90:93], v[34:37]
	v_mfma_f32_16x16x32_f16 v[38:41], v[86:89], v[90:93], v[38:41]
	v_mfma_f32_16x16x32_f16 v[46:49], v[94:97], v[90:93], v[46:49]
	ds_read_b128 v[90:93], v6
	ds_read_b128 v[98:101], v6 offset:2048
	ds_read_b128 v[102:105], v6 offset:4096
	ds_read_b128 v[106:109], v6 offset:6144
	ds_read_b128 v[110:113], v4 offset:16384
	ds_read_b128 v[114:117], v4 offset:18432
	ds_read_b128 v[118:121], v4 offset:20480
	v_mfma_f32_16x16x32_f16 v[78:81], v[74:77], v[62:65], v[78:81]
	v_mfma_f32_16x16x32_f16 v[82:85], v[86:89], v[62:65], v[82:85]
	v_mfma_f32_16x16x32_f16 v[26:29], v[94:97], v[62:65], v[26:29]
	v_mfma_f32_16x16x32_f16 v[50:53], v[74:77], v[66:69], v[50:53]
	v_mfma_f32_16x16x32_f16 v[54:57], v[86:89], v[66:69], v[54:57]
	v_mfma_f32_16x16x32_f16 v[42:45], v[94:97], v[66:69], v[42:45]
	v_mfma_f32_16x16x32_f16 v[58:61], v[74:77], v[70:73], v[58:61]
	v_mfma_f32_16x16x32_f16 v[22:25], v[86:89], v[70:73], v[22:25]
	v_mfma_f32_16x16x32_f16 v[30:33], v[94:97], v[70:73], v[30:33]
	s_waitcnt lgkmcnt(0)
	v_mfma_f32_16x16x32_f16 v[34:37], v[110:113], v[90:93], v[34:37]
	v_mfma_f32_16x16x32_f16 v[38:41], v[114:117], v[90:93], v[38:41]
	v_mfma_f32_16x16x32_f16 v[46:49], v[118:121], v[90:93], v[46:49]
	ds_read_b128 v[62:65], v0
	ds_read_b128 v[66:69], v0 offset:2048
	ds_read_b128 v[70:73], v0 offset:4096
	ds_read_b128 v[74:77], v0 offset:6144
	ds_read_b128 v[86:89], v5 offset:16384
	ds_read_b128 v[90:93], v5 offset:18432
	ds_read_b128 v[94:97], v5 offset:20480
	v_mfma_f32_16x16x32_f16 v[78:81], v[110:113], v[98:101], v[78:81]
	v_mfma_f32_16x16x32_f16 v[82:85], v[114:117], v[98:101], v[82:85]
	v_mfma_f32_16x16x32_f16 v[26:29], v[118:121], v[98:101], v[26:29]
	v_mfma_f32_16x16x32_f16 v[50:53], v[110:113], v[102:105], v[50:53]
	v_mfma_f32_16x16x32_f16 v[54:57], v[114:117], v[102:105], v[54:57]
	v_mfma_f32_16x16x32_f16 v[42:45], v[118:121], v[102:105], v[42:45]
	v_mfma_f32_16x16x32_f16 v[58:61], v[110:113], v[106:109], v[58:61]
	v_mfma_f32_16x16x32_f16 v[22:25], v[114:117], v[106:109], v[22:25]
	v_mfma_f32_16x16x32_f16 v[30:33], v[118:121], v[106:109], v[30:33]
	s_add_u32 s24, s0, 0x480
	s_mov_b32 m0, s13
	s_waitcnt vmcnt(5) lgkmcnt(0)
	s_barrier
	s_addc_u32 s25, s1, 0
	s_add_u32 s26, s2, 0x480
	global_load_lds_dwordx4 v1, s[24:25]
	s_mov_b32 m0, s4
	s_addc_u32 s27, s3, 0
	global_load_lds_dwordx4 v2, s[24:25]
	s_mov_b32 m0, s5
	s_nop 0
	global_load_lds_dwordx4 v1, s[26:27]
	s_mov_b32 m0, s6
	s_nop 0
	global_load_lds_dwordx4 v2, s[26:27]
	s_mov_b32 m0, s7
	s_nop 0
	global_load_lds_dwordx4 v3, s[26:27]
	s_waitcnt lgkmcnt(0)
	v_mfma_f32_16x16x32_f16 v[34:37], v[86:89], v[62:65], v[34:37]
	v_mfma_f32_16x16x32_f16 v[38:41], v[90:93], v[62:65], v[38:41]
	v_mfma_f32_16x16x32_f16 v[46:49], v[94:97], v[62:65], v[46:49]
	ds_read_b128 v[62:65], v6 offset:40960
	ds_read_b128 v[98:101], v6 offset:43008
	ds_read_b128 v[102:105], v6 offset:45056
	ds_read_b128 v[106:109], v6 offset:47104
	ds_read_b128 v[110:113], v4 offset:57344
	ds_read_b128 v[114:117], v4 offset:59392
	ds_read_b128 v[118:121], v4 offset:61440
	v_mfma_f32_16x16x32_f16 v[78:81], v[86:89], v[66:69], v[78:81]
	v_mfma_f32_16x16x32_f16 v[82:85], v[90:93], v[66:69], v[82:85]
	v_mfma_f32_16x16x32_f16 v[26:29], v[94:97], v[66:69], v[26:29]
	v_mfma_f32_16x16x32_f16 v[50:53], v[86:89], v[70:73], v[50:53]
	v_mfma_f32_16x16x32_f16 v[54:57], v[90:93], v[70:73], v[54:57]
	v_mfma_f32_16x16x32_f16 v[42:45], v[94:97], v[70:73], v[42:45]
	v_mfma_f32_16x16x32_f16 v[58:61], v[86:89], v[74:77], v[58:61]
	v_mfma_f32_16x16x32_f16 v[22:25], v[90:93], v[74:77], v[22:25]
	v_mfma_f32_16x16x32_f16 v[30:33], v[94:97], v[74:77], v[30:33]
	s_waitcnt lgkmcnt(0)
	v_mfma_f32_16x16x32_f16 v[34:37], v[110:113], v[62:65], v[34:37]
	v_mfma_f32_16x16x32_f16 v[38:41], v[114:117], v[62:65], v[38:41]
	v_mfma_f32_16x16x32_f16 v[46:49], v[118:121], v[62:65], v[46:49]
	ds_read_b128 v[62:65], v0 offset:40960
	ds_read_b128 v[66:69], v0 offset:43008
	ds_read_b128 v[70:73], v0 offset:45056
	ds_read_b128 v[74:77], v0 offset:47104
	ds_read_b128 v[86:89], v5 offset:57344
	ds_read_b128 v[90:93], v5 offset:59392
	ds_read_b128 v[94:97], v5 offset:61440
	v_mfma_f32_16x16x32_f16 v[78:81], v[110:113], v[98:101], v[78:81]
	v_mfma_f32_16x16x32_f16 v[82:85], v[114:117], v[98:101], v[82:85]
	v_mfma_f32_16x16x32_f16 v[26:29], v[118:121], v[98:101], v[26:29]
	v_mfma_f32_16x16x32_f16 v[50:53], v[110:113], v[102:105], v[50:53]
	v_mfma_f32_16x16x32_f16 v[54:57], v[114:117], v[102:105], v[54:57]
	v_mfma_f32_16x16x32_f16 v[42:45], v[118:121], v[102:105], v[42:45]
	v_mfma_f32_16x16x32_f16 v[58:61], v[110:113], v[106:109], v[58:61]
	v_mfma_f32_16x16x32_f16 v[22:25], v[114:117], v[106:109], v[22:25]
	v_mfma_f32_16x16x32_f16 v[30:33], v[118:121], v[106:109], v[30:33]
	s_add_u32 s24, s0, 0x500
	s_mov_b32 m0, s18
	s_waitcnt vmcnt(5) lgkmcnt(0)
	s_barrier
	s_addc_u32 s25, s1, 0
	s_add_u32 s26, s2, 0x500
	global_load_lds_dwordx4 v1, s[24:25]
	s_mov_b32 m0, s14
	s_addc_u32 s27, s3, 0
	global_load_lds_dwordx4 v2, s[24:25]
	s_mov_b32 m0, s15
	s_nop 0
	global_load_lds_dwordx4 v1, s[26:27]
	s_mov_b32 m0, s16
	s_nop 0
	global_load_lds_dwordx4 v2, s[26:27]
	s_mov_b32 m0, s17
	s_nop 0
	global_load_lds_dwordx4 v3, s[26:27]
	s_waitcnt lgkmcnt(0)
	v_mfma_f32_16x16x32_f16 v[34:37], v[86:89], v[62:65], v[34:37]
	v_mfma_f32_16x16x32_f16 v[38:41], v[90:93], v[62:65], v[38:41]
	v_mfma_f32_16x16x32_f16 v[46:49], v[94:97], v[62:65], v[46:49]
	ds_read_b128 v[62:65], v13
	ds_read_b128 v[98:101], v14
	ds_read_b128 v[102:105], v15
	ds_read_b128 v[106:109], v16
	ds_read_b128 v[110:113], v18
	ds_read_b128 v[114:117], v19
	ds_read_b128 v[118:121], v20
	v_mfma_f32_16x16x32_f16 v[78:81], v[86:89], v[66:69], v[78:81]
	v_mfma_f32_16x16x32_f16 v[82:85], v[90:93], v[66:69], v[82:85]
	v_mfma_f32_16x16x32_f16 v[26:29], v[94:97], v[66:69], v[26:29]
	v_mfma_f32_16x16x32_f16 v[50:53], v[86:89], v[70:73], v[50:53]
	v_mfma_f32_16x16x32_f16 v[54:57], v[90:93], v[70:73], v[54:57]
	v_mfma_f32_16x16x32_f16 v[42:45], v[94:97], v[70:73], v[42:45]
	v_mfma_f32_16x16x32_f16 v[58:61], v[86:89], v[74:77], v[58:61]
	v_mfma_f32_16x16x32_f16 v[22:25], v[90:93], v[74:77], v[22:25]
	v_mfma_f32_16x16x32_f16 v[30:33], v[94:97], v[74:77], v[30:33]
	s_waitcnt lgkmcnt(0)
	v_mfma_f32_16x16x32_f16 v[34:37], v[110:113], v[62:65], v[34:37]
	v_mfma_f32_16x16x32_f16 v[38:41], v[114:117], v[62:65], v[38:41]
	v_mfma_f32_16x16x32_f16 v[46:49], v[118:121], v[62:65], v[46:49]
	ds_read_b128 v[62:65], v17 offset:2048
	ds_read_b128 v[66:69], v17 offset:4096
	ds_read_b128 v[70:73], v17 offset:6144
	ds_read_b128 v[74:77], v7 offset:16384
	ds_read_b128 v[86:89], v7 offset:18432
	ds_read_b128 v[90:93], v17
	ds_read_b128 v[94:97], v7 offset:20480
	v_mfma_f32_16x16x32_f16 v[78:81], v[110:113], v[98:101], v[78:81]
	v_mfma_f32_16x16x32_f16 v[82:85], v[114:117], v[98:101], v[82:85]
	v_mfma_f32_16x16x32_f16 v[26:29], v[118:121], v[98:101], v[26:29]
	v_mfma_f32_16x16x32_f16 v[50:53], v[110:113], v[102:105], v[50:53]
	v_mfma_f32_16x16x32_f16 v[54:57], v[114:117], v[102:105], v[54:57]
	v_mfma_f32_16x16x32_f16 v[42:45], v[118:121], v[102:105], v[42:45]
	v_mfma_f32_16x16x32_f16 v[58:61], v[110:113], v[106:109], v[58:61]
	v_mfma_f32_16x16x32_f16 v[22:25], v[114:117], v[106:109], v[22:25]
	v_mfma_f32_16x16x32_f16 v[30:33], v[118:121], v[106:109], v[30:33]
	s_add_u32 s24, s0, 0x580
	s_mov_b32 m0, s23
	s_waitcnt vmcnt(5) lgkmcnt(0)
	s_barrier
	s_addc_u32 s25, s1, 0
	s_add_u32 s26, s2, 0x580
	global_load_lds_dwordx4 v1, s[24:25]
	s_mov_b32 m0, s19
	s_addc_u32 s27, s3, 0
	global_load_lds_dwordx4 v2, s[24:25]
	s_mov_b32 m0, s20
	s_nop 0
	global_load_lds_dwordx4 v1, s[26:27]
	s_mov_b32 m0, s21
	s_nop 0
	global_load_lds_dwordx4 v2, s[26:27]
	s_mov_b32 m0, s22
	s_nop 0
	global_load_lds_dwordx4 v3, s[26:27]
	s_waitcnt lgkmcnt(0)
	v_mfma_f32_16x16x32_f16 v[34:37], v[74:77], v[90:93], v[34:37]
	v_mfma_f32_16x16x32_f16 v[38:41], v[86:89], v[90:93], v[38:41]
	v_mfma_f32_16x16x32_f16 v[46:49], v[94:97], v[90:93], v[46:49]
	ds_read_b128 v[90:93], v6
	ds_read_b128 v[98:101], v6 offset:2048
	ds_read_b128 v[102:105], v6 offset:4096
	ds_read_b128 v[106:109], v6 offset:6144
	ds_read_b128 v[110:113], v4 offset:16384
	ds_read_b128 v[114:117], v4 offset:18432
	ds_read_b128 v[118:121], v4 offset:20480
	v_mfma_f32_16x16x32_f16 v[78:81], v[74:77], v[62:65], v[78:81]
	v_mfma_f32_16x16x32_f16 v[82:85], v[86:89], v[62:65], v[82:85]
	v_mfma_f32_16x16x32_f16 v[26:29], v[94:97], v[62:65], v[26:29]
	v_mfma_f32_16x16x32_f16 v[50:53], v[74:77], v[66:69], v[50:53]
	v_mfma_f32_16x16x32_f16 v[54:57], v[86:89], v[66:69], v[54:57]
	v_mfma_f32_16x16x32_f16 v[42:45], v[94:97], v[66:69], v[42:45]
	v_mfma_f32_16x16x32_f16 v[58:61], v[74:77], v[70:73], v[58:61]
	v_mfma_f32_16x16x32_f16 v[22:25], v[86:89], v[70:73], v[22:25]
	v_mfma_f32_16x16x32_f16 v[30:33], v[94:97], v[70:73], v[30:33]
	s_waitcnt lgkmcnt(0)
	v_mfma_f32_16x16x32_f16 v[34:37], v[110:113], v[90:93], v[34:37]
	v_mfma_f32_16x16x32_f16 v[38:41], v[114:117], v[90:93], v[38:41]
	v_mfma_f32_16x16x32_f16 v[46:49], v[118:121], v[90:93], v[46:49]
	ds_read_b128 v[62:65], v0
	ds_read_b128 v[66:69], v0 offset:2048
	ds_read_b128 v[70:73], v0 offset:4096
	ds_read_b128 v[74:77], v0 offset:6144
	ds_read_b128 v[86:89], v5 offset:16384
	ds_read_b128 v[90:93], v5 offset:18432
	ds_read_b128 v[94:97], v5 offset:20480
	v_mfma_f32_16x16x32_f16 v[78:81], v[110:113], v[98:101], v[78:81]
	v_mfma_f32_16x16x32_f16 v[82:85], v[114:117], v[98:101], v[82:85]
	v_mfma_f32_16x16x32_f16 v[26:29], v[118:121], v[98:101], v[26:29]
	v_mfma_f32_16x16x32_f16 v[50:53], v[110:113], v[102:105], v[50:53]
	v_mfma_f32_16x16x32_f16 v[54:57], v[114:117], v[102:105], v[54:57]
	v_mfma_f32_16x16x32_f16 v[42:45], v[118:121], v[102:105], v[42:45]
	v_mfma_f32_16x16x32_f16 v[58:61], v[110:113], v[106:109], v[58:61]
	v_mfma_f32_16x16x32_f16 v[22:25], v[114:117], v[106:109], v[22:25]
	v_mfma_f32_16x16x32_f16 v[30:33], v[118:121], v[106:109], v[30:33]
	s_add_u32 s24, s0, 0x600
	s_mov_b32 m0, s13
	s_waitcnt vmcnt(5) lgkmcnt(0)
	s_barrier
	s_addc_u32 s25, s1, 0
	s_add_u32 s26, s2, 0x600
	global_load_lds_dwordx4 v1, s[24:25]
	s_mov_b32 m0, s4
	s_addc_u32 s27, s3, 0
	global_load_lds_dwordx4 v2, s[24:25]
	s_mov_b32 m0, s5
	s_nop 0
	global_load_lds_dwordx4 v1, s[26:27]
	s_mov_b32 m0, s6
	s_nop 0
	global_load_lds_dwordx4 v2, s[26:27]
	s_mov_b32 m0, s7
	s_nop 0
	global_load_lds_dwordx4 v3, s[26:27]
	s_waitcnt lgkmcnt(0)
	v_mfma_f32_16x16x32_f16 v[34:37], v[86:89], v[62:65], v[34:37]
	v_mfma_f32_16x16x32_f16 v[38:41], v[90:93], v[62:65], v[38:41]
	v_mfma_f32_16x16x32_f16 v[46:49], v[94:97], v[62:65], v[46:49]
	ds_read_b128 v[62:65], v6 offset:40960
	ds_read_b128 v[98:101], v6 offset:43008
	ds_read_b128 v[102:105], v6 offset:45056
	ds_read_b128 v[106:109], v6 offset:47104
	ds_read_b128 v[110:113], v4 offset:57344
	ds_read_b128 v[114:117], v4 offset:59392
	ds_read_b128 v[118:121], v4 offset:61440
	v_mfma_f32_16x16x32_f16 v[78:81], v[86:89], v[66:69], v[78:81]
	v_mfma_f32_16x16x32_f16 v[82:85], v[90:93], v[66:69], v[82:85]
	v_mfma_f32_16x16x32_f16 v[26:29], v[94:97], v[66:69], v[26:29]
	v_mfma_f32_16x16x32_f16 v[50:53], v[86:89], v[70:73], v[50:53]
	v_mfma_f32_16x16x32_f16 v[54:57], v[90:93], v[70:73], v[54:57]
	v_mfma_f32_16x16x32_f16 v[42:45], v[94:97], v[70:73], v[42:45]
	v_mfma_f32_16x16x32_f16 v[58:61], v[86:89], v[74:77], v[58:61]
	v_mfma_f32_16x16x32_f16 v[22:25], v[90:93], v[74:77], v[22:25]
	v_mfma_f32_16x16x32_f16 v[30:33], v[94:97], v[74:77], v[30:33]
	s_waitcnt lgkmcnt(0)
	v_mfma_f32_16x16x32_f16 v[34:37], v[110:113], v[62:65], v[34:37]
	v_mfma_f32_16x16x32_f16 v[38:41], v[114:117], v[62:65], v[38:41]
	v_mfma_f32_16x16x32_f16 v[46:49], v[118:121], v[62:65], v[46:49]
	ds_read_b128 v[62:65], v0 offset:40960
	ds_read_b128 v[66:69], v0 offset:43008
	ds_read_b128 v[70:73], v0 offset:45056
	ds_read_b128 v[74:77], v0 offset:47104
	ds_read_b128 v[86:89], v5 offset:57344
	ds_read_b128 v[90:93], v5 offset:59392
	ds_read_b128 v[94:97], v5 offset:61440
	v_mfma_f32_16x16x32_f16 v[78:81], v[110:113], v[98:101], v[78:81]
	v_mfma_f32_16x16x32_f16 v[82:85], v[114:117], v[98:101], v[82:85]
	v_mfma_f32_16x16x32_f16 v[26:29], v[118:121], v[98:101], v[26:29]
	v_mfma_f32_16x16x32_f16 v[50:53], v[110:113], v[102:105], v[50:53]
	v_mfma_f32_16x16x32_f16 v[54:57], v[114:117], v[102:105], v[54:57]
	v_mfma_f32_16x16x32_f16 v[42:45], v[118:121], v[102:105], v[42:45]
	v_mfma_f32_16x16x32_f16 v[58:61], v[110:113], v[106:109], v[58:61]
	v_mfma_f32_16x16x32_f16 v[22:25], v[114:117], v[106:109], v[22:25]
	v_mfma_f32_16x16x32_f16 v[30:33], v[118:121], v[106:109], v[30:33]
	s_add_u32 s24, s0, 0x680
	s_mov_b32 m0, s18
	s_waitcnt vmcnt(5) lgkmcnt(0)
	s_barrier
	s_addc_u32 s25, s1, 0
	s_add_u32 s26, s2, 0x680
	global_load_lds_dwordx4 v1, s[24:25]
	s_mov_b32 m0, s14
	s_addc_u32 s27, s3, 0
	global_load_lds_dwordx4 v2, s[24:25]
	s_mov_b32 m0, s15
	s_nop 0
	global_load_lds_dwordx4 v1, s[26:27]
	s_mov_b32 m0, s16
	s_nop 0
	global_load_lds_dwordx4 v2, s[26:27]
	s_mov_b32 m0, s17
	s_nop 0
	global_load_lds_dwordx4 v3, s[26:27]
	s_waitcnt lgkmcnt(0)
	v_mfma_f32_16x16x32_f16 v[34:37], v[86:89], v[62:65], v[34:37]
	v_mfma_f32_16x16x32_f16 v[38:41], v[90:93], v[62:65], v[38:41]
	v_mfma_f32_16x16x32_f16 v[46:49], v[94:97], v[62:65], v[46:49]
	ds_read_b128 v[62:65], v13
	ds_read_b128 v[98:101], v14
	ds_read_b128 v[102:105], v15
	ds_read_b128 v[106:109], v16
	ds_read_b128 v[110:113], v18
	ds_read_b128 v[114:117], v19
	ds_read_b128 v[118:121], v20
	v_mfma_f32_16x16x32_f16 v[78:81], v[86:89], v[66:69], v[78:81]
	v_mfma_f32_16x16x32_f16 v[82:85], v[90:93], v[66:69], v[82:85]
	v_mfma_f32_16x16x32_f16 v[26:29], v[94:97], v[66:69], v[26:29]
	v_mfma_f32_16x16x32_f16 v[50:53], v[86:89], v[70:73], v[50:53]
	v_mfma_f32_16x16x32_f16 v[54:57], v[90:93], v[70:73], v[54:57]
	v_mfma_f32_16x16x32_f16 v[42:45], v[94:97], v[70:73], v[42:45]
	v_mfma_f32_16x16x32_f16 v[58:61], v[86:89], v[74:77], v[58:61]
	v_mfma_f32_16x16x32_f16 v[22:25], v[90:93], v[74:77], v[22:25]
	v_mfma_f32_16x16x32_f16 v[30:33], v[94:97], v[74:77], v[30:33]
	s_waitcnt lgkmcnt(0)
	v_mfma_f32_16x16x32_f16 v[34:37], v[110:113], v[62:65], v[34:37]
	v_mfma_f32_16x16x32_f16 v[38:41], v[114:117], v[62:65], v[38:41]
	v_mfma_f32_16x16x32_f16 v[46:49], v[118:121], v[62:65], v[46:49]
	ds_read_b128 v[62:65], v17 offset:2048
	ds_read_b128 v[66:69], v17 offset:4096
	ds_read_b128 v[70:73], v17 offset:6144
	ds_read_b128 v[74:77], v7 offset:16384
	ds_read_b128 v[86:89], v7 offset:18432
	ds_read_b128 v[90:93], v17
	ds_read_b128 v[94:97], v7 offset:20480
	v_mfma_f32_16x16x32_f16 v[78:81], v[110:113], v[98:101], v[78:81]
	v_mfma_f32_16x16x32_f16 v[82:85], v[114:117], v[98:101], v[82:85]
	v_mfma_f32_16x16x32_f16 v[26:29], v[118:121], v[98:101], v[26:29]
	v_mfma_f32_16x16x32_f16 v[50:53], v[110:113], v[102:105], v[50:53]
	v_mfma_f32_16x16x32_f16 v[54:57], v[114:117], v[102:105], v[54:57]
	v_mfma_f32_16x16x32_f16 v[42:45], v[118:121], v[102:105], v[42:45]
	v_mfma_f32_16x16x32_f16 v[58:61], v[110:113], v[106:109], v[58:61]
	v_mfma_f32_16x16x32_f16 v[22:25], v[114:117], v[106:109], v[22:25]
	v_mfma_f32_16x16x32_f16 v[30:33], v[118:121], v[106:109], v[30:33]
	s_add_u32 s14, s0, 0x700
	s_mov_b32 m0, s23
	s_waitcnt vmcnt(5) lgkmcnt(0)
	s_barrier
	s_addc_u32 s15, s1, 0
	s_add_u32 s16, s2, 0x700
	global_load_lds_dwordx4 v1, s[14:15]
	s_mov_b32 m0, s19
	s_addc_u32 s17, s3, 0
	global_load_lds_dwordx4 v2, s[14:15]
	s_mov_b32 m0, s20
	s_nop 0
	global_load_lds_dwordx4 v1, s[16:17]
	s_mov_b32 m0, s21
	s_nop 0
	global_load_lds_dwordx4 v2, s[16:17]
	s_mov_b32 m0, s22
	s_nop 0
	global_load_lds_dwordx4 v3, s[16:17]
	s_waitcnt lgkmcnt(0)
	v_mfma_f32_16x16x32_f16 v[34:37], v[74:77], v[90:93], v[34:37]
	v_mfma_f32_16x16x32_f16 v[38:41], v[86:89], v[90:93], v[38:41]
	v_mfma_f32_16x16x32_f16 v[46:49], v[94:97], v[90:93], v[46:49]
	ds_read_b128 v[90:93], v6
	ds_read_b128 v[98:101], v6 offset:2048
	ds_read_b128 v[102:105], v6 offset:4096
	ds_read_b128 v[106:109], v6 offset:6144
	ds_read_b128 v[110:113], v4 offset:16384
	ds_read_b128 v[114:117], v4 offset:18432
	ds_read_b128 v[118:121], v4 offset:20480
	v_mfma_f32_16x16x32_f16 v[78:81], v[74:77], v[62:65], v[78:81]
	v_mfma_f32_16x16x32_f16 v[82:85], v[86:89], v[62:65], v[82:85]
	v_mfma_f32_16x16x32_f16 v[26:29], v[94:97], v[62:65], v[26:29]
	v_mfma_f32_16x16x32_f16 v[50:53], v[74:77], v[66:69], v[50:53]
	v_mfma_f32_16x16x32_f16 v[54:57], v[86:89], v[66:69], v[54:57]
	v_mfma_f32_16x16x32_f16 v[42:45], v[94:97], v[66:69], v[42:45]
	v_mfma_f32_16x16x32_f16 v[58:61], v[74:77], v[70:73], v[58:61]
	v_mfma_f32_16x16x32_f16 v[22:25], v[86:89], v[70:73], v[22:25]
	v_mfma_f32_16x16x32_f16 v[30:33], v[94:97], v[70:73], v[30:33]
	s_waitcnt lgkmcnt(0)
	v_mfma_f32_16x16x32_f16 v[34:37], v[110:113], v[90:93], v[34:37]
	v_mfma_f32_16x16x32_f16 v[38:41], v[114:117], v[90:93], v[38:41]
	v_mfma_f32_16x16x32_f16 v[46:49], v[118:121], v[90:93], v[46:49]
	ds_read_b128 v[62:65], v0
	ds_read_b128 v[66:69], v0 offset:2048
	ds_read_b128 v[70:73], v0 offset:4096
	ds_read_b128 v[74:77], v0 offset:6144
	ds_read_b128 v[86:89], v5 offset:16384
	ds_read_b128 v[90:93], v5 offset:18432
	ds_read_b128 v[94:97], v5 offset:20480
	v_mfma_f32_16x16x32_f16 v[78:81], v[110:113], v[98:101], v[78:81]
	v_mfma_f32_16x16x32_f16 v[82:85], v[114:117], v[98:101], v[82:85]
	v_mfma_f32_16x16x32_f16 v[26:29], v[118:121], v[98:101], v[26:29]
	v_mfma_f32_16x16x32_f16 v[50:53], v[110:113], v[102:105], v[50:53]
	v_mfma_f32_16x16x32_f16 v[54:57], v[114:117], v[102:105], v[54:57]
	v_mfma_f32_16x16x32_f16 v[42:45], v[118:121], v[102:105], v[42:45]
	v_mfma_f32_16x16x32_f16 v[58:61], v[110:113], v[106:109], v[58:61]
	v_mfma_f32_16x16x32_f16 v[22:25], v[114:117], v[106:109], v[22:25]
	v_mfma_f32_16x16x32_f16 v[30:33], v[118:121], v[106:109], v[30:33]
	s_add_u32 s0, s0, 0x780
	s_mov_b32 m0, s13
	s_waitcnt vmcnt(5) lgkmcnt(0)
	s_barrier
	s_addc_u32 s1, s1, 0
	s_add_u32 s2, s2, 0x780
	global_load_lds_dwordx4 v1, s[0:1]
	s_mov_b32 m0, s4
	s_addc_u32 s3, s3, 0
	global_load_lds_dwordx4 v2, s[0:1]
	s_mov_b32 m0, s5
	s_nop 0
	global_load_lds_dwordx4 v1, s[2:3]
	s_mov_b32 m0, s6
	s_nop 0
	global_load_lds_dwordx4 v2, s[2:3]
	s_mov_b32 m0, s7
	s_nop 0
	global_load_lds_dwordx4 v3, s[2:3]
	s_waitcnt lgkmcnt(0)
	v_mfma_f32_16x16x32_f16 v[34:37], v[86:89], v[62:65], v[34:37]
	v_mfma_f32_16x16x32_f16 v[38:41], v[90:93], v[62:65], v[38:41]
	v_mfma_f32_16x16x32_f16 v[46:49], v[94:97], v[62:65], v[46:49]
	ds_read_b128 v[62:65], v6 offset:40960
	ds_read_b128 v[98:101], v6 offset:43008
	ds_read_b128 v[102:105], v6 offset:45056
	ds_read_b128 v[106:109], v6 offset:47104
	ds_read_b128 v[110:113], v4 offset:57344
	ds_read_b128 v[114:117], v4 offset:59392
	ds_read_b128 v[118:121], v4 offset:61440
	v_mfma_f32_16x16x32_f16 v[78:81], v[86:89], v[66:69], v[78:81]
	v_mfma_f32_16x16x32_f16 v[82:85], v[90:93], v[66:69], v[82:85]
	v_mfma_f32_16x16x32_f16 v[26:29], v[94:97], v[66:69], v[26:29]
	v_mfma_f32_16x16x32_f16 v[50:53], v[86:89], v[70:73], v[50:53]
	v_mfma_f32_16x16x32_f16 v[54:57], v[90:93], v[70:73], v[54:57]
	v_mfma_f32_16x16x32_f16 v[42:45], v[94:97], v[70:73], v[42:45]
	v_mfma_f32_16x16x32_f16 v[58:61], v[86:89], v[74:77], v[58:61]
	v_mfma_f32_16x16x32_f16 v[22:25], v[90:93], v[74:77], v[22:25]
	v_mfma_f32_16x16x32_f16 v[30:33], v[94:97], v[74:77], v[30:33]
	s_waitcnt lgkmcnt(0)
	v_mfma_f32_16x16x32_f16 v[34:37], v[110:113], v[62:65], v[34:37]
	v_mfma_f32_16x16x32_f16 v[38:41], v[114:117], v[62:65], v[38:41]
	v_mfma_f32_16x16x32_f16 v[46:49], v[118:121], v[62:65], v[46:49]
	ds_read_b128 v[62:65], v0 offset:40960
	ds_read_b128 v[66:69], v0 offset:43008
	ds_read_b128 v[70:73], v0 offset:45056
	ds_read_b128 v[74:77], v0 offset:47104
	ds_read_b128 v[86:89], v5 offset:57344
	ds_read_b128 v[90:93], v5 offset:59392
	ds_read_b128 v[94:97], v5 offset:61440
	v_mfma_f32_16x16x32_f16 v[78:81], v[110:113], v[98:101], v[78:81]
	v_mfma_f32_16x16x32_f16 v[82:85], v[114:117], v[98:101], v[82:85]
	v_mfma_f32_16x16x32_f16 v[26:29], v[118:121], v[98:101], v[26:29]
	v_mfma_f32_16x16x32_f16 v[50:53], v[110:113], v[102:105], v[50:53]
	v_mfma_f32_16x16x32_f16 v[54:57], v[114:117], v[102:105], v[54:57]
	v_mfma_f32_16x16x32_f16 v[42:45], v[118:121], v[102:105], v[42:45]
	v_mfma_f32_16x16x32_f16 v[58:61], v[110:113], v[106:109], v[58:61]
	v_mfma_f32_16x16x32_f16 v[22:25], v[114:117], v[106:109], v[22:25]
	v_mfma_f32_16x16x32_f16 v[30:33], v[118:121], v[106:109], v[30:33]
	s_waitcnt vmcnt(5) lgkmcnt(0)
	s_barrier
	s_waitcnt lgkmcnt(0)
	v_mfma_f32_16x16x32_f16 v[34:37], v[86:89], v[62:65], v[34:37]
	v_mfma_f32_16x16x32_f16 v[38:41], v[90:93], v[62:65], v[38:41]
	v_mfma_f32_16x16x32_f16 v[46:49], v[94:97], v[62:65], v[46:49]
	ds_read_b128 v[62:65], v13
	ds_read_b128 v[98:101], v14
	ds_read_b128 v[102:105], v15
	ds_read_b128 v[106:109], v16
	ds_read_b128 v[110:113], v18
	ds_read_b128 v[114:117], v19
	ds_read_b128 v[18:21], v20
	v_mfma_f32_16x16x32_f16 v[78:81], v[86:89], v[66:69], v[78:81]
	v_mfma_f32_16x16x32_f16 v[82:85], v[90:93], v[66:69], v[82:85]
	v_mfma_f32_16x16x32_f16 v[26:29], v[94:97], v[66:69], v[26:29]
	v_mfma_f32_16x16x32_f16 v[50:53], v[86:89], v[70:73], v[50:53]
	v_mfma_f32_16x16x32_f16 v[54:57], v[90:93], v[70:73], v[54:57]
	v_mfma_f32_16x16x32_f16 v[42:45], v[94:97], v[70:73], v[42:45]
	v_mfma_f32_16x16x32_f16 v[58:61], v[86:89], v[74:77], v[58:61]
	v_mfma_f32_16x16x32_f16 v[22:25], v[90:93], v[74:77], v[22:25]
	v_mfma_f32_16x16x32_f16 v[30:33], v[94:97], v[74:77], v[30:33]
	s_waitcnt lgkmcnt(0)
	v_mfma_f32_16x16x32_f16 v[34:37], v[110:113], v[62:65], v[34:37]
	v_mfma_f32_16x16x32_f16 v[38:41], v[114:117], v[62:65], v[38:41]
	v_mfma_f32_16x16x32_f16 v[46:49], v[18:21], v[62:65], v[46:49]
	ds_read_b128 v[62:65], v17 offset:2048
	ds_read_b128 v[66:69], v17 offset:4096
	ds_read_b128 v[70:73], v17 offset:6144
	ds_read_b128 v[74:77], v7 offset:16384
	ds_read_b128 v[86:89], v7 offset:18432
	ds_read_b128 v[14:17], v17
	ds_read_b128 v[90:93], v7 offset:20480
	v_mfma_f32_16x16x32_f16 v[78:81], v[110:113], v[98:101], v[78:81]
	v_mfma_f32_16x16x32_f16 v[82:85], v[114:117], v[98:101], v[82:85]
	v_mfma_f32_16x16x32_f16 v[26:29], v[18:21], v[98:101], v[26:29]
	v_mfma_f32_16x16x32_f16 v[50:53], v[110:113], v[102:105], v[50:53]
	v_mfma_f32_16x16x32_f16 v[54:57], v[114:117], v[102:105], v[54:57]
	v_mfma_f32_16x16x32_f16 v[42:45], v[18:21], v[102:105], v[42:45]
	v_mfma_f32_16x16x32_f16 v[58:61], v[110:113], v[106:109], v[58:61]
	v_mfma_f32_16x16x32_f16 v[22:25], v[114:117], v[106:109], v[22:25]
	v_mfma_f32_16x16x32_f16 v[18:21], v[18:21], v[106:109], v[30:33]
	s_waitcnt vmcnt(0) lgkmcnt(0)
	s_barrier
	s_waitcnt lgkmcnt(0)
	v_mfma_f32_16x16x32_f16 v[30:33], v[74:77], v[14:17], v[34:37]
	v_mfma_f32_16x16x32_f16 v[34:37], v[86:89], v[14:17], v[38:41]
	v_mfma_f32_16x16x32_f16 v[14:17], v[90:93], v[14:17], v[46:49]
	s_nop 1
	ds_read_b128 v[38:41], v6
	ds_read_b128 v[46:49], v6 offset:2048
	ds_read_b128 v[94:97], v6 offset:4096
	ds_read_b128 v[98:101], v6 offset:6144
	ds_read_b128 v[102:105], v4 offset:16384
	ds_read_b128 v[106:109], v4 offset:18432
	ds_read_b128 v[110:113], v4 offset:20480
	v_mfma_f32_16x16x32_f16 v[78:81], v[74:77], v[62:65], v[78:81]
	v_mfma_f32_16x16x32_f16 v[82:85], v[86:89], v[62:65], v[82:85]
	v_mfma_f32_16x16x32_f16 v[26:29], v[90:93], v[62:65], v[26:29]
	v_mfma_f32_16x16x32_f16 v[50:53], v[74:77], v[66:69], v[50:53]
	v_mfma_f32_16x16x32_f16 v[54:57], v[86:89], v[66:69], v[54:57]
	v_mfma_f32_16x16x32_f16 v[42:45], v[90:93], v[66:69], v[42:45]
	v_mfma_f32_16x16x32_f16 v[58:61], v[74:77], v[70:73], v[58:61]
	v_mfma_f32_16x16x32_f16 v[22:25], v[86:89], v[70:73], v[22:25]
	v_mfma_f32_16x16x32_f16 v[18:21], v[90:93], v[70:73], v[18:21]
	s_waitcnt lgkmcnt(0)
	v_mfma_f32_16x16x32_f16 v[30:33], v[102:105], v[38:41], v[30:33]
	v_mfma_f32_16x16x32_f16 v[34:37], v[106:109], v[38:41], v[34:37]
	v_mfma_f32_16x16x32_f16 v[14:17], v[110:113], v[38:41], v[14:17]
	ds_read_b128 v[38:41], v0
	ds_read_b128 v[62:65], v0 offset:2048
	ds_read_b128 v[66:69], v0 offset:4096
	ds_read_b128 v[0:3], v0 offset:6144
	ds_read_b128 v[70:73], v5 offset:16384
	ds_read_b128 v[74:77], v5 offset:18432
	ds_read_b128 v[86:89], v5 offset:20480
	v_mfma_f32_16x16x32_f16 v[4:7], v[102:105], v[46:49], v[78:81]
	v_mfma_f32_16x16x32_f16 v[78:81], v[106:109], v[46:49], v[82:85]
	v_mfma_f32_16x16x32_f16 v[26:29], v[110:113], v[46:49], v[26:29]
	v_mfma_f32_16x16x32_f16 v[46:49], v[102:105], v[94:97], v[50:53]
	v_mfma_f32_16x16x32_f16 v[50:53], v[106:109], v[94:97], v[54:57]
	v_mfma_f32_16x16x32_f16 v[42:45], v[110:113], v[94:97], v[42:45]
	v_mfma_f32_16x16x32_f16 v[54:57], v[102:105], v[98:101], v[58:61]
	v_mfma_f32_16x16x32_f16 v[22:25], v[106:109], v[98:101], v[22:25]
	v_mfma_f32_16x16x32_f16 v[18:21], v[110:113], v[98:101], v[18:21]
	s_waitcnt lgkmcnt(0)
	v_mfma_f32_16x16x32_f16 v[30:33], v[70:73], v[38:41], v[30:33]
	v_mfma_f32_16x16x32_f16 v[34:37], v[74:77], v[38:41], v[34:37]
	v_mfma_f32_16x16x32_f16 v[14:17], v[86:89], v[38:41], v[14:17]
	v_mfma_f32_16x16x32_f16 v[38:41], v[70:73], v[62:65], v[4:7]
	v_mfma_f32_16x16x32_f16 v[58:61], v[74:77], v[62:65], v[78:81]
	v_mfma_f32_16x16x32_f16 v[26:29], v[86:89], v[62:65], v[26:29]
	v_mfma_f32_16x16x32_f16 v[46:49], v[70:73], v[66:69], v[46:49]
	v_mfma_f32_16x16x32_f16 v[50:53], v[74:77], v[66:69], v[50:53]
	v_mfma_f32_16x16x32_f16 v[42:45], v[86:89], v[66:69], v[42:45]
	v_mfma_f32_16x16x32_f16 v[54:57], v[70:73], v[0:3], v[54:57]
	v_mfma_f32_16x16x32_f16 v[4:7], v[74:77], v[0:3], v[22:25]
	v_mfma_f32_16x16x32_f16 v[0:3], v[86:89], v[0:3], v[18:21]
	s_lshl_b32 s0, s12, 1
	v_or_b32_e32 v11, s10, v11
	s_and_b32 s5, s0, 0x3fffff0
	s_movk_i32 s0, 0x3c0
	v_mad_u32_u24 v62, v9, 48, s11
	v_lshlrev_b32_e32 v24, 2, v12
	v_and_or_b32 v63, v11, s0, v8
	s_movk_i32 s0, 0x400
	s_mov_b32 s4, 0x3e38aa3b
	v_and_or_b32 v20, v10, 48, v24
	v_pk_mul_f32 v[10:11], v[32:33], s[4:5] op_sel_hi:[1,0]
	v_cmp_gt_u32_e32 vcc, s0, v62
	v_pk_mul_f32 v[12:13], v[30:31], s[4:5] op_sel_hi:[1,0]
	v_lshrrev_b32_e32 v8, 10, v62
	v_cndmask_b32_e32 v9, v33, v11, vcc
	v_cndmask_b32_e32 v11, v32, v10, vcc
	v_lshrrev_b32_e32 v18, 6, v62
	v_cndmask_b32_e32 v10, v31, v13, vcc
	v_cndmask_b32_e32 v12, v30, v12, vcc
	v_cvt_pk_f16_f32 v11, v11, v9
	v_mov_b32_e32 v9, 0
	v_cvt_pk_f16_f32 v10, v12, v10
	v_lshlrev_b64 v[12:13], 22, v[8:9]
	v_and_or_b32 v8, v18, 15, s5
	v_lshlrev_b32_e32 v30, 10, v8
	v_or_b32_e32 v8, v30, v63
	v_lshl_add_u64 v[12:13], s[8:9], 0, v[12:13]
	v_lshlrev_b64 v[18:19], 7, v[8:9]
	v_lshl_add_u64 v[18:19], v[12:13], 0, v[18:19]
	v_lshlrev_b32_e32 v8, 1, v20
	v_lshl_add_u64 v[18:19], v[18:19], 0, v[8:9]
	s_movk_i32 s0, 0x3f0
	global_store_dwordx2 v[18:19], v[10:11], off
	v_add_u32_e32 v11, 16, v62
	v_pk_mul_f32 v[18:19], v[36:37], s[4:5] op_sel_hi:[1,0]
	v_pk_mul_f32 v[20:21], v[34:35], s[4:5] op_sel_hi:[1,0]
	v_cmp_gt_u32_e64 s[0:1], s0, v62
	v_lshrrev_b32_e32 v10, 10, v11
	v_and_or_b32 v23, v11, 48, v24
	v_cndmask_b32_e64 v22, v36, v18, s[0:1]
	v_cndmask_b32_e64 v18, v35, v21, s[0:1]
	v_cndmask_b32_e64 v20, v34, v20, s[0:1]
	v_lshrrev_b32_e32 v21, 6, v11
	v_cvt_pk_f16_f32 v18, v20, v18
	v_and_or_b32 v20, v21, 15, s5
	v_mov_b32_e32 v11, v9
	v_lshlrev_b32_e32 v31, 10, v20
	v_lshlrev_b64 v[10:11], 22, v[10:11]
	v_or_b32_e32 v20, v31, v63
	v_mov_b32_e32 v21, v9
	v_cndmask_b32_e64 v19, v37, v19, s[0:1]
	v_lshl_add_u64 v[10:11], s[8:9], 0, v[10:11]
	v_lshlrev_b64 v[20:21], 7, v[20:21]
	v_cvt_pk_f16_f32 v19, v22, v19
	v_lshl_add_u64 v[20:21], v[10:11], 0, v[20:21]
	v_lshlrev_b32_e32 v22, 1, v23
	v_mov_b32_e32 v23, v9
	v_lshl_add_u64 v[20:21], v[20:21], 0, v[22:23]
	global_store_dwordx2 v[20:21], v[18:19], off
	v_add_u32_e32 v19, 32, v62
	s_movk_i32 s2, 0x3e0
	v_and_or_b32 v33, v19, 48, v24
	v_pk_mul_f32 v[20:21], v[16:17], s[4:5] op_sel_hi:[1,0]
	v_pk_mul_f32 v[24:25], v[14:15], s[4:5] op_sel_hi:[1,0]
	v_cmp_gt_u32_e64 s[2:3], s2, v62
	v_lshrrev_b32_e32 v18, 10, v19
	v_lshrrev_b32_e32 v32, 6, v19
	v_cndmask_b32_e64 v17, v17, v21, s[2:3]
	v_cndmask_b32_e64 v16, v16, v20, s[2:3]
	v_cndmask_b32_e64 v15, v15, v25, s[2:3]
	v_cndmask_b32_e64 v14, v14, v24, s[2:3]
	v_mov_b32_e32 v19, v9
	v_cvt_pk_f16_f32 v14, v14, v15
	v_cvt_pk_f16_f32 v15, v16, v17
	v_lshlrev_b64 v[16:17], 22, v[18:19]
	v_and_or_b32 v18, v32, 15, s5
	v_lshlrev_b32_e32 v24, 10, v18
	v_or_b32_e32 v18, v24, v63
	v_lshl_add_u64 v[16:17], s[8:9], 0, v[16:17]
	v_lshlrev_b64 v[18:19], 7, v[18:19]
	v_lshl_add_u64 v[18:19], v[16:17], 0, v[18:19]
	v_lshlrev_b32_e32 v20, 1, v33
	v_mov_b32_e32 v21, v9
	v_lshl_add_u64 v[18:19], v[18:19], 0, v[20:21]
	global_store_dwordx2 v[18:19], v[14:15], off
	v_pk_mul_f32 v[14:15], v[40:41], s[4:5] op_sel_hi:[1,0]
	v_pk_mul_f32 v[18:19], v[38:39], s[4:5] op_sel_hi:[1,0]
	v_or_b32_e32 v25, 16, v63
	v_cndmask_b32_e32 v32, v40, v14, vcc
	v_cndmask_b32_e32 v14, v39, v19, vcc
	v_cndmask_b32_e32 v18, v38, v18, vcc
	v_cvt_pk_f16_f32 v14, v18, v14
	v_or_b32_e32 v18, v30, v25
	v_mov_b32_e32 v19, v9
	v_lshlrev_b64 v[18:19], 7, v[18:19]
	v_cndmask_b32_e32 v15, v41, v15, vcc
	v_lshl_add_u64 v[18:19], v[12:13], 0, v[18:19]
	v_cvt_pk_f16_f32 v15, v32, v15
	v_lshl_add_u64 v[18:19], v[18:19], 0, v[8:9]
	global_store_dwordx2 v[18:19], v[14:15], off
	v_pk_mul_f32 v[14:15], v[60:61], s[4:5] op_sel_hi:[1,0]
	v_pk_mul_f32 v[18:19], v[58:59], s[4:5] op_sel_hi:[1,0]
	v_cndmask_b32_e64 v32, v60, v14, s[0:1]
	v_cndmask_b32_e64 v14, v59, v19, s[0:1]
	v_cndmask_b32_e64 v18, v58, v18, s[0:1]
	v_cvt_pk_f16_f32 v14, v18, v14
	v_or_b32_e32 v18, v31, v25
	v_mov_b32_e32 v19, v9
	v_lshlrev_b64 v[18:19], 7, v[18:19]
	v_cndmask_b32_e64 v15, v61, v15, s[0:1]
	v_lshl_add_u64 v[18:19], v[10:11], 0, v[18:19]
	v_cvt_pk_f16_f32 v15, v32, v15
	v_lshl_add_u64 v[18:19], v[18:19], 0, v[22:23]
	global_store_dwordx2 v[18:19], v[14:15], off
	v_pk_mul_f32 v[14:15], v[28:29], s[4:5] op_sel_hi:[1,0]
	v_pk_mul_f32 v[18:19], v[26:27], s[4:5] op_sel_hi:[1,0]
	v_cndmask_b32_e64 v28, v28, v14, s[2:3]
	v_cndmask_b32_e64 v14, v27, v19, s[2:3]
	v_cndmask_b32_e64 v18, v26, v18, s[2:3]
	v_cvt_pk_f16_f32 v14, v18, v14
	v_or_b32_e32 v18, v24, v25
	v_mov_b32_e32 v19, v9
	v_lshlrev_b64 v[18:19], 7, v[18:19]
	v_cndmask_b32_e64 v15, v29, v15, s[2:3]
	v_lshl_add_u64 v[18:19], v[16:17], 0, v[18:19]
	v_cvt_pk_f16_f32 v15, v28, v15
	v_lshl_add_u64 v[18:19], v[18:19], 0, v[20:21]
	global_store_dwordx2 v[18:19], v[14:15], off
	v_pk_mul_f32 v[14:15], v[48:49], s[4:5] op_sel_hi:[1,0]
	v_pk_mul_f32 v[18:19], v[46:47], s[4:5] op_sel_hi:[1,0]
	v_or_b32_e32 v25, 32, v63
	v_cndmask_b32_e32 v26, v48, v14, vcc
	v_cndmask_b32_e32 v14, v47, v19, vcc
	v_cndmask_b32_e32 v18, v46, v18, vcc
	v_cvt_pk_f16_f32 v14, v18, v14
	v_or_b32_e32 v18, v30, v25
	v_mov_b32_e32 v19, v9
	v_lshlrev_b64 v[18:19], 7, v[18:19]
	v_cndmask_b32_e32 v15, v49, v15, vcc
	v_lshl_add_u64 v[18:19], v[12:13], 0, v[18:19]
	v_cvt_pk_f16_f32 v15, v26, v15
	v_lshl_add_u64 v[18:19], v[18:19], 0, v[8:9]
	global_store_dwordx2 v[18:19], v[14:15], off
	v_pk_mul_f32 v[14:15], v[52:53], s[4:5] op_sel_hi:[1,0]
	v_pk_mul_f32 v[18:19], v[50:51], s[4:5] op_sel_hi:[1,0]
	v_cndmask_b32_e64 v26, v52, v14, s[0:1]
	v_cndmask_b32_e64 v14, v51, v19, s[0:1]
	v_cndmask_b32_e64 v18, v50, v18, s[0:1]
	v_cvt_pk_f16_f32 v14, v18, v14
	v_or_b32_e32 v18, v31, v25
	v_mov_b32_e32 v19, v9
	v_lshlrev_b64 v[18:19], 7, v[18:19]
	v_cndmask_b32_e64 v15, v53, v15, s[0:1]
	v_lshl_add_u64 v[18:19], v[10:11], 0, v[18:19]
	v_cvt_pk_f16_f32 v15, v26, v15
	v_lshl_add_u64 v[18:19], v[18:19], 0, v[22:23]
	global_store_dwordx2 v[18:19], v[14:15], off
	v_pk_mul_f32 v[14:15], v[44:45], s[4:5] op_sel_hi:[1,0]
	v_pk_mul_f32 v[18:19], v[42:43], s[4:5] op_sel_hi:[1,0]
	v_cndmask_b32_e64 v26, v44, v14, s[2:3]
	v_cndmask_b32_e64 v14, v43, v19, s[2:3]
	v_cndmask_b32_e64 v18, v42, v18, s[2:3]
	v_cvt_pk_f16_f32 v14, v18, v14
	v_or_b32_e32 v18, v24, v25
	v_mov_b32_e32 v19, v9
	v_lshlrev_b64 v[18:19], 7, v[18:19]
	v_cndmask_b32_e64 v15, v45, v15, s[2:3]
	v_lshl_add_u64 v[18:19], v[16:17], 0, v[18:19]
	v_cvt_pk_f16_f32 v15, v26, v15
	v_lshl_add_u64 v[18:19], v[18:19], 0, v[20:21]
	global_store_dwordx2 v[18:19], v[14:15], off
	v_pk_mul_f32 v[14:15], v[56:57], s[4:5] op_sel_hi:[1,0]
	v_pk_mul_f32 v[18:19], v[54:55], s[4:5] op_sel_hi:[1,0]
	v_or_b32_e32 v25, 48, v63
	v_cndmask_b32_e32 v26, v56, v14, vcc
	v_cndmask_b32_e32 v14, v55, v19, vcc
	v_cndmask_b32_e32 v18, v54, v18, vcc
	v_cvt_pk_f16_f32 v14, v18, v14
	v_or_b32_e32 v18, v30, v25
	v_mov_b32_e32 v19, v9
	v_lshlrev_b64 v[18:19], 7, v[18:19]
	v_cndmask_b32_e32 v15, v57, v15, vcc
	v_lshl_add_u64 v[12:13], v[12:13], 0, v[18:19]
	v_cvt_pk_f16_f32 v15, v26, v15
	v_lshl_add_u64 v[12:13], v[12:13], 0, v[8:9]
	global_store_dwordx2 v[12:13], v[14:15], off
	v_pk_mul_f32 v[12:13], v[6:7], s[4:5] op_sel_hi:[1,0]
	v_pk_mul_f32 v[14:15], v[4:5], s[4:5] op_sel_hi:[1,0]
	v_cndmask_b32_e64 v7, v7, v13, s[0:1]
	v_cndmask_b32_e64 v6, v6, v12, s[0:1]
	v_cndmask_b32_e64 v5, v5, v15, s[0:1]
	v_cndmask_b32_e64 v4, v4, v14, s[0:1]
	v_or_b32_e32 v8, v31, v25
	v_cvt_pk_f16_f32 v4, v4, v5
	v_cvt_pk_f16_f32 v5, v6, v7
	v_lshlrev_b64 v[6:7], 7, v[8:9]
	v_lshl_add_u64 v[6:7], v[10:11], 0, v[6:7]
	v_lshl_add_u64 v[6:7], v[6:7], 0, v[22:23]
	global_store_dwordx2 v[6:7], v[4:5], off
	v_pk_mul_f32 v[4:5], v[2:3], s[4:5] op_sel_hi:[1,0]
	v_pk_mul_f32 v[6:7], v[0:1], s[4:5] op_sel_hi:[1,0]
	v_cndmask_b32_e64 v3, v3, v5, s[2:3]
	v_cndmask_b32_e64 v2, v2, v4, s[2:3]
	v_cndmask_b32_e64 v1, v1, v7, s[2:3]
	v_cndmask_b32_e64 v0, v0, v6, s[2:3]
	v_or_b32_e32 v8, v24, v25
	v_cvt_pk_f16_f32 v0, v0, v1
	v_cvt_pk_f16_f32 v1, v2, v3
	v_lshlrev_b64 v[2:3], 7, v[8:9]
	v_lshl_add_u64 v[2:3], v[16:17], 0, v[2:3]
	v_lshl_add_u64 v[2:3], v[2:3], 0, v[20:21]
	global_store_dwordx2 v[2:3], v[0:1], off
	s_endpgm
	s_endpgm
	s_endpgm
	s_endpgm
	s_endpgm
	s_endpgm
	s_endpgm
	s_endpgm
	s_endpgm
	s_endpgm
	s_endpgm
	s_endpgm
	s_endpgm
	s_endpgm
	s_endpgm
	s_endpgm
	s_endpgm
	s_endpgm
	s_endpgm
	s_endpgm
	s_endpgm
	s_endpgm
	s_endpgm
	s_endpgm
	s_endpgm
	s_endpgm
	s_endpgm
	s_endpgm
	s_endpgm
	s_endpgm
	s_endpgm
	s_endpgm
	s_endpgm
	s_endpgm
	s_endpgm
	s_endpgm
	s_endpgm
	s_endpgm
	s_endpgm
	s_endpgm
	s_endpgm
	s_endpgm
	s_endpgm
	s_endpgm
	s_endpgm
	s_endpgm
	s_endpgm
	s_endpgm
	s_endpgm
	s_endpgm
	s_endpgm
	s_endpgm
	.section	.rodata,"a",@progbits
	.p2align	6, 0x0

_Z5gemm8ILi128ELi2ELi2ELi2ELi1ELi16EEvPKDF16_S1_iiiPDF16_PfPKf:
	v_readfirstlane_b32 s24, v0
	s_nop 3
	s_nop 0
	s_bitcmp1_b32 s24, 8
	s_cbranch_scc0 .Lprio_skip1
	s_setprio 1

.LBB5_4:
	s_load_dwordx2 s[2:3], s[0:1], 0x14
	v_lshrrev_b32_e32 v3, 4, v0
	s_lshl_b32 s12, s15, 7
	s_lshl_b32 s13, s14, 7
	v_xor_b32_e32 v1, v3, v0
	s_waitcnt lgkmcnt(0)
	s_ashr_i32 s14, s3, 31
	s_mul_i32 s0, s12, s14
	s_mul_hi_u32 s1, s12, s3
	v_lshlrev_b32_e32 v1, 3, v1
	v_or_b32_e32 v4, 0x200, v0
	s_add_i32 s1, s1, s0
	s_mul_i32 s0, s12, s3
	v_and_b32_e32 v2, 56, v1
	v_lshrrev_b32_e32 v1, 3, v0
	v_lshrrev_b32_e32 v4, 3, v4
	s_lshl_b64 s[0:1], s[0:1], 1
	v_mul_lo_u32 v1, v1, s3
	v_mul_lo_u32 v4, v4, s3
	s_add_u32 s0, s4, s0
	v_add_lshl_u32 v1, v1, v2, 1
	v_add_lshl_u32 v2, v4, v2, 1
	s_addc_u32 s1, s5, s1
	s_mul_i32 s4, s13, s14
	s_mul_hi_u32 s5, s13, s3
	v_lshl_add_u32 v4, v0, 4, 0
	s_add_i32 s5, s5, s4
	s_mul_i32 s4, s13, s3
	v_readfirstlane_b32 s18, v4
	v_add_u32_e32 v5, 0x2000, v4
	s_lshl_b64 s[4:5], s[4:5], 1
	s_mov_b32 m0, s18
	v_readfirstlane_b32 s15, v5
	v_add_u32_e32 v5, 0x4000, v4
	s_add_u32 s4, s6, s4
	global_load_lds_dwordx4 v1, s[0:1]
	s_mov_b32 m0, s15
	v_readfirstlane_b32 s16, v5
	v_add_u32_e32 v5, 0x6000, v4
	s_addc_u32 s5, s7, s5
	global_load_lds_dwordx4 v2, s[0:1]
	s_mov_b32 m0, s16
	v_readfirstlane_b32 s17, v5
	v_add_u32_e32 v5, 0x8000, v4
	global_load_lds_dwordx4 v1, s[4:5]
	s_mov_b32 m0, s17
	s_add_u32 s6, s0, 0x80
	v_readfirstlane_b32 s14, v5
	v_add_u32_e32 v5, 0xa000, v4
	global_load_lds_dwordx4 v2, s[4:5]
	s_addc_u32 s7, s1, 0
	s_mov_b32 m0, s14
	v_readfirstlane_b32 s3, v5
	global_load_lds_dwordx4 v1, s[6:7]
	s_mov_b32 m0, s3
	v_add_u32_e32 v5, 0xc000, v4
	s_add_u32 s20, s4, 0x80
	global_load_lds_dwordx4 v2, s[6:7]
	v_readfirstlane_b32 s6, v5
	v_add_u32_e32 v4, 0xe000, v4
	s_addc_u32 s21, s5, 0
	s_mov_b32 m0, s6
	v_readfirstlane_b32 s7, v4
	global_load_lds_dwordx4 v1, s[20:21]
	s_mov_b32 m0, s7
	v_lshrrev_b32_e32 v5, 1, v0
	global_load_lds_dwordx4 v2, s[20:21]
	v_bfe_u32 v6, v0, 1, 3
	v_and_b32_e32 v4, 15, v0
	v_lshrrev_b32_e32 v7, 2, v0
	v_bitop3_b32 v3, v3, v6, 3 bitop3:0x6c
	v_and_b32_e32 v8, 0x60, v5
	v_and_or_b32 v32, v7, 64, v4
	v_lshlrev_b32_e32 v7, 4, v3
	v_or_b32_e32 v3, v8, v4
	v_lshl_add_u32 v4, v3, 7, 0
	s_waitcnt vmcnt(4)
	s_barrier
	v_add_u32_e32 v3, v4, v7
	ds_read_b128 v[10:13], v3 offset:16384
	v_lshl_add_u32 v30, v32, 7, 0
	v_add_u32_e32 v5, v30, v7
	ds_read_b128 v[14:17], v5
	ds_read_b128 v[18:21], v3 offset:18432
	ds_read_b128 v[22:25], v5 offset:2048
	ds_read_b128 v[34:37], v5 offset:4096
	ds_read_b128 v[38:41], v5 offset:6144
	v_bfe_u32 v9, v0, 4, 2
	v_bitop3_b32 v0, v9, v6, 4 bitop3:0x36
	s_waitcnt lgkmcnt(0)
	v_mfma_f32_16x16x32_f16 v[26:29], v[10:13], v[14:17], 0
	v_lshlrev_b32_e32 v6, 4, v0
	v_mfma_f32_16x16x32_f16 v[14:17], v[18:21], v[14:17], 0
	v_add_u32_e32 v0, v30, v6
	ds_read_b128 v[42:45], v0
	ds_read_b128 v[46:49], v0 offset:2048
	ds_read_b128 v[50:53], v0 offset:4096
	ds_read_b128 v[54:57], v0 offset:6144
	v_add_u32_e32 v4, v4, v6
	ds_read_b128 v[58:61], v4 offset:16384
	ds_read_b128 v[62:65], v4 offset:18432
	v_mfma_f32_16x16x32_f16 v[66:69], v[10:13], v[22:25], 0
	v_mfma_f32_16x16x32_f16 v[22:25], v[18:21], v[22:25], 0
	v_mfma_f32_16x16x32_f16 v[70:73], v[10:13], v[34:37], 0
	v_mfma_f32_16x16x32_f16 v[34:37], v[18:21], v[34:37], 0
	v_mfma_f32_16x16x32_f16 v[10:13], v[10:13], v[38:41], 0
	v_mfma_f32_16x16x32_f16 v[18:21], v[18:21], v[38:41], 0
	s_add_u32 s20, s0, 0x100
	s_mov_b32 m0, s18
	s_waitcnt vmcnt(0) lgkmcnt(0)
	s_barrier
	s_addc_u32 s21, s1, 0
	s_add_u32 s22, s4, 0x100
	global_load_lds_dwordx4 v1, s[20:21]
	s_mov_b32 m0, s15
	s_addc_u32 s23, s5, 0
	global_load_lds_dwordx4 v2, s[20:21]
	s_mov_b32 m0, s16
	s_nop 0
	global_load_lds_dwordx4 v1, s[22:23]
	s_mov_b32 m0, s17
	s_nop 0
	global_load_lds_dwordx4 v2, s[22:23]
	s_waitcnt lgkmcnt(0)
	v_mfma_f32_16x16x32_f16 v[26:29], v[58:61], v[42:45], v[26:29]
	v_mfma_f32_16x16x32_f16 v[14:17], v[62:65], v[42:45], v[14:17]
	ds_read_b128 v[38:41], v5 offset:32768
	ds_read_b128 v[42:45], v5 offset:34816
	ds_read_b128 v[74:77], v5 offset:36864
	ds_read_b128 v[78:81], v5 offset:38912
	ds_read_b128 v[82:85], v3 offset:49152
	ds_read_b128 v[86:89], v3 offset:51200
	v_mfma_f32_16x16x32_f16 v[66:69], v[58:61], v[46:49], v[66:69]
	v_mfma_f32_16x16x32_f16 v[22:25], v[62:65], v[46:49], v[22:25]
	v_mfma_f32_16x16x32_f16 v[46:49], v[58:61], v[50:53], v[70:73]
	v_mfma_f32_16x16x32_f16 v[34:37], v[62:65], v[50:53], v[34:37]
	v_mfma_f32_16x16x32_f16 v[10:13], v[58:61], v[54:57], v[10:13]
	v_mfma_f32_16x16x32_f16 v[18:21], v[62:65], v[54:57], v[18:21]
	s_waitcnt lgkmcnt(0)
	v_mfma_f32_16x16x32_f16 v[26:29], v[82:85], v[38:41], v[26:29]
	v_mfma_f32_16x16x32_f16 v[14:17], v[86:89], v[38:41], v[14:17]
	ds_read_b128 v[38:41], v0 offset:32768
	ds_read_b128 v[50:53], v0 offset:34816
	ds_read_b128 v[54:57], v0 offset:36864
	ds_read_b128 v[58:61], v0 offset:38912
	ds_read_b128 v[62:65], v4 offset:49152
	ds_read_b128 v[70:73], v4 offset:51200
	v_mfma_f32_16x16x32_f16 v[66:69], v[82:85], v[42:45], v[66:69]
	v_mfma_f32_16x16x32_f16 v[22:25], v[86:89], v[42:45], v[22:25]
	v_mfma_f32_16x16x32_f16 v[42:45], v[82:85], v[74:77], v[46:49]
	v_mfma_f32_16x16x32_f16 v[34:37], v[86:89], v[74:77], v[34:37]
	v_mfma_f32_16x16x32_f16 v[10:13], v[82:85], v[78:81], v[10:13]
	v_mfma_f32_16x16x32_f16 v[18:21], v[86:89], v[78:81], v[18:21]
	s_add_u32 s20, s0, 0x180
	s_mov_b32 m0, s14
	s_waitcnt vmcnt(0) lgkmcnt(0)
	s_barrier
	s_addc_u32 s21, s1, 0
	s_add_u32 s22, s4, 0x180
	global_load_lds_dwordx4 v1, s[20:21]
	s_mov_b32 m0, s3
	s_addc_u32 s23, s5, 0
	global_load_lds_dwordx4 v2, s[20:21]
	s_mov_b32 m0, s6
	s_nop 0
	global_load_lds_dwordx4 v1, s[22:23]
	s_mov_b32 m0, s7
	s_nop 0
	global_load_lds_dwordx4 v2, s[22:23]
	s_waitcnt lgkmcnt(0)
	v_mfma_f32_16x16x32_f16 v[26:29], v[62:65], v[38:41], v[26:29]
	v_mfma_f32_16x16x32_f16 v[14:17], v[70:73], v[38:41], v[14:17]
	ds_read_b128 v[38:41], v5
	ds_read_b128 v[46:49], v5 offset:2048
	ds_read_b128 v[74:77], v5 offset:4096
	ds_read_b128 v[78:81], v5 offset:6144
	ds_read_b128 v[82:85], v3 offset:16384
	ds_read_b128 v[86:89], v3 offset:18432
	v_mfma_f32_16x16x32_f16 v[66:69], v[62:65], v[50:53], v[66:69]
	v_mfma_f32_16x16x32_f16 v[22:25], v[70:73], v[50:53], v[22:25]
	v_mfma_f32_16x16x32_f16 v[42:45], v[62:65], v[54:57], v[42:45]
	v_mfma_f32_16x16x32_f16 v[34:37], v[70:73], v[54:57], v[34:37]
	v_mfma_f32_16x16x32_f16 v[10:13], v[62:65], v[58:61], v[10:13]
	v_mfma_f32_16x16x32_f16 v[18:21], v[70:73], v[58:61], v[18:21]
	s_waitcnt lgkmcnt(0)
	v_mfma_f32_16x16x32_f16 v[26:29], v[82:85], v[38:41], v[26:29]
	v_mfma_f32_16x16x32_f16 v[14:17], v[86:89], v[38:41], v[14:17]
	ds_read_b128 v[38:41], v0
	ds_read_b128 v[50:53], v0 offset:2048
	ds_read_b128 v[54:57], v0 offset:4096
	ds_read_b128 v[58:61], v0 offset:6144
	ds_read_b128 v[62:65], v4 offset:16384
	ds_read_b128 v[70:73], v4 offset:18432
	v_mfma_f32_16x16x32_f16 v[66:69], v[82:85], v[46:49], v[66:69]
	v_mfma_f32_16x16x32_f16 v[22:25], v[86:89], v[46:49], v[22:25]
	v_mfma_f32_16x16x32_f16 v[42:45], v[82:85], v[74:77], v[42:45]
	v_mfma_f32_16x16x32_f16 v[34:37], v[86:89], v[74:77], v[34:37]
	v_mfma_f32_16x16x32_f16 v[10:13], v[82:85], v[78:81], v[10:13]
	v_mfma_f32_16x16x32_f16 v[18:21], v[86:89], v[78:81], v[18:21]
	s_add_u32 s20, s0, 0x200
	s_mov_b32 m0, s18
	s_waitcnt vmcnt(0) lgkmcnt(0)
	s_barrier
	s_addc_u32 s21, s1, 0
	s_add_u32 s22, s4, 0x200
	global_load_lds_dwordx4 v1, s[20:21]
	s_mov_b32 m0, s15
	s_addc_u32 s23, s5, 0
	global_load_lds_dwordx4 v2, s[20:21]
	s_mov_b32 m0, s16
	s_nop 0
	global_load_lds_dwordx4 v1, s[22:23]
	s_mov_b32 m0, s17
	s_nop 0
	global_load_lds_dwordx4 v2, s[22:23]
	s_waitcnt lgkmcnt(0)
	v_mfma_f32_16x16x32_f16 v[26:29], v[62:65], v[38:41], v[26:29]
	v_mfma_f32_16x16x32_f16 v[14:17], v[70:73], v[38:41], v[14:17]
	ds_read_b128 v[38:41], v5 offset:32768
	ds_read_b128 v[46:49], v5 offset:34816
	ds_read_b128 v[74:77], v5 offset:36864
	ds_read_b128 v[78:81], v5 offset:38912
	ds_read_b128 v[82:85], v3 offset:49152
	ds_read_b128 v[86:89], v3 offset:51200
	v_mfma_f32_16x16x32_f16 v[66:69], v[62:65], v[50:53], v[66:69]
	v_mfma_f32_16x16x32_f16 v[22:25], v[70:73], v[50:53], v[22:25]
	v_mfma_f32_16x16x32_f16 v[42:45], v[62:65], v[54:57], v[42:45]
	v_mfma_f32_16x16x32_f16 v[34:37], v[70:73], v[54:57], v[34:37]
	v_mfma_f32_16x16x32_f16 v[10:13], v[62:65], v[58:61], v[10:13]
	v_mfma_f32_16x16x32_f16 v[18:21], v[70:73], v[58:61], v[18:21]
	s_waitcnt lgkmcnt(0)
	v_mfma_f32_16x16x32_f16 v[26:29], v[82:85], v[38:41], v[26:29]
	v_mfma_f32_16x16x32_f16 v[14:17], v[86:89], v[38:41], v[14:17]
	ds_read_b128 v[38:41], v0 offset:32768
	ds_read_b128 v[50:53], v0 offset:34816
	ds_read_b128 v[54:57], v0 offset:36864
	ds_read_b128 v[58:61], v0 offset:38912
	ds_read_b128 v[62:65], v4 offset:49152
	ds_read_b128 v[70:73], v4 offset:51200
	v_mfma_f32_16x16x32_f16 v[66:69], v[82:85], v[46:49], v[66:69]
	v_mfma_f32_16x16x32_f16 v[22:25], v[86:89], v[46:49], v[22:25]
	v_mfma_f32_16x16x32_f16 v[42:45], v[82:85], v[74:77], v[42:45]
	v_mfma_f32_16x16x32_f16 v[34:37], v[86:89], v[74:77], v[34:37]
	v_mfma_f32_16x16x32_f16 v[10:13], v[82:85], v[78:81], v[10:13]
	v_mfma_f32_16x16x32_f16 v[18:21], v[86:89], v[78:81], v[18:21]
	s_add_u32 s20, s0, 0x280
	s_mov_b32 m0, s14
	s_waitcnt vmcnt(0) lgkmcnt(0)
	s_barrier
	s_addc_u32 s21, s1, 0
	s_add_u32 s22, s4, 0x280
	global_load_lds_dwordx4 v1, s[20:21]
	s_mov_b32 m0, s3
	s_addc_u32 s23, s5, 0
	global_load_lds_dwordx4 v2, s[20:21]
	s_mov_b32 m0, s6
	s_nop 0
	global_load_lds_dwordx4 v1, s[22:23]
	s_mov_b32 m0, s7
	s_nop 0
	global_load_lds_dwordx4 v2, s[22:23]
	s_waitcnt lgkmcnt(0)
	v_mfma_f32_16x16x32_f16 v[26:29], v[62:65], v[38:41], v[26:29]
	v_mfma_f32_16x16x32_f16 v[14:17], v[70:73], v[38:41], v[14:17]
	ds_read_b128 v[38:41], v5
	ds_read_b128 v[46:49], v5 offset:2048
	ds_read_b128 v[74:77], v5 offset:4096
	ds_read_b128 v[78:81], v5 offset:6144
	ds_read_b128 v[82:85], v3 offset:16384
	ds_read_b128 v[86:89], v3 offset:18432
	v_mfma_f32_16x16x32_f16 v[66:69], v[62:65], v[50:53], v[66:69]
	v_mfma_f32_16x16x32_f16 v[22:25], v[70:73], v[50:53], v[22:25]
	v_mfma_f32_16x16x32_f16 v[42:45], v[62:65], v[54:57], v[42:45]
	v_mfma_f32_16x16x32_f16 v[34:37], v[70:73], v[54:57], v[34:37]
	v_mfma_f32_16x16x32_f16 v[10:13], v[62:65], v[58:61], v[10:13]
	v_mfma_f32_16x16x32_f16 v[18:21], v[70:73], v[58:61], v[18:21]
	s_waitcnt lgkmcnt(0)
	v_mfma_f32_16x16x32_f16 v[26:29], v[82:85], v[38:41], v[26:29]
	v_mfma_f32_16x16x32_f16 v[14:17], v[86:89], v[38:41], v[14:17]
	ds_read_b128 v[38:41], v0
	ds_read_b128 v[50:53], v0 offset:2048
	ds_read_b128 v[54:57], v0 offset:4096
	ds_read_b128 v[58:61], v0 offset:6144
	ds_read_b128 v[62:65], v4 offset:16384
	ds_read_b128 v[70:73], v4 offset:18432
	v_mfma_f32_16x16x32_f16 v[66:69], v[82:85], v[46:49], v[66:69]
	v_mfma_f32_16x16x32_f16 v[22:25], v[86:89], v[46:49], v[22:25]
	v_mfma_f32_16x16x32_f16 v[42:45], v[82:85], v[74:77], v[42:45]
	v_mfma_f32_16x16x32_f16 v[34:37], v[86:89], v[74:77], v[34:37]
	v_mfma_f32_16x16x32_f16 v[10:13], v[82:85], v[78:81], v[10:13]
	v_mfma_f32_16x16x32_f16 v[18:21], v[86:89], v[78:81], v[18:21]
	s_add_u32 s20, s0, 0x300
	s_mov_b32 m0, s18
	s_waitcnt vmcnt(0) lgkmcnt(0)
	s_barrier
	s_addc_u32 s21, s1, 0
	s_add_u32 s22, s4, 0x300
	global_load_lds_dwordx4 v1, s[20:21]
	s_mov_b32 m0, s15
	s_addc_u32 s23, s5, 0
	global_load_lds_dwordx4 v2, s[20:21]
	s_mov_b32 m0, s16
	s_nop 0
	global_load_lds_dwordx4 v1, s[22:23]
	s_mov_b32 m0, s17
	s_nop 0
	global_load_lds_dwordx4 v2, s[22:23]
	s_waitcnt lgkmcnt(0)
	v_mfma_f32_16x16x32_f16 v[26:29], v[62:65], v[38:41], v[26:29]
	v_mfma_f32_16x16x32_f16 v[14:17], v[70:73], v[38:41], v[14:17]
	ds_read_b128 v[38:41], v5 offset:32768
	ds_read_b128 v[46:49], v5 offset:34816
	ds_read_b128 v[74:77], v5 offset:36864
	ds_read_b128 v[78:81], v5 offset:38912
	ds_read_b128 v[82:85], v3 offset:49152
	ds_read_b128 v[86:89], v3 offset:51200
	v_mfma_f32_16x16x32_f16 v[66:69], v[62:65], v[50:53], v[66:69]
	v_mfma_f32_16x16x32_f16 v[22:25], v[70:73], v[50:53], v[22:25]
	v_mfma_f32_16x16x32_f16 v[42:45], v[62:65], v[54:57], v[42:45]
	v_mfma_f32_16x16x32_f16 v[34:37], v[70:73], v[54:57], v[34:37]
	v_mfma_f32_16x16x32_f16 v[10:13], v[62:65], v[58:61], v[10:13]
	v_mfma_f32_16x16x32_f16 v[18:21], v[70:73], v[58:61], v[18:21]
	s_waitcnt lgkmcnt(0)
	v_mfma_f32_16x16x32_f16 v[26:29], v[82:85], v[38:41], v[26:29]
	v_mfma_f32_16x16x32_f16 v[14:17], v[86:89], v[38:41], v[14:17]
	ds_read_b128 v[38:41], v0 offset:32768
	ds_read_b128 v[50:53], v0 offset:34816
	ds_read_b128 v[54:57], v0 offset:36864
	ds_read_b128 v[58:61], v0 offset:38912
	ds_read_b128 v[62:65], v4 offset:49152
	ds_read_b128 v[70:73], v4 offset:51200
	v_mfma_f32_16x16x32_f16 v[66:69], v[82:85], v[46:49], v[66:69]
	v_mfma_f32_16x16x32_f16 v[22:25], v[86:89], v[46:49], v[22:25]
	v_mfma_f32_16x16x32_f16 v[42:45], v[82:85], v[74:77], v[42:45]
	v_mfma_f32_16x16x32_f16 v[34:37], v[86:89], v[74:77], v[34:37]
	v_mfma_f32_16x16x32_f16 v[10:13], v[82:85], v[78:81], v[10:13]
	v_mfma_f32_16x16x32_f16 v[18:21], v[86:89], v[78:81], v[18:21]
	s_add_u32 s20, s0, 0x380
	s_mov_b32 m0, s14
	s_waitcnt vmcnt(0) lgkmcnt(0)
	s_barrier
	s_addc_u32 s21, s1, 0
	s_add_u32 s22, s4, 0x380
	global_load_lds_dwordx4 v1, s[20:21]
	s_mov_b32 m0, s3
	s_addc_u32 s23, s5, 0
	global_load_lds_dwordx4 v2, s[20:21]
	s_mov_b32 m0, s6
	s_nop 0
	global_load_lds_dwordx4 v1, s[22:23]
	s_mov_b32 m0, s7
	s_nop 0
	global_load_lds_dwordx4 v2, s[22:23]
	s_waitcnt lgkmcnt(0)
	v_mfma_f32_16x16x32_f16 v[26:29], v[62:65], v[38:41], v[26:29]
	v_mfma_f32_16x16x32_f16 v[14:17], v[70:73], v[38:41], v[14:17]
	ds_read_b128 v[38:41], v5
	ds_read_b128 v[46:49], v5 offset:2048
	ds_read_b128 v[74:77], v5 offset:4096
	ds_read_b128 v[78:81], v5 offset:6144
	ds_read_b128 v[82:85], v3 offset:16384
	ds_read_b128 v[86:89], v3 offset:18432
	v_mfma_f32_16x16x32_f16 v[66:69], v[62:65], v[50:53], v[66:69]
	v_mfma_f32_16x16x32_f16 v[22:25], v[70:73], v[50:53], v[22:25]
	v_mfma_f32_16x16x32_f16 v[42:45], v[62:65], v[54:57], v[42:45]
	v_mfma_f32_16x16x32_f16 v[34:37], v[70:73], v[54:57], v[34:37]
	v_mfma_f32_16x16x32_f16 v[10:13], v[62:65], v[58:61], v[10:13]
	v_mfma_f32_16x16x32_f16 v[18:21], v[70:73], v[58:61], v[18:21]
	s_waitcnt lgkmcnt(0)
	v_mfma_f32_16x16x32_f16 v[26:29], v[82:85], v[38:41], v[26:29]
	v_mfma_f32_16x16x32_f16 v[14:17], v[86:89], v[38:41], v[14:17]
	ds_read_b128 v[38:41], v0
	ds_read_b128 v[50:53], v0 offset:2048
	ds_read_b128 v[54:57], v0 offset:4096
	ds_read_b128 v[58:61], v0 offset:6144
	ds_read_b128 v[62:65], v4 offset:16384
	ds_read_b128 v[70:73], v4 offset:18432
	v_mfma_f32_16x16x32_f16 v[66:69], v[82:85], v[46:49], v[66:69]
	v_mfma_f32_16x16x32_f16 v[22:25], v[86:89], v[46:49], v[22:25]
	v_mfma_f32_16x16x32_f16 v[42:45], v[82:85], v[74:77], v[42:45]
	v_mfma_f32_16x16x32_f16 v[34:37], v[86:89], v[74:77], v[34:37]
	v_mfma_f32_16x16x32_f16 v[10:13], v[82:85], v[78:81], v[10:13]
	v_mfma_f32_16x16x32_f16 v[18:21], v[86:89], v[78:81], v[18:21]
	s_add_u32 s20, s0, 0x400
	s_mov_b32 m0, s18
	s_waitcnt vmcnt(0) lgkmcnt(0)
	s_barrier
	s_addc_u32 s21, s1, 0
	s_add_u32 s22, s4, 0x400
	global_load_lds_dwordx4 v1, s[20:21]
	s_mov_b32 m0, s15
	s_addc_u32 s23, s5, 0
	global_load_lds_dwordx4 v2, s[20:21]
	s_mov_b32 m0, s16
	s_nop 0
	global_load_lds_dwordx4 v1, s[22:23]
	s_mov_b32 m0, s17
	s_nop 0
	global_load_lds_dwordx4 v2, s[22:23]
	s_waitcnt lgkmcnt(0)
	v_mfma_f32_16x16x32_f16 v[26:29], v[62:65], v[38:41], v[26:29]
	v_mfma_f32_16x16x32_f16 v[14:17], v[70:73], v[38:41], v[14:17]
	ds_read_b128 v[38:41], v5 offset:32768
	ds_read_b128 v[46:49], v5 offset:34816
	ds_read_b128 v[74:77], v5 offset:36864
	ds_read_b128 v[78:81], v5 offset:38912
	ds_read_b128 v[82:85], v3 offset:49152
	ds_read_b128 v[86:89], v3 offset:51200
	v_mfma_f32_16x16x32_f16 v[66:69], v[62:65], v[50:53], v[66:69]
	v_mfma_f32_16x16x32_f16 v[22:25], v[70:73], v[50:53], v[22:25]
	v_mfma_f32_16x16x32_f16 v[42:45], v[62:65], v[54:57], v[42:45]
	v_mfma_f32_16x16x32_f16 v[34:37], v[70:73], v[54:57], v[34:37]
	v_mfma_f32_16x16x32_f16 v[10:13], v[62:65], v[58:61], v[10:13]
	v_mfma_f32_16x16x32_f16 v[18:21], v[70:73], v[58:61], v[18:21]
	s_waitcnt lgkmcnt(0)
	v_mfma_f32_16x16x32_f16 v[26:29], v[82:85], v[38:41], v[26:29]
	v_mfma_f32_16x16x32_f16 v[14:17], v[86:89], v[38:41], v[14:17]
	ds_read_b128 v[38:41], v0 offset:32768
	ds_read_b128 v[50:53], v0 offset:34816
	ds_read_b128 v[54:57], v0 offset:36864
	ds_read_b128 v[58:61], v0 offset:38912
	ds_read_b128 v[62:65], v4 offset:49152
	ds_read_b128 v[70:73], v4 offset:51200
	v_mfma_f32_16x16x32_f16 v[66:69], v[82:85], v[46:49], v[66:69]
	v_mfma_f32_16x16x32_f16 v[22:25], v[86:89], v[46:49], v[22:25]
	v_mfma_f32_16x16x32_f16 v[42:45], v[82:85], v[74:77], v[42:45]
	v_mfma_f32_16x16x32_f16 v[34:37], v[86:89], v[74:77], v[34:37]
	v_mfma_f32_16x16x32_f16 v[10:13], v[82:85], v[78:81], v[10:13]
	v_mfma_f32_16x16x32_f16 v[18:21], v[86:89], v[78:81], v[18:21]
	s_add_u32 s20, s0, 0x480
	s_mov_b32 m0, s14
	s_waitcnt vmcnt(0) lgkmcnt(0)
	s_barrier
	s_addc_u32 s21, s1, 0
	s_add_u32 s22, s4, 0x480
	global_load_lds_dwordx4 v1, s[20:21]
	s_mov_b32 m0, s3
	s_addc_u32 s23, s5, 0
	global_load_lds_dwordx4 v2, s[20:21]
	s_mov_b32 m0, s6
	s_nop 0
	global_load_lds_dwordx4 v1, s[22:23]
	s_mov_b32 m0, s7
	s_nop 0
	global_load_lds_dwordx4 v2, s[22:23]
	s_waitcnt lgkmcnt(0)
	v_mfma_f32_16x16x32_f16 v[26:29], v[62:65], v[38:41], v[26:29]
	v_mfma_f32_16x16x32_f16 v[14:17], v[70:73], v[38:41], v[14:17]
	ds_read_b128 v[38:41], v5
	ds_read_b128 v[46:49], v5 offset:2048
	ds_read_b128 v[74:77], v5 offset:4096
	ds_read_b128 v[78:81], v5 offset:6144
	ds_read_b128 v[82:85], v3 offset:16384
	ds_read_b128 v[86:89], v3 offset:18432
	v_mfma_f32_16x16x32_f16 v[66:69], v[62:65], v[50:53], v[66:69]
	v_mfma_f32_16x16x32_f16 v[22:25], v[70:73], v[50:53], v[22:25]
	v_mfma_f32_16x16x32_f16 v[42:45], v[62:65], v[54:57], v[42:45]
	v_mfma_f32_16x16x32_f16 v[34:37], v[70:73], v[54:57], v[34:37]
	v_mfma_f32_16x16x32_f16 v[10:13], v[62:65], v[58:61], v[10:13]
	v_mfma_f32_16x16x32_f16 v[18:21], v[70:73], v[58:61], v[18:21]
	s_waitcnt lgkmcnt(0)
	v_mfma_f32_16x16x32_f16 v[26:29], v[82:85], v[38:41], v[26:29]
	v_mfma_f32_16x16x32_f16 v[14:17], v[86:89], v[38:41], v[14:17]
	ds_read_b128 v[38:41], v0
	ds_read_b128 v[50:53], v0 offset:2048
	ds_read_b128 v[54:57], v0 offset:4096
	ds_read_b128 v[58:61], v0 offset:6144
	ds_read_b128 v[62:65], v4 offset:16384
	ds_read_b128 v[70:73], v4 offset:18432
	v_mfma_f32_16x16x32_f16 v[66:69], v[82:85], v[46:49], v[66:69]
	v_mfma_f32_16x16x32_f16 v[22:25], v[86:89], v[46:49], v[22:25]
	v_mfma_f32_16x16x32_f16 v[42:45], v[82:85], v[74:77], v[42:45]
	v_mfma_f32_16x16x32_f16 v[34:37], v[86:89], v[74:77], v[34:37]
	v_mfma_f32_16x16x32_f16 v[10:13], v[82:85], v[78:81], v[10:13]
	v_mfma_f32_16x16x32_f16 v[18:21], v[86:89], v[78:81], v[18:21]
	s_add_u32 s20, s0, 0x500
	s_mov_b32 m0, s18
	s_waitcnt vmcnt(0) lgkmcnt(0)
	s_barrier
	s_addc_u32 s21, s1, 0
	s_add_u32 s22, s4, 0x500
	global_load_lds_dwordx4 v1, s[20:21]
	s_mov_b32 m0, s15
	s_addc_u32 s23, s5, 0
	global_load_lds_dwordx4 v2, s[20:21]
	s_mov_b32 m0, s16
	s_nop 0
	global_load_lds_dwordx4 v1, s[22:23]
	s_mov_b32 m0, s17
	s_nop 0
	global_load_lds_dwordx4 v2, s[22:23]
	s_waitcnt lgkmcnt(0)
	v_mfma_f32_16x16x32_f16 v[26:29], v[62:65], v[38:41], v[26:29]
	v_mfma_f32_16x16x32_f16 v[14:17], v[70:73], v[38:41], v[14:17]
	ds_read_b128 v[38:41], v5 offset:32768
	ds_read_b128 v[46:49], v5 offset:34816
	ds_read_b128 v[74:77], v5 offset:36864
	ds_read_b128 v[78:81], v5 offset:38912
	ds_read_b128 v[82:85], v3 offset:49152
	ds_read_b128 v[86:89], v3 offset:51200
	v_mfma_f32_16x16x32_f16 v[66:69], v[62:65], v[50:53], v[66:69]
	v_mfma_f32_16x16x32_f16 v[22:25], v[70:73], v[50:53], v[22:25]
	v_mfma_f32_16x16x32_f16 v[42:45], v[62:65], v[54:57], v[42:45]
	v_mfma_f32_16x16x32_f16 v[34:37], v[70:73], v[54:57], v[34:37]
	v_mfma_f32_16x16x32_f16 v[10:13], v[62:65], v[58:61], v[10:13]
	v_mfma_f32_16x16x32_f16 v[18:21], v[70:73], v[58:61], v[18:21]
	s_waitcnt lgkmcnt(0)
	v_mfma_f32_16x16x32_f16 v[26:29], v[82:85], v[38:41], v[26:29]
	v_mfma_f32_16x16x32_f16 v[14:17], v[86:89], v[38:41], v[14:17]
	ds_read_b128 v[38:41], v0 offset:32768
	ds_read_b128 v[50:53], v0 offset:34816
	ds_read_b128 v[54:57], v0 offset:36864
	ds_read_b128 v[58:61], v0 offset:38912
	ds_read_b128 v[62:65], v4 offset:49152
	ds_read_b128 v[70:73], v4 offset:51200
	v_mfma_f32_16x16x32_f16 v[66:69], v[82:85], v[46:49], v[66:69]
	v_mfma_f32_16x16x32_f16 v[22:25], v[86:89], v[46:49], v[22:25]
	v_mfma_f32_16x16x32_f16 v[42:45], v[82:85], v[74:77], v[42:45]
	v_mfma_f32_16x16x32_f16 v[34:37], v[86:89], v[74:77], v[34:37]
	v_mfma_f32_16x16x32_f16 v[10:13], v[82:85], v[78:81], v[10:13]
	v_mfma_f32_16x16x32_f16 v[18:21], v[86:89], v[78:81], v[18:21]
	s_add_u32 s20, s0, 0x580
	s_mov_b32 m0, s14
	s_waitcnt vmcnt(0) lgkmcnt(0)
	s_barrier
	s_addc_u32 s21, s1, 0
	s_add_u32 s22, s4, 0x580
	global_load_lds_dwordx4 v1, s[20:21]
	s_mov_b32 m0, s3
	s_addc_u32 s23, s5, 0
	global_load_lds_dwordx4 v2, s[20:21]
	s_mov_b32 m0, s6
	s_nop 0
	global_load_lds_dwordx4 v1, s[22:23]
	s_mov_b32 m0, s7
	s_nop 0
	global_load_lds_dwordx4 v2, s[22:23]
	s_waitcnt lgkmcnt(0)
	v_mfma_f32_16x16x32_f16 v[26:29], v[62:65], v[38:41], v[26:29]
	v_mfma_f32_16x16x32_f16 v[14:17], v[70:73], v[38:41], v[14:17]
	ds_read_b128 v[38:41], v5
	ds_read_b128 v[46:49], v5 offset:2048
	ds_read_b128 v[74:77], v5 offset:4096
	ds_read_b128 v[78:81], v5 offset:6144
	ds_read_b128 v[82:85], v3 offset:16384
	ds_read_b128 v[86:89], v3 offset:18432
	v_mfma_f32_16x16x32_f16 v[66:69], v[62:65], v[50:53], v[66:69]
	v_mfma_f32_16x16x32_f16 v[22:25], v[70:73], v[50:53], v[22:25]
	v_mfma_f32_16x16x32_f16 v[42:45], v[62:65], v[54:57], v[42:45]
	v_mfma_f32_16x16x32_f16 v[34:37], v[70:73], v[54:57], v[34:37]
	v_mfma_f32_16x16x32_f16 v[10:13], v[62:65], v[58:61], v[10:13]
	v_mfma_f32_16x16x32_f16 v[18:21], v[70:73], v[58:61], v[18:21]
	s_waitcnt lgkmcnt(0)
	v_mfma_f32_16x16x32_f16 v[26:29], v[82:85], v[38:41], v[26:29]
	v_mfma_f32_16x16x32_f16 v[14:17], v[86:89], v[38:41], v[14:17]
	ds_read_b128 v[38:41], v0
	ds_read_b128 v[50:53], v0 offset:2048
	ds_read_b128 v[54:57], v0 offset:4096
	ds_read_b128 v[58:61], v0 offset:6144
	ds_read_b128 v[62:65], v4 offset:16384
	ds_read_b128 v[70:73], v4 offset:18432
	v_mfma_f32_16x16x32_f16 v[66:69], v[82:85], v[46:49], v[66:69]
	v_mfma_f32_16x16x32_f16 v[22:25], v[86:89], v[46:49], v[22:25]
	v_mfma_f32_16x16x32_f16 v[42:45], v[82:85], v[74:77], v[42:45]
	v_mfma_f32_16x16x32_f16 v[34:37], v[86:89], v[74:77], v[34:37]
	v_mfma_f32_16x16x32_f16 v[10:13], v[82:85], v[78:81], v[10:13]
	v_mfma_f32_16x16x32_f16 v[18:21], v[86:89], v[78:81], v[18:21]
	s_add_u32 s20, s0, 0x600
	s_mov_b32 m0, s18
	s_waitcnt vmcnt(0) lgkmcnt(0)
	s_barrier
	s_addc_u32 s21, s1, 0
	s_add_u32 s22, s4, 0x600
	global_load_lds_dwordx4 v1, s[20:21]
	s_mov_b32 m0, s15
	s_addc_u32 s23, s5, 0
	global_load_lds_dwordx4 v2, s[20:21]
	s_mov_b32 m0, s16
	s_nop 0
	global_load_lds_dwordx4 v1, s[22:23]
	s_mov_b32 m0, s17
	s_nop 0
	global_load_lds_dwordx4 v2, s[22:23]
	s_waitcnt lgkmcnt(0)
	v_mfma_f32_16x16x32_f16 v[26:29], v[62:65], v[38:41], v[26:29]
	v_mfma_f32_16x16x32_f16 v[14:17], v[70:73], v[38:41], v[14:17]
	ds_read_b128 v[38:41], v5 offset:32768
	ds_read_b128 v[46:49], v5 offset:34816
	ds_read_b128 v[74:77], v5 offset:36864
	ds_read_b128 v[78:81], v5 offset:38912
	ds_read_b128 v[82:85], v3 offset:49152
	ds_read_b128 v[86:89], v3 offset:51200
	v_mfma_f32_16x16x32_f16 v[66:69], v[62:65], v[50:53], v[66:69]
	v_mfma_f32_16x16x32_f16 v[22:25], v[70:73], v[50:53], v[22:25]
	v_mfma_f32_16x16x32_f16 v[42:45], v[62:65], v[54:57], v[42:45]
	v_mfma_f32_16x16x32_f16 v[34:37], v[70:73], v[54:57], v[34:37]
	v_mfma_f32_16x16x32_f16 v[10:13], v[62:65], v[58:61], v[10:13]
	v_mfma_f32_16x16x32_f16 v[18:21], v[70:73], v[58:61], v[18:21]
	s_waitcnt lgkmcnt(0)
	v_mfma_f32_16x16x32_f16 v[26:29], v[82:85], v[38:41], v[26:29]
	v_mfma_f32_16x16x32_f16 v[14:17], v[86:89], v[38:41], v[14:17]
	ds_read_b128 v[38:41], v0 offset:32768
	ds_read_b128 v[50:53], v0 offset:34816
	ds_read_b128 v[54:57], v0 offset:36864
	ds_read_b128 v[58:61], v0 offset:38912
	ds_read_b128 v[62:65], v4 offset:49152
	ds_read_b128 v[70:73], v4 offset:51200
	v_mfma_f32_16x16x32_f16 v[66:69], v[82:85], v[46:49], v[66:69]
	v_mfma_f32_16x16x32_f16 v[22:25], v[86:89], v[46:49], v[22:25]
	v_mfma_f32_16x16x32_f16 v[42:45], v[82:85], v[74:77], v[42:45]
	v_mfma_f32_16x16x32_f16 v[34:37], v[86:89], v[74:77], v[34:37]
	v_mfma_f32_16x16x32_f16 v[10:13], v[82:85], v[78:81], v[10:13]
	v_mfma_f32_16x16x32_f16 v[18:21], v[86:89], v[78:81], v[18:21]
	s_add_u32 s20, s0, 0x680
	s_mov_b32 m0, s14
	s_waitcnt vmcnt(0) lgkmcnt(0)
	s_barrier
	s_addc_u32 s21, s1, 0
	s_add_u32 s22, s4, 0x680
	global_load_lds_dwordx4 v1, s[20:21]
	s_mov_b32 m0, s3
	s_addc_u32 s23, s5, 0
	global_load_lds_dwordx4 v2, s[20:21]
	s_mov_b32 m0, s6
	s_nop 0
	global_load_lds_dwordx4 v1, s[22:23]
	s_mov_b32 m0, s7
	s_nop 0
	global_load_lds_dwordx4 v2, s[22:23]
	s_waitcnt lgkmcnt(0)
	v_mfma_f32_16x16x32_f16 v[26:29], v[62:65], v[38:41], v[26:29]
	v_mfma_f32_16x16x32_f16 v[14:17], v[70:73], v[38:41], v[14:17]
	ds_read_b128 v[38:41], v5
	ds_read_b128 v[46:49], v5 offset:2048
	ds_read_b128 v[74:77], v5 offset:4096
	ds_read_b128 v[78:81], v5 offset:6144
	ds_read_b128 v[82:85], v3 offset:16384
	ds_read_b128 v[86:89], v3 offset:18432
	v_mfma_f32_16x16x32_f16 v[66:69], v[62:65], v[50:53], v[66:69]
	v_mfma_f32_16x16x32_f16 v[22:25], v[70:73], v[50:53], v[22:25]
	v_mfma_f32_16x16x32_f16 v[42:45], v[62:65], v[54:57], v[42:45]
	v_mfma_f32_16x16x32_f16 v[34:37], v[70:73], v[54:57], v[34:37]
	v_mfma_f32_16x16x32_f16 v[10:13], v[62:65], v[58:61], v[10:13]
	v_mfma_f32_16x16x32_f16 v[18:21], v[70:73], v[58:61], v[18:21]
	s_waitcnt lgkmcnt(0)
	v_mfma_f32_16x16x32_f16 v[26:29], v[82:85], v[38:41], v[26:29]
	v_mfma_f32_16x16x32_f16 v[14:17], v[86:89], v[38:41], v[14:17]
	ds_read_b128 v[38:41], v0
	ds_read_b128 v[50:53], v0 offset:2048
	ds_read_b128 v[54:57], v0 offset:4096
	ds_read_b128 v[58:61], v0 offset:6144
	ds_read_b128 v[62:65], v4 offset:16384
	ds_read_b128 v[70:73], v4 offset:18432
	v_mfma_f32_16x16x32_f16 v[66:69], v[82:85], v[46:49], v[66:69]
	v_mfma_f32_16x16x32_f16 v[22:25], v[86:89], v[46:49], v[22:25]
	v_mfma_f32_16x16x32_f16 v[42:45], v[82:85], v[74:77], v[42:45]
	v_mfma_f32_16x16x32_f16 v[34:37], v[86:89], v[74:77], v[34:37]
	v_mfma_f32_16x16x32_f16 v[10:13], v[82:85], v[78:81], v[10:13]
	v_mfma_f32_16x16x32_f16 v[18:21], v[86:89], v[78:81], v[18:21]
	s_mov_b32 m0, s18
	s_add_u32 s18, s0, 0x700
	s_waitcnt vmcnt(0) lgkmcnt(0)
	s_barrier
	s_addc_u32 s19, s1, 0
	s_add_u32 s20, s4, 0x700
	global_load_lds_dwordx4 v1, s[18:19]
	s_mov_b32 m0, s15
	s_addc_u32 s21, s5, 0
	global_load_lds_dwordx4 v2, s[18:19]
	s_mov_b32 m0, s16
	s_nop 0
	global_load_lds_dwordx4 v1, s[20:21]
	s_mov_b32 m0, s17
	s_nop 0
	global_load_lds_dwordx4 v2, s[20:21]
	s_waitcnt lgkmcnt(0)
	v_mfma_f32_16x16x32_f16 v[26:29], v[62:65], v[38:41], v[26:29]
	v_mfma_f32_16x16x32_f16 v[14:17], v[70:73], v[38:41], v[14:17]
	ds_read_b128 v[38:41], v5 offset:32768
	ds_read_b128 v[46:49], v5 offset:34816
	ds_read_b128 v[74:77], v5 offset:36864
	ds_read_b128 v[78:81], v5 offset:38912
	ds_read_b128 v[82:85], v3 offset:49152
	ds_read_b128 v[86:89], v3 offset:51200
	v_mfma_f32_16x16x32_f16 v[66:69], v[62:65], v[50:53], v[66:69]
	v_mfma_f32_16x16x32_f16 v[22:25], v[70:73], v[50:53], v[22:25]
	v_mfma_f32_16x16x32_f16 v[42:45], v[62:65], v[54:57], v[42:45]
	v_mfma_f32_16x16x32_f16 v[34:37], v[70:73], v[54:57], v[34:37]
	v_mfma_f32_16x16x32_f16 v[10:13], v[62:65], v[58:61], v[10:13]
	v_mfma_f32_16x16x32_f16 v[18:21], v[70:73], v[58:61], v[18:21]
	s_waitcnt lgkmcnt(0)
	v_mfma_f32_16x16x32_f16 v[26:29], v[82:85], v[38:41], v[26:29]
	v_mfma_f32_16x16x32_f16 v[14:17], v[86:89], v[38:41], v[14:17]
	ds_read_b128 v[38:41], v0 offset:32768
	ds_read_b128 v[50:53], v0 offset:34816
	ds_read_b128 v[54:57], v0 offset:36864
	ds_read_b128 v[58:61], v0 offset:38912
	ds_read_b128 v[62:65], v4 offset:49152
	ds_read_b128 v[70:73], v4 offset:51200
	v_mfma_f32_16x16x32_f16 v[66:69], v[82:85], v[46:49], v[66:69]
	v_mfma_f32_16x16x32_f16 v[22:25], v[86:89], v[46:49], v[22:25]
	v_mfma_f32_16x16x32_f16 v[42:45], v[82:85], v[74:77], v[42:45]
	v_mfma_f32_16x16x32_f16 v[34:37], v[86:89], v[74:77], v[34:37]
	v_mfma_f32_16x16x32_f16 v[10:13], v[82:85], v[78:81], v[10:13]
	v_mfma_f32_16x16x32_f16 v[18:21], v[86:89], v[78:81], v[18:21]
	s_add_u32 s0, s0, 0x780
	s_mov_b32 m0, s14
	s_waitcnt vmcnt(0) lgkmcnt(0)
	s_barrier
	s_addc_u32 s1, s1, 0
	s_add_u32 s4, s4, 0x780
	global_load_lds_dwordx4 v1, s[0:1]
	s_mov_b32 m0, s3
	s_addc_u32 s5, s5, 0
	global_load_lds_dwordx4 v2, s[0:1]
	s_mov_b32 m0, s6
	s_nop 0
	global_load_lds_dwordx4 v1, s[4:5]
	s_mov_b32 m0, s7
	s_nop 0
	global_load_lds_dwordx4 v2, s[4:5]
	s_waitcnt lgkmcnt(0)
	v_mfma_f32_16x16x32_f16 v[26:29], v[62:65], v[38:41], v[26:29]
	v_mfma_f32_16x16x32_f16 v[14:17], v[70:73], v[38:41], v[14:17]
	ds_read_b128 v[38:41], v5
	ds_read_b128 v[46:49], v5 offset:2048
	ds_read_b128 v[74:77], v5 offset:4096
	ds_read_b128 v[78:81], v5 offset:6144
	ds_read_b128 v[82:85], v3 offset:16384
	ds_read_b128 v[86:89], v3 offset:18432
	v_mfma_f32_16x16x32_f16 v[66:69], v[62:65], v[50:53], v[66:69]
	v_mfma_f32_16x16x32_f16 v[22:25], v[70:73], v[50:53], v[22:25]
	v_mfma_f32_16x16x32_f16 v[42:45], v[62:65], v[54:57], v[42:45]
	v_mfma_f32_16x16x32_f16 v[34:37], v[70:73], v[54:57], v[34:37]
	v_mfma_f32_16x16x32_f16 v[10:13], v[62:65], v[58:61], v[10:13]
	v_mfma_f32_16x16x32_f16 v[18:21], v[70:73], v[58:61], v[18:21]
	s_waitcnt lgkmcnt(0)
	v_mfma_f32_16x16x32_f16 v[26:29], v[82:85], v[38:41], v[26:29]
	v_mfma_f32_16x16x32_f16 v[14:17], v[86:89], v[38:41], v[14:17]
	ds_read_b128 v[38:41], v0
	ds_read_b128 v[50:53], v0 offset:2048
	ds_read_b128 v[54:57], v0 offset:4096
	ds_read_b128 v[58:61], v0 offset:6144
	ds_read_b128 v[62:65], v4 offset:16384
	ds_read_b128 v[70:73], v4 offset:18432
	v_mfma_f32_16x16x32_f16 v[66:69], v[82:85], v[46:49], v[66:69]
	v_mfma_f32_16x16x32_f16 v[22:25], v[86:89], v[46:49], v[22:25]
	v_mfma_f32_16x16x32_f16 v[42:45], v[82:85], v[74:77], v[42:45]
	v_mfma_f32_16x16x32_f16 v[34:37], v[86:89], v[74:77], v[34:37]
	v_mfma_f32_16x16x32_f16 v[10:13], v[82:85], v[78:81], v[10:13]
	v_mfma_f32_16x16x32_f16 v[18:21], v[86:89], v[78:81], v[18:21]
	s_waitcnt vmcnt(0) lgkmcnt(0)
	s_barrier
	s_waitcnt lgkmcnt(0)
	v_mfma_f32_16x16x32_f16 v[26:29], v[62:65], v[38:41], v[26:29]
	v_mfma_f32_16x16x32_f16 v[14:17], v[70:73], v[38:41], v[14:17]
	ds_read_b128 v[38:41], v5 offset:32768
	ds_read_b128 v[46:49], v5 offset:34816
	ds_read_b128 v[74:77], v5 offset:36864
	ds_read_b128 v[78:81], v5 offset:38912
	ds_read_b128 v[82:85], v3 offset:49152
	ds_read_b128 v[86:89], v3 offset:51200
	v_mfma_f32_16x16x32_f16 v[66:69], v[62:65], v[50:53], v[66:69]
	v_mfma_f32_16x16x32_f16 v[22:25], v[70:73], v[50:53], v[22:25]
	v_mfma_f32_16x16x32_f16 v[42:45], v[62:65], v[54:57], v[42:45]
	v_mfma_f32_16x16x32_f16 v[34:37], v[70:73], v[54:57], v[34:37]
	v_mfma_f32_16x16x32_f16 v[10:13], v[62:65], v[58:61], v[10:13]
	v_mfma_f32_16x16x32_f16 v[18:21], v[70:73], v[58:61], v[18:21]
	s_waitcnt lgkmcnt(0)
	v_mfma_f32_16x16x32_f16 v[26:29], v[82:85], v[38:41], v[26:29]
	v_mfma_f32_16x16x32_f16 v[14:17], v[86:89], v[38:41], v[14:17]
	ds_read_b128 v[38:41], v0 offset:32768
	ds_read_b128 v[50:53], v0 offset:34816
	ds_read_b128 v[54:57], v0 offset:36864
	ds_read_b128 v[0:3], v0 offset:38912
	ds_read_b128 v[58:61], v4 offset:49152
	ds_read_b128 v[62:65], v4 offset:51200
	v_mfma_f32_16x16x32_f16 v[4:7], v[82:85], v[46:49], v[66:69]
	v_mfma_f32_16x16x32_f16 v[22:25], v[86:89], v[46:49], v[22:25]
	v_mfma_f32_16x16x32_f16 v[42:45], v[82:85], v[74:77], v[42:45]
	v_mfma_f32_16x16x32_f16 v[34:37], v[86:89], v[74:77], v[34:37]
	v_mfma_f32_16x16x32_f16 v[10:13], v[82:85], v[78:81], v[10:13]
	v_mfma_f32_16x16x32_f16 v[46:49], v[86:89], v[78:81], v[18:21]
	s_waitcnt lgkmcnt(0)
	v_mfma_f32_16x16x32_f16 v[66:69], v[58:61], v[38:41], v[26:29]
	v_mfma_f32_16x16x32_f16 v[38:41], v[62:65], v[38:41], v[14:17]
	v_mfma_f32_16x16x32_f16 v[28:31], v[58:61], v[50:53], v[4:7]
	v_mfma_f32_16x16x32_f16 v[24:27], v[62:65], v[50:53], v[22:25]
	v_mfma_f32_16x16x32_f16 v[20:23], v[58:61], v[54:57], v[42:45]
	v_mfma_f32_16x16x32_f16 v[16:19], v[62:65], v[54:57], v[34:37]
	v_mfma_f32_16x16x32_f16 v[4:7], v[58:61], v[0:3], v[10:13]
	v_mfma_f32_16x16x32_f16 v[0:3], v[62:65], v[0:3], v[46:49]
	v_lshlrev_b32_e32 v9, 2, v9
	v_or3_b32 v34, v9, v8, s13
	v_mov_b32_e32 v35, 0
	v_lshl_add_u64 v[36:37], v[34:35], 2, s[10:11]
	global_load_dwordx4 v[8:11], v[36:37], off
	global_load_dwordx4 v[12:15], v[36:37], off offset:64
	v_or_b32_e32 v36, s12, v32
	v_mad_u64_u32 v[42:43], s[18:19], v36, s2, 0
	s_ashr_i32 s1, s2, 31
	s_mov_b32 s16, 0xbf3a00e3
	v_mov_b32_e32 v44, v43
	v_mov_b64_e32 v[32:33], s[16:17]
	v_mad_u64_u32 v[44:45], s[16:17], v36, s1, v[44:45]
	s_mov_b32 s14, 0x3e6d3388
	v_mov_b32_e32 v43, v44
	s_mov_b32 s10, 0x3f07dc22
	s_mov_b32 s6, 0xbf38aa3b
	s_mov_b32 s12, 0x3f35f0e3
	s_mov_b32 s0, 0xbe11a98e
	s_mov_b32 s4, 0x3e027906
	v_lshlrev_b64 v[34:35], 1, v[34:35]
	v_lshl_add_u64 v[42:43], v[42:43], 1, s[8:9]
	v_lshl_add_u64 v[42:43], v[42:43], 0, v[34:35]
	s_waitcnt vmcnt(0)
	v_pk_add_f32 v[46:47], v[66:67], v[8:9]
	v_pk_add_f32 v[44:45], v[68:69], v[10:11]
	v_and_b32_e32 v49, 0x7fffffff, v47
	v_and_b32_e32 v48, 0x7fffffff, v46
	v_and_b32_e32 v55, 0x7fffffff, v45
	v_and_b32_e32 v54, 0x7fffffff, v44
	v_pk_fma_f32 v[48:49], v[48:49], s[14:15], 1.0 op_sel_hi:[1,0,0]
	v_pk_add_f32 v[38:39], v[38:39], v[12:13]
	v_pk_fma_f32 v[54:55], v[54:55], s[14:15], 1.0 op_sel_hi:[1,0,0]
	v_rcp_f32_e32 v48, v48
	v_rcp_f32_e32 v49, v49
	v_and_b32_e32 v57, 0x7fffffff, v39
	v_and_b32_e32 v56, 0x7fffffff, v38
	v_rcp_f32_e32 v54, v54
	v_rcp_f32_e32 v55, v55
	v_pk_fma_f32 v[56:57], v[56:57], s[14:15], 1.0 op_sel_hi:[1,0,0]
	v_pk_mul_f32 v[52:53], v[46:47], v[46:47]
	v_rcp_f32_e32 v56, v56
	v_rcp_f32_e32 v57, v57
	v_pk_mul_f32 v[50:51], v[44:45], v[44:45]
	v_pk_mul_f32 v[52:53], v[52:53], s[6:7] op_sel_hi:[1,0]
	v_pk_fma_f32 v[64:65], v[48:49], s[10:11], v[32:33] op_sel_hi:[1,0,0]
	v_pk_mul_f32 v[50:51], v[50:51], s[6:7] op_sel_hi:[1,0]
	v_exp_f32_e32 v52, v52
	v_exp_f32_e32 v53, v53
	v_pk_fma_f32 v[66:67], v[54:55], s[10:11], v[32:33] op_sel_hi:[1,0,0]
	v_pk_fma_f32 v[64:65], v[48:49], v[64:65], s[12:13] op_sel_hi:[1,1,0]
	v_pk_mul_f32 v[60:61], v[38:39], v[38:39]
	v_exp_f32_e32 v50, v50
	v_exp_f32_e32 v51, v51
	v_pk_fma_f32 v[66:67], v[54:55], v[66:67], s[12:13] op_sel_hi:[1,1,0]
	v_pk_fma_f32 v[64:65], v[48:49], v[64:65], s[0:1] op_sel_hi:[1,1,0]
	v_pk_mul_f32 v[60:61], v[60:61], s[6:7] op_sel_hi:[1,0]
	v_pk_fma_f32 v[68:69], v[56:57], s[10:11], v[32:33] op_sel_hi:[1,0,0]
	v_pk_fma_f32 v[66:67], v[54:55], v[66:67], s[0:1] op_sel_hi:[1,1,0]
	v_pk_fma_f32 v[64:65], v[48:49], v[64:65], s[4:5] op_sel_hi:[1,1,0]
	v_exp_f32_e32 v60, v60
	v_exp_f32_e32 v61, v61
	v_pk_fma_f32 v[68:69], v[56:57], v[68:69], s[12:13] op_sel_hi:[1,1,0]
	v_pk_fma_f32 v[66:67], v[54:55], v[66:67], s[4:5] op_sel_hi:[1,1,0]
	v_pk_mul_f32 v[48:49], v[48:49], v[64:65]
	v_pk_add_f32 v[40:41], v[40:41], v[14:15]
	v_pk_fma_f32 v[68:69], v[56:57], v[68:69], s[0:1] op_sel_hi:[1,1,0]
	v_pk_mul_f32 v[54:55], v[54:55], v[66:67]
	v_pk_mul_f32 v[48:49], v[52:53], v[48:49]
	v_and_b32_e32 v63, 0x7fffffff, v41
	v_and_b32_e32 v62, 0x7fffffff, v40
	v_pk_fma_f32 v[68:69], v[56:57], v[68:69], s[4:5] op_sel_hi:[1,1,0]
	v_pk_mul_f32 v[50:51], v[50:51], v[54:55]
	v_pk_mul_f32 v[54:55], v[46:47], v[48:49]
	v_pk_fma_f32 v[48:49], v[46:47], v[48:49], v[46:47] neg_lo:[1,0,0] neg_hi:[1,0,0]
	v_cmp_gt_f32_e32 vcc, 0, v46
	v_pk_fma_f32 v[62:63], v[62:63], s[14:15], 1.0 op_sel_hi:[1,0,0]
	v_pk_mul_f32 v[56:57], v[56:57], v[68:69]
	v_cndmask_b32_e32 v37, v48, v54, vcc
	v_cmp_gt_f32_e32 vcc, 0, v47
	v_rcp_f32_e32 v62, v62
	v_rcp_f32_e32 v63, v63
	v_pk_mul_f32 v[52:53], v[60:61], v[56:57]
	v_pk_mul_f32 v[56:57], v[44:45], v[50:51]
	v_pk_fma_f32 v[50:51], v[44:45], v[50:51], v[44:45] neg_lo:[1,0,0] neg_hi:[1,0,0]
	v_cndmask_b32_e32 v46, v49, v55, vcc
	v_cmp_gt_f32_e32 vcc, 0, v44
	v_pk_mul_f32 v[58:59], v[40:41], v[40:41]
	v_pk_mul_f32 v[60:61], v[38:39], v[52:53]
	v_cndmask_b32_e32 v44, v50, v56, vcc
	v_cmp_gt_f32_e32 vcc, 0, v45
	v_pk_fma_f32 v[52:53], v[38:39], v[52:53], v[38:39] neg_lo:[1,0,0] neg_hi:[1,0,0]
	v_pk_add_f32 v[28:29], v[28:29], v[8:9]
	v_cndmask_b32_e32 v45, v51, v57, vcc
	v_cmp_gt_f32_e32 vcc, 0, v38
	v_cvt_pk_f16_f32 v45, v44, v45
	v_cvt_pk_f16_f32 v44, v37, v46
	v_cndmask_b32_e32 v47, v52, v60, vcc
	global_store_dwordx2 v[42:43], v[44:45], off
	v_cmp_gt_f32_e32 vcc, 0, v39
	v_pk_fma_f32 v[38:39], v[62:63], s[10:11], v[32:33] op_sel_hi:[1,0,0]
	v_pk_mul_f32 v[44:45], v[58:59], s[6:7] op_sel_hi:[1,0]
	v_pk_fma_f32 v[38:39], v[62:63], v[38:39], s[12:13] op_sel_hi:[1,1,0]
	v_exp_f32_e32 v44, v44
	v_exp_f32_e32 v45, v45
	v_pk_fma_f32 v[38:39], v[62:63], v[38:39], s[0:1] op_sel_hi:[1,1,0]
	v_cndmask_b32_e32 v37, v53, v61, vcc
	v_pk_fma_f32 v[38:39], v[62:63], v[38:39], s[4:5] op_sel_hi:[1,1,0]
	v_cmp_gt_f32_e32 vcc, 0, v40
	v_pk_mul_f32 v[38:39], v[62:63], v[38:39]
	v_pk_add_f32 v[30:31], v[30:31], v[10:11]
	v_pk_mul_f32 v[38:39], v[44:45], v[38:39]
	v_and_b32_e32 v46, 0x7fffffff, v30
	v_pk_mul_f32 v[44:45], v[40:41], v[38:39]
	v_pk_fma_f32 v[38:39], v[40:41], v[38:39], v[40:41] neg_lo:[1,0,0] neg_hi:[1,0,0]
	v_pk_add_f32 v[24:25], v[24:25], v[12:13]
	v_cndmask_b32_e32 v38, v38, v44, vcc
	v_cmp_gt_f32_e32 vcc, 0, v41
	v_pk_add_f32 v[26:27], v[26:27], v[14:15]
	v_pk_add_f32 v[20:21], v[20:21], v[8:9]
	v_cndmask_b32_e32 v39, v39, v45, vcc
	v_cvt_pk_f16_f32 v39, v38, v39
	v_cvt_pk_f16_f32 v38, v47, v37
	global_store_dwordx2 v[42:43], v[38:39], off offset:32
	v_and_b32_e32 v43, 0x7fffffff, v29
	v_and_b32_e32 v42, 0x7fffffff, v28
	v_pk_fma_f32 v[42:43], v[42:43], s[14:15], 1.0 op_sel_hi:[1,0,0]
	v_or_b32_e32 v37, 16, v36
	v_rcp_f32_e32 v42, v42
	v_rcp_f32_e32 v43, v43
	v_mad_u64_u32 v[38:39], s[16:17], v37, s2, 0
	v_mov_b32_e32 v40, v39
	v_mad_u64_u32 v[40:41], s[16:17], v37, s1, v[40:41]
	v_pk_mul_f32 v[44:45], v[28:29], v[28:29]
	v_mov_b32_e32 v39, v40
	v_pk_fma_f32 v[40:41], v[42:43], s[10:11], v[32:33] op_sel_hi:[1,0,0]
	v_pk_mul_f32 v[44:45], v[44:45], s[6:7] op_sel_hi:[1,0]
	v_pk_fma_f32 v[40:41], v[42:43], v[40:41], s[12:13] op_sel_hi:[1,1,0]
	v_exp_f32_e32 v44, v44
	v_exp_f32_e32 v45, v45
	v_pk_fma_f32 v[40:41], v[42:43], v[40:41], s[0:1] op_sel_hi:[1,1,0]
	v_and_b32_e32 v47, 0x7fffffff, v31
	v_pk_fma_f32 v[40:41], v[42:43], v[40:41], s[4:5] op_sel_hi:[1,1,0]
	v_pk_fma_f32 v[46:47], v[46:47], s[14:15], 1.0 op_sel_hi:[1,0,0]
	v_pk_mul_f32 v[40:41], v[42:43], v[40:41]
	v_rcp_f32_e32 v46, v46
	v_rcp_f32_e32 v47, v47
	v_pk_mul_f32 v[40:41], v[44:45], v[40:41]
	v_cmp_gt_f32_e32 vcc, 0, v28
	v_pk_mul_f32 v[44:45], v[28:29], v[40:41]
	v_pk_fma_f32 v[40:41], v[28:29], v[40:41], v[28:29] neg_lo:[1,0,0] neg_hi:[1,0,0]
	v_pk_mul_f32 v[42:43], v[30:31], v[30:31]
	v_cndmask_b32_e32 v37, v40, v44, vcc
	v_cmp_gt_f32_e32 vcc, 0, v29
	v_pk_fma_f32 v[28:29], v[46:47], s[10:11], v[32:33] op_sel_hi:[1,0,0]
	v_lshl_add_u64 v[38:39], v[38:39], 1, s[8:9]
	v_cndmask_b32_e32 v44, v41, v45, vcc
	v_pk_mul_f32 v[40:41], v[42:43], s[6:7] op_sel_hi:[1,0]
	v_pk_fma_f32 v[28:29], v[46:47], v[28:29], s[12:13] op_sel_hi:[1,1,0]
	v_exp_f32_e32 v40, v40
	v_exp_f32_e32 v41, v41
	v_pk_fma_f32 v[28:29], v[46:47], v[28:29], s[0:1] op_sel_hi:[1,1,0]
	v_cmp_gt_f32_e32 vcc, 0, v30
	v_pk_fma_f32 v[28:29], v[46:47], v[28:29], s[4:5] op_sel_hi:[1,1,0]
	v_lshl_add_u64 v[38:39], v[38:39], 0, v[34:35]
	v_pk_mul_f32 v[28:29], v[46:47], v[28:29]
	v_and_b32_e32 v43, 0x7fffffff, v27
	v_pk_mul_f32 v[28:29], v[40:41], v[28:29]
	v_and_b32_e32 v42, 0x7fffffff, v26
	v_pk_mul_f32 v[40:41], v[30:31], v[28:29]
	v_pk_fma_f32 v[28:29], v[30:31], v[28:29], v[30:31] neg_lo:[1,0,0] neg_hi:[1,0,0]
	v_and_b32_e32 v30, 0x7fffffff, v24
	v_cndmask_b32_e32 v28, v28, v40, vcc
	v_cmp_gt_f32_e32 vcc, 0, v31
	v_and_b32_e32 v31, 0x7fffffff, v25
	v_pk_fma_f32 v[30:31], v[30:31], s[14:15], 1.0 op_sel_hi:[1,0,0]
	v_cndmask_b32_e32 v29, v29, v41, vcc
	v_rcp_f32_e32 v30, v30
	v_rcp_f32_e32 v31, v31
	v_cvt_pk_f16_f32 v29, v28, v29
	v_cvt_pk_f16_f32 v28, v37, v44
	v_pk_mul_f32 v[40:41], v[24:25], v[24:25]
	global_store_dwordx2 v[38:39], v[28:29], off
	v_pk_fma_f32 v[28:29], v[30:31], s[10:11], v[32:33] op_sel_hi:[1,0,0]
	v_pk_mul_f32 v[40:41], v[40:41], s[6:7] op_sel_hi:[1,0]
	v_pk_fma_f32 v[28:29], v[30:31], v[28:29], s[12:13] op_sel_hi:[1,1,0]
	v_exp_f32_e32 v40, v40
	v_exp_f32_e32 v41, v41
	v_pk_fma_f32 v[28:29], v[30:31], v[28:29], s[0:1] op_sel_hi:[1,1,0]
	v_pk_fma_f32 v[42:43], v[42:43], s[14:15], 1.0 op_sel_hi:[1,0,0]
	v_pk_fma_f32 v[28:29], v[30:31], v[28:29], s[4:5] op_sel_hi:[1,1,0]
	v_rcp_f32_e32 v42, v42
	v_pk_mul_f32 v[28:29], v[30:31], v[28:29]
	v_rcp_f32_e32 v43, v43
	v_pk_mul_f32 v[28:29], v[40:41], v[28:29]
	v_cmp_gt_f32_e32 vcc, 0, v24
	v_pk_mul_f32 v[40:41], v[24:25], v[28:29]
	v_pk_fma_f32 v[28:29], v[24:25], v[28:29], v[24:25] neg_lo:[1,0,0] neg_hi:[1,0,0]
	v_pk_mul_f32 v[30:31], v[26:27], v[26:27]
	v_cndmask_b32_e32 v37, v28, v40, vcc
	v_cmp_gt_f32_e32 vcc, 0, v25
	v_pk_fma_f32 v[24:25], v[42:43], s[10:11], v[32:33] op_sel_hi:[1,0,0]
	v_pk_add_f32 v[22:23], v[22:23], v[10:11]
	v_cndmask_b32_e32 v40, v29, v41, vcc
	v_pk_mul_f32 v[28:29], v[30:31], s[6:7] op_sel_hi:[1,0]
	v_pk_fma_f32 v[24:25], v[42:43], v[24:25], s[12:13] op_sel_hi:[1,1,0]
	v_exp_f32_e32 v28, v28
	v_exp_f32_e32 v29, v29
	v_pk_fma_f32 v[24:25], v[42:43], v[24:25], s[0:1] op_sel_hi:[1,1,0]
	v_cmp_gt_f32_e32 vcc, 0, v26
	v_pk_fma_f32 v[24:25], v[42:43], v[24:25], s[4:5] op_sel_hi:[1,1,0]
	v_pk_mul_f32 v[30:31], v[20:21], v[20:21]
	v_pk_mul_f32 v[24:25], v[42:43], v[24:25]
	v_pk_mul_f32 v[30:31], v[30:31], s[6:7] op_sel_hi:[1,0]
	v_pk_mul_f32 v[24:25], v[28:29], v[24:25]
	v_exp_f32_e32 v30, v30
	v_pk_mul_f32 v[28:29], v[26:27], v[24:25]
	v_pk_fma_f32 v[24:25], v[26:27], v[24:25], v[26:27] neg_lo:[1,0,0] neg_hi:[1,0,0]
	v_exp_f32_e32 v31, v31
	v_cndmask_b32_e32 v24, v24, v28, vcc
	v_cmp_gt_f32_e32 vcc, 0, v27
	v_and_b32_e32 v28, 0x7fffffff, v20
	v_or_b32_e32 v27, 32, v36
	v_cndmask_b32_e32 v25, v25, v29, vcc
	v_and_b32_e32 v29, 0x7fffffff, v21
	v_pk_fma_f32 v[28:29], v[28:29], s[14:15], 1.0 op_sel_hi:[1,0,0]
	v_cvt_pk_f16_f32 v25, v24, v25
	v_cvt_pk_f16_f32 v24, v37, v40
	v_rcp_f32_e32 v28, v28
	v_rcp_f32_e32 v29, v29
	global_store_dwordx2 v[38:39], v[24:25], off offset:32
	v_mad_u64_u32 v[24:25], s[16:17], v27, s2, 0
	v_mov_b32_e32 v26, v25
	v_mad_u64_u32 v[26:27], s[16:17], v27, s1, v[26:27]
	v_mov_b32_e32 v25, v26
	v_pk_fma_f32 v[26:27], v[28:29], s[10:11], v[32:33] op_sel_hi:[1,0,0]
	v_and_b32_e32 v39, 0x7fffffff, v23
	v_pk_fma_f32 v[26:27], v[28:29], v[26:27], s[12:13] op_sel_hi:[1,1,0]
	v_and_b32_e32 v38, 0x7fffffff, v22
	v_pk_fma_f32 v[26:27], v[28:29], v[26:27], s[0:1] op_sel_hi:[1,1,0]
	v_pk_fma_f32 v[38:39], v[38:39], s[14:15], 1.0 op_sel_hi:[1,0,0]
	v_pk_fma_f32 v[26:27], v[28:29], v[26:27], s[4:5] op_sel_hi:[1,1,0]
	v_rcp_f32_e32 v38, v38
	v_pk_mul_f32 v[26:27], v[28:29], v[26:27]
	v_rcp_f32_e32 v39, v39
	v_pk_mul_f32 v[26:27], v[30:31], v[26:27]
	v_cmp_gt_f32_e32 vcc, 0, v20
	v_pk_mul_f32 v[30:31], v[20:21], v[26:27]
	v_pk_fma_f32 v[26:27], v[20:21], v[26:27], v[20:21] neg_lo:[1,0,0] neg_hi:[1,0,0]
	v_pk_mul_f32 v[28:29], v[22:23], v[22:23]
	v_cndmask_b32_e32 v30, v26, v30, vcc
	v_cmp_gt_f32_e32 vcc, 0, v21
	v_pk_fma_f32 v[20:21], v[38:39], s[10:11], v[32:33] op_sel_hi:[1,0,0]
	v_pk_add_f32 v[16:17], v[16:17], v[12:13]
	v_cndmask_b32_e32 v31, v27, v31, vcc
	v_pk_mul_f32 v[26:27], v[28:29], s[6:7] op_sel_hi:[1,0]
	v_pk_fma_f32 v[20:21], v[38:39], v[20:21], s[12:13] op_sel_hi:[1,1,0]
	v_exp_f32_e32 v26, v26
	v_exp_f32_e32 v27, v27
	v_pk_fma_f32 v[20:21], v[38:39], v[20:21], s[0:1] op_sel_hi:[1,1,0]
	v_cmp_gt_f32_e32 vcc, 0, v22
	v_pk_fma_f32 v[20:21], v[38:39], v[20:21], s[4:5] op_sel_hi:[1,1,0]
	v_lshl_add_u64 v[24:25], v[24:25], 1, s[8:9]
	v_pk_mul_f32 v[20:21], v[38:39], v[20:21]
	v_lshl_add_u64 v[24:25], v[24:25], 0, v[34:35]
	v_pk_mul_f32 v[20:21], v[26:27], v[20:21]
	v_pk_add_f32 v[18:19], v[18:19], v[14:15]
	v_pk_mul_f32 v[26:27], v[22:23], v[20:21]
	v_pk_fma_f32 v[20:21], v[22:23], v[20:21], v[22:23] neg_lo:[1,0,0] neg_hi:[1,0,0]
	v_and_b32_e32 v22, 0x7fffffff, v16
	v_cndmask_b32_e32 v20, v20, v26, vcc
	v_cmp_gt_f32_e32 vcc, 0, v23
	v_and_b32_e32 v23, 0x7fffffff, v17
	v_pk_fma_f32 v[22:23], v[22:23], s[14:15], 1.0 op_sel_hi:[1,0,0]
	v_cndmask_b32_e32 v21, v21, v27, vcc
	v_rcp_f32_e32 v22, v22
	v_rcp_f32_e32 v23, v23
	v_cvt_pk_f16_f32 v21, v20, v21
	v_cvt_pk_f16_f32 v20, v30, v31
	v_pk_mul_f32 v[26:27], v[16:17], v[16:17]
	global_store_dwordx2 v[24:25], v[20:21], off
	v_pk_fma_f32 v[20:21], v[22:23], s[10:11], v[32:33] op_sel_hi:[1,0,0]
	v_pk_mul_f32 v[26:27], v[26:27], s[6:7] op_sel_hi:[1,0]
	v_pk_fma_f32 v[20:21], v[22:23], v[20:21], s[12:13] op_sel_hi:[1,1,0]
	v_exp_f32_e32 v26, v26
	v_exp_f32_e32 v27, v27
	v_pk_fma_f32 v[20:21], v[22:23], v[20:21], s[0:1] op_sel_hi:[1,1,0]
	v_and_b32_e32 v29, 0x7fffffff, v19
	v_and_b32_e32 v28, 0x7fffffff, v18
	v_pk_fma_f32 v[20:21], v[22:23], v[20:21], s[4:5] op_sel_hi:[1,1,0]
	v_pk_fma_f32 v[28:29], v[28:29], s[14:15], 1.0 op_sel_hi:[1,0,0]
	v_pk_mul_f32 v[20:21], v[22:23], v[20:21]
	v_rcp_f32_e32 v28, v28
	v_rcp_f32_e32 v29, v29
	v_pk_mul_f32 v[20:21], v[26:27], v[20:21]
	v_cmp_gt_f32_e32 vcc, 0, v16
	v_pk_mul_f32 v[26:27], v[16:17], v[20:21]
	v_pk_fma_f32 v[20:21], v[16:17], v[20:21], v[16:17] neg_lo:[1,0,0] neg_hi:[1,0,0]
	v_pk_mul_f32 v[22:23], v[18:19], v[18:19]
	v_cndmask_b32_e32 v26, v20, v26, vcc
	v_cmp_gt_f32_e32 vcc, 0, v17
	v_pk_fma_f32 v[16:17], v[28:29], s[10:11], v[32:33] op_sel_hi:[1,0,0]
	v_pk_add_f32 v[4:5], v[4:5], v[8:9]
	v_cndmask_b32_e32 v27, v21, v27, vcc
	v_pk_mul_f32 v[20:21], v[22:23], s[6:7] op_sel_hi:[1,0]
	v_pk_fma_f32 v[16:17], v[28:29], v[16:17], s[12:13] op_sel_hi:[1,1,0]
	v_exp_f32_e32 v20, v20
	v_exp_f32_e32 v21, v21
	v_pk_fma_f32 v[16:17], v[28:29], v[16:17], s[0:1] op_sel_hi:[1,1,0]
	v_cmp_gt_f32_e32 vcc, 0, v18
	v_pk_fma_f32 v[16:17], v[28:29], v[16:17], s[4:5] op_sel_hi:[1,1,0]
	v_and_b32_e32 v9, 0x7fffffff, v5
	v_pk_mul_f32 v[16:17], v[28:29], v[16:17]
	v_and_b32_e32 v8, 0x7fffffff, v4
	v_pk_mul_f32 v[16:17], v[20:21], v[16:17]
	v_pk_fma_f32 v[8:9], v[8:9], s[14:15], 1.0 op_sel_hi:[1,0,0]
	v_pk_mul_f32 v[20:21], v[18:19], v[16:17]
	v_pk_fma_f32 v[16:17], v[18:19], v[16:17], v[18:19] neg_lo:[1,0,0] neg_hi:[1,0,0]
	v_rcp_f32_e32 v8, v8
	v_cndmask_b32_e32 v16, v16, v20, vcc
	v_cmp_gt_f32_e32 vcc, 0, v19
	v_or_b32_e32 v19, 48, v36
	v_rcp_f32_e32 v9, v9
	v_cndmask_b32_e32 v17, v17, v21, vcc
	v_cvt_pk_f16_f32 v17, v16, v17
	v_cvt_pk_f16_f32 v16, v26, v27
	global_store_dwordx2 v[24:25], v[16:17], off offset:32
	v_mad_u64_u32 v[16:17], s[2:3], v19, s2, 0
	v_mov_b32_e32 v18, v17
	v_mad_u64_u32 v[18:19], s[2:3], v19, s1, v[18:19]
	v_mov_b32_e32 v17, v18
	v_pk_mul_f32 v[18:19], v[4:5], v[4:5]
	v_pk_add_f32 v[6:7], v[6:7], v[10:11]
	v_pk_fma_f32 v[10:11], v[8:9], s[10:11], v[32:33] op_sel_hi:[1,0,0]
	v_pk_mul_f32 v[18:19], v[18:19], s[6:7] op_sel_hi:[1,0]
	v_pk_fma_f32 v[10:11], v[8:9], v[10:11], s[12:13] op_sel_hi:[1,1,0]
	v_exp_f32_e32 v18, v18
	v_exp_f32_e32 v19, v19
	v_pk_fma_f32 v[10:11], v[8:9], v[10:11], s[0:1] op_sel_hi:[1,1,0]
	v_and_b32_e32 v21, 0x7fffffff, v7
	v_and_b32_e32 v20, 0x7fffffff, v6
	v_pk_fma_f32 v[10:11], v[8:9], v[10:11], s[4:5] op_sel_hi:[1,1,0]
	v_pk_fma_f32 v[20:21], v[20:21], s[14:15], 1.0 op_sel_hi:[1,0,0]
	v_pk_mul_f32 v[8:9], v[8:9], v[10:11]
	v_rcp_f32_e32 v20, v20
	v_rcp_f32_e32 v21, v21
	v_pk_mul_f32 v[8:9], v[18:19], v[8:9]
	v_cmp_gt_f32_e32 vcc, 0, v4
	v_pk_mul_f32 v[18:19], v[4:5], v[8:9]
	v_pk_fma_f32 v[8:9], v[4:5], v[8:9], v[4:5] neg_lo:[1,0,0] neg_hi:[1,0,0]
	v_pk_mul_f32 v[10:11], v[6:7], v[6:7]
	v_cndmask_b32_e32 v18, v8, v18, vcc
	v_cmp_gt_f32_e32 vcc, 0, v5
	v_pk_fma_f32 v[4:5], v[20:21], s[10:11], v[32:33] op_sel_hi:[1,0,0]
	v_pk_add_f32 v[0:1], v[0:1], v[12:13]
	v_cndmask_b32_e32 v19, v9, v19, vcc
	v_pk_mul_f32 v[8:9], v[10:11], s[6:7] op_sel_hi:[1,0]
	v_pk_fma_f32 v[4:5], v[20:21], v[4:5], s[12:13] op_sel_hi:[1,1,0]
	v_exp_f32_e32 v8, v8
	v_exp_f32_e32 v9, v9
	v_pk_fma_f32 v[4:5], v[20:21], v[4:5], s[0:1] op_sel_hi:[1,1,0]
	v_cmp_gt_f32_e32 vcc, 0, v6
	v_pk_fma_f32 v[4:5], v[20:21], v[4:5], s[4:5] op_sel_hi:[1,1,0]
	v_lshl_add_u64 v[16:17], v[16:17], 1, s[8:9]
	v_pk_mul_f32 v[4:5], v[20:21], v[4:5]
	v_pk_mul_f32 v[10:11], v[0:1], v[0:1]
	v_pk_mul_f32 v[4:5], v[8:9], v[4:5]
	v_pk_mul_f32 v[10:11], v[10:11], s[6:7] op_sel_hi:[1,0]
	v_pk_mul_f32 v[8:9], v[6:7], v[4:5]
	v_pk_fma_f32 v[4:5], v[6:7], v[4:5], v[6:7] neg_lo:[1,0,0] neg_hi:[1,0,0]
	v_and_b32_e32 v6, 0x7fffffff, v0
	v_cndmask_b32_e32 v4, v4, v8, vcc
	v_cmp_gt_f32_e32 vcc, 0, v7
	v_and_b32_e32 v7, 0x7fffffff, v1
	v_pk_fma_f32 v[6:7], v[6:7], s[14:15], 1.0 op_sel_hi:[1,0,0]
	v_cndmask_b32_e32 v5, v5, v9, vcc
	v_rcp_f32_e32 v6, v6
	v_rcp_f32_e32 v7, v7
	v_cvt_pk_f16_f32 v5, v4, v5
	v_cvt_pk_f16_f32 v4, v18, v19
	v_lshl_add_u64 v[8:9], v[16:17], 0, v[34:35]
	global_store_dwordx2 v[8:9], v[4:5], off
	v_pk_fma_f32 v[4:5], v[6:7], s[10:11], v[32:33] op_sel_hi:[1,0,0]
	v_pk_add_f32 v[2:3], v[2:3], v[14:15]
	v_pk_fma_f32 v[4:5], v[6:7], v[4:5], s[12:13] op_sel_hi:[1,1,0]
	v_exp_f32_e32 v10, v10
	v_exp_f32_e32 v11, v11
	v_pk_fma_f32 v[4:5], v[6:7], v[4:5], s[0:1] op_sel_hi:[1,1,0]
	v_and_b32_e32 v13, 0x7fffffff, v3
	v_and_b32_e32 v12, 0x7fffffff, v2
	v_pk_fma_f32 v[4:5], v[6:7], v[4:5], s[4:5] op_sel_hi:[1,1,0]
	v_pk_fma_f32 v[12:13], v[12:13], s[14:15], 1.0 op_sel_hi:[1,0,0]
	v_pk_mul_f32 v[4:5], v[6:7], v[4:5]
	v_rcp_f32_e32 v12, v12
	v_rcp_f32_e32 v13, v13
	v_pk_mul_f32 v[4:5], v[10:11], v[4:5]
	v_cmp_gt_f32_e32 vcc, 0, v0
	v_pk_mul_f32 v[10:11], v[0:1], v[4:5]
	v_pk_fma_f32 v[4:5], v[0:1], v[4:5], v[0:1] neg_lo:[1,0,0] neg_hi:[1,0,0]
	v_pk_mul_f32 v[6:7], v[2:3], v[2:3]
	v_cndmask_b32_e32 v10, v4, v10, vcc
	v_cmp_gt_f32_e32 vcc, 0, v1
	v_pk_fma_f32 v[0:1], v[12:13], s[10:11], v[32:33] op_sel_hi:[1,0,0]
	s_nop 0
	v_cndmask_b32_e32 v11, v5, v11, vcc
	v_pk_mul_f32 v[4:5], v[6:7], s[6:7] op_sel_hi:[1,0]
	v_pk_fma_f32 v[0:1], v[12:13], v[0:1], s[12:13] op_sel_hi:[1,1,0]
	v_exp_f32_e32 v4, v4
	v_exp_f32_e32 v5, v5
	v_pk_fma_f32 v[0:1], v[12:13], v[0:1], s[0:1] op_sel_hi:[1,1,0]
	v_cmp_gt_f32_e32 vcc, 0, v2
	v_pk_fma_f32 v[0:1], v[12:13], v[0:1], s[4:5] op_sel_hi:[1,1,0]
	s_nop 0
	v_pk_mul_f32 v[0:1], v[12:13], v[0:1]
	s_nop 0
	v_pk_mul_f32 v[0:1], v[4:5], v[0:1]
	s_nop 0
	v_pk_mul_f32 v[4:5], v[2:3], v[0:1]
	v_pk_fma_f32 v[0:1], v[2:3], v[0:1], v[2:3] neg_lo:[1,0,0] neg_hi:[1,0,0]
	s_nop 0
	v_cndmask_b32_e32 v0, v0, v4, vcc
	v_cmp_gt_f32_e32 vcc, 0, v3
	s_nop 1
	v_cndmask_b32_e32 v1, v1, v5, vcc
	v_cvt_pk_f16_f32 v1, v0, v1
	v_cvt_pk_f16_f32 v0, v10, v11
	global_store_dwordx2 v[8:9], v[0:1], off offset:32
	s_endpgm
	s_endpgm
	s_endpgm
	s_endpgm
	s_endpgm
	s_endpgm
	s_endpgm
	s_endpgm
	s_endpgm
	s_endpgm
	s_endpgm
	s_endpgm
	s_endpgm
	s_endpgm
	s_endpgm
	.section	.rodata,"a",@progbits
	.p2align	6, 0x0

_Z5gemm8ILi64ELi4ELi6ELi1ELi1ELi16EEvPKDF16_S1_iiiPDF16_PfPKf:
	v_readfirstlane_b32 s28, v0
	s_nop 3
	s_nop 0
	s_bitcmp1_b32 s28, 8
	s_cbranch_scc0 .Lprio_skip2
	s_setprio 1

.LBB6_4:
	s_load_dwordx2 s[2:3], s[0:1], 0x14
	s_lshl_b32 s12, s15, 7
	s_lshl_b32 s13, s14, 6
	v_lshrrev_b32_e32 v2, 4, v0
	v_xor_b32_e32 v1, v2, v0
	s_waitcnt lgkmcnt(0)
	v_and_b32_e32 v76, 15, v0
	v_lshrrev_b32_e32 v77, 7, v0
	v_lshl_or_b32 v76, v77, 5, v76
	v_or_b32_e32 v76, s12, v76
	v_bfe_u32 v77, v0, 4, 2
	v_bfe_u32 v78, v0, 6, 1
	v_lshlrev_b32_e32 v77, 2, v77
	v_lshl_or_b32 v77, v78, 5, v77
	v_or_b32_e32 v77, s13, v77
	v_mul_lo_u32 v78, v76, s2
	s_lshl_b32 s22, s2, 6
	v_add_lshl_u32 v78, v78, v77, 2
	v_lshlrev_b32_e32 v77, 2, v77
	v_add_u32_e32 v79, s22, v78
	global_load_dwordx4 v[80:83], v78, s[8:9]
	global_load_dwordx4 v[84:87], v78, s[8:9] offset:64
	global_load_dwordx4 v[88:91], v77, s[10:11]
	global_load_dwordx4 v[92:95], v77, s[10:11] offset:64
	global_load_dwordx4 v[96:99], v79, s[8:9]
	global_load_dwordx4 v[100:103], v79, s[8:9] offset:64
	s_ashr_i32 s14, s3, 31
	s_mul_i32 s0, s12, s14
	s_mul_hi_u32 s1, s12, s3
	s_add_i32 s1, s1, s0
	s_mul_i32 s0, s12, s3
	v_or_b32_e32 v4, 0x200, v0
	s_lshl_b64 s[0:1], s[0:1], 1
	v_lshlrev_b32_e32 v1, 3, v1
	v_lshrrev_b32_e32 v3, 3, v0
	v_lshrrev_b32_e32 v4, 3, v4
	s_add_u32 s0, s4, s0
	v_and_b32_e32 v1, 56, v1
	v_mul_lo_u32 v3, v3, s3
	v_mul_lo_u32 v4, v4, s3
	s_addc_u32 s1, s5, s1
	s_mul_i32 s4, s13, s14
	s_mul_hi_u32 s5, s13, s3
	v_lshlrev_b32_e32 v54, 4, v0
	v_add_lshl_u32 v3, v3, v1, 1
	v_add_lshl_u32 v4, v4, v1, 1
	s_add_i32 s5, s5, s4
	s_mul_i32 s4, s13, s3
	v_add_u32_e32 v1, 0, v54
	s_lshl_b64 s[4:5], s[4:5], 1
	v_readfirstlane_b32 s19, v1
	v_add_u32_e32 v5, 0x2000, v1
	s_add_u32 s4, s6, s4
	s_mov_b32 m0, s19
	v_readfirstlane_b32 s17, v5
	v_add_u32_e32 v5, 0x4000, v1
	s_addc_u32 s5, s7, s5
	global_load_lds_dwordx4 v3, s[0:1]
	s_mov_b32 m0, s17
	v_readfirstlane_b32 s18, v5
	v_add_u32_e32 v5, 0x6000, v1
	global_load_lds_dwordx4 v4, s[0:1]
	s_mov_b32 m0, s18
	s_add_u32 s6, s0, 0x80
	v_readfirstlane_b32 s16, v5
	v_add_u32_e32 v5, 0x8000, v1
	global_load_lds_dwordx4 v3, s[4:5]
	s_addc_u32 s7, s1, 0
	s_mov_b32 m0, s16
	v_readfirstlane_b32 s14, v5
	v_add_u32_e32 v5, 0xa000, v1
	s_add_u32 s20, s4, 0x80
	global_load_lds_dwordx4 v3, s[6:7]
	s_mov_b32 m0, s14
	v_readfirstlane_b32 s15, v5
	s_addc_u32 s21, s5, 0
	global_load_lds_dwordx4 v4, s[6:7]
	s_mov_b32 m0, s15
	v_add_u32_e32 v5, 0xc000, v1
	global_load_lds_dwordx4 v3, s[20:21]
	s_add_u32 s20, s0, 0x100
	s_addc_u32 s21, s1, 0
	v_readfirstlane_b32 s7, v5
	v_add_u32_e32 v5, 0xe000, v1
	s_add_u32 s22, s4, 0x100
	s_mov_b32 m0, s7
	v_readfirstlane_b32 s3, v5
	v_add_u32_e32 v5, 0x10000, v1
	s_addc_u32 s23, s5, 0
	global_load_lds_dwordx4 v3, s[20:21]
	s_mov_b32 m0, s3
	v_readfirstlane_b32 s6, v5
	v_add_u32_e32 v5, 0x12000, v1
	global_load_lds_dwordx4 v4, s[20:21]
	s_mov_b32 m0, s6
	s_add_u32 s20, s0, 0x180
	v_readfirstlane_b32 s24, v5
	v_add_u32_e32 v5, 0x14000, v1
	global_load_lds_dwordx4 v3, s[22:23]
	s_addc_u32 s21, s1, 0
	s_mov_b32 m0, s24
	v_readfirstlane_b32 s24, v5
	s_add_u32 s22, s4, 0x180
	global_load_lds_dwordx4 v3, s[20:21]
	s_mov_b32 m0, s24
	v_add_u32_e32 v5, 0x16000, v1
	s_addc_u32 s23, s5, 0
	global_load_lds_dwordx4 v4, s[20:21]
	v_readfirstlane_b32 s20, v5
	v_add_u32_e32 v5, 0x18000, v1
	s_mov_b32 m0, s20
	s_add_u32 s20, s0, 0x200
	v_readfirstlane_b32 s24, v5
	v_add_u32_e32 v5, 0x1a000, v1
	global_load_lds_dwordx4 v3, s[22:23]
	s_addc_u32 s21, s1, 0
	s_mov_b32 m0, s24
	v_readfirstlane_b32 s24, v5
	s_add_u32 s22, s4, 0x200
	global_load_lds_dwordx4 v3, s[20:21]
	s_mov_b32 m0, s24
	v_add_u32_e32 v5, 0x1c000, v1
	s_addc_u32 s23, s5, 0
	global_load_lds_dwordx4 v4, s[20:21]
	v_readfirstlane_b32 s20, v5
	v_add_u32_e32 v5, 0x1e000, v1
	s_mov_b32 m0, s20
	s_add_u32 s20, s0, 0x280
	v_readfirstlane_b32 s24, v5
	v_add_u32_e32 v5, 0x20000, v1
	global_load_lds_dwordx4 v3, s[22:23]
	s_addc_u32 s21, s1, 0
	s_mov_b32 m0, s24
	v_readfirstlane_b32 s24, v5
	global_load_lds_dwordx4 v3, s[20:21]
	s_mov_b32 m0, s24
	v_add_u32_e32 v1, 0x22000, v1
	s_add_u32 s22, s4, 0x280
	global_load_lds_dwordx4 v4, s[20:21]
	v_readfirstlane_b32 s20, v1
	s_addc_u32 s23, s5, 0
	s_mov_b32 m0, s20
	v_bfe_u32 v7, v0, 1, 3
	global_load_lds_dwordx4 v3, s[22:23]
	v_lshrrev_b32_e32 v6, 1, v0
	v_bitop3_b32 v2, v2, v7, 3 bitop3:0x6c
	v_and_b32_e32 v5, 15, v0
	v_lshrrev_b32_e32 v1, 2, v0
	s_movk_i32 s20, 0x60
	v_lshlrev_b32_e32 v9, 4, v2
	v_and_b32_e32 v2, 32, v6
	v_and_or_b32 v1, v1, s20, v5
	v_or_b32_e32 v5, v2, v5
	v_lshlrev_b32_e32 v6, 7, v5
	v_add_u32_e32 v38, 0, v6
	s_waitcnt vmcnt(15)
	s_barrier
	v_add_u32_e32 v8, v38, v9
	ds_read_b128 v[10:13], v8 offset:16384
	v_lshlrev_b32_e32 v55, 7, v1
	v_add_u32_e32 v30, 0, v55
	v_add_u32_e32 v5, v30, v9
	ds_read_b128 v[14:17], v5
	ds_read_b128 v[18:21], v8 offset:18432
	ds_read_b128 v[22:25], v5 offset:2048
	v_bfe_u32 v0, v0, 4, 2
	v_bitop3_b32 v9, v0, v7, 4 bitop3:0x36
	s_waitcnt lgkmcnt(0)
	v_mfma_f32_16x16x32_f16 v[26:29], v[10:13], v[14:17], 0
	v_or_b32_e32 v56, 0x4000, v6
	v_add_u32_e32 v7, 0x4000, v8
	v_lshlrev_b32_e32 v57, 4, v9
	v_mfma_f32_16x16x32_f16 v[14:17], v[18:21], v[14:17], 0
	v_add_u32_e32 v6, v30, v57
	v_add_u32_e32 v9, v38, v57
	ds_read_b128 v[30:33], v6
	ds_read_b128 v[34:37], v6 offset:2048
	ds_read_b128 v[38:41], v9 offset:16384
	ds_read_b128 v[42:45], v9 offset:18432
	v_mfma_f32_16x16x32_f16 v[10:13], v[10:13], v[22:25], 0
	v_mfma_f32_16x16x32_f16 v[18:21], v[18:21], v[22:25], 0
	s_add_u32 s20, s0, 0x300
	s_mov_b32 m0, s19
	s_waitcnt vmcnt(12) lgkmcnt(0)
	s_barrier
	s_addc_u32 s21, s1, 0
	s_add_u32 s22, s4, 0x300
	global_load_lds_dwordx4 v3, s[20:21]
	s_mov_b32 m0, s17
	s_addc_u32 s23, s5, 0
	global_load_lds_dwordx4 v4, s[20:21]
	s_mov_b32 m0, s18
	s_nop 0
	global_load_lds_dwordx4 v3, s[22:23]
	s_waitcnt lgkmcnt(0)
	v_mfma_f32_16x16x32_f16 v[22:25], v[38:41], v[30:33], v[26:29]
	v_mfma_f32_16x16x32_f16 v[14:17], v[42:45], v[30:33], v[14:17]
	s_nop 1
	ds_read_b128 v[26:29], v5 offset:24576
	ds_read_b128 v[30:33], v5 offset:26624
	ds_read_b128 v[46:49], v8 offset:40960
	ds_read_b128 v[50:53], v8 offset:43008
	v_mfma_f32_16x16x32_f16 v[10:13], v[38:41], v[34:37], v[10:13]
	v_mfma_f32_16x16x32_f16 v[18:21], v[42:45], v[34:37], v[18:21]
	s_waitcnt lgkmcnt(0)
	v_mfma_f32_16x16x32_f16 v[22:25], v[46:49], v[26:29], v[22:25]
	v_mfma_f32_16x16x32_f16 v[14:17], v[50:53], v[26:29], v[14:17]
	ds_read_b128 v[26:29], v6 offset:24576
	ds_read_b128 v[34:37], v6 offset:26624
	ds_read_b128 v[38:41], v9 offset:40960
	ds_read_b128 v[42:45], v9 offset:43008
	v_mfma_f32_16x16x32_f16 v[10:13], v[46:49], v[30:33], v[10:13]
	v_mfma_f32_16x16x32_f16 v[18:21], v[50:53], v[30:33], v[18:21]
	s_add_u32 s20, s0, 0x380
	s_mov_b32 m0, s16
	s_waitcnt vmcnt(12) lgkmcnt(0)
	s_barrier
	s_addc_u32 s21, s1, 0
	s_add_u32 s22, s4, 0x380
	global_load_lds_dwordx4 v3, s[20:21]
	s_mov_b32 m0, s14
	s_addc_u32 s23, s5, 0
	global_load_lds_dwordx4 v4, s[20:21]
	s_mov_b32 m0, s15
	s_nop 0
	global_load_lds_dwordx4 v3, s[22:23]
	s_waitcnt lgkmcnt(0)
	v_mfma_f32_16x16x32_f16 v[22:25], v[38:41], v[26:29], v[22:25]
	v_mfma_f32_16x16x32_f16 v[14:17], v[42:45], v[26:29], v[14:17]
	ds_read_b128 v[26:29], v5 offset:49152
	ds_read_b128 v[30:33], v5 offset:51200
	ds_read_b128 v[46:49], v7 offset:49152
	ds_read_b128 v[50:53], v7 offset:51200
	v_mfma_f32_16x16x32_f16 v[10:13], v[38:41], v[34:37], v[10:13]
	v_mfma_f32_16x16x32_f16 v[18:21], v[42:45], v[34:37], v[18:21]
	s_waitcnt lgkmcnt(0)
	v_mfma_f32_16x16x32_f16 v[22:25], v[46:49], v[26:29], v[22:25]
	v_mfma_f32_16x16x32_f16 v[14:17], v[50:53], v[26:29], v[14:17]
	s_add_i32 s20, 0, 0xc000
	v_add3_u32 v58, s20, v57, v56
	ds_read_b128 v[26:29], v6 offset:49152
	ds_read_b128 v[34:37], v6 offset:51200
	ds_read_b128 v[38:41], v58
	ds_read_b128 v[42:45], v58 offset:2048
	v_mfma_f32_16x16x32_f16 v[10:13], v[46:49], v[30:33], v[10:13]
	v_mfma_f32_16x16x32_f16 v[18:21], v[50:53], v[30:33], v[18:21]
	s_add_u32 s20, s0, 0x400
	s_mov_b32 m0, s7
	s_waitcnt vmcnt(12) lgkmcnt(0)
	s_barrier
	s_addc_u32 s21, s1, 0
	s_add_u32 s22, s4, 0x400
	global_load_lds_dwordx4 v3, s[20:21]
	s_mov_b32 m0, s3
	s_addc_u32 s23, s5, 0
	global_load_lds_dwordx4 v4, s[20:21]
	s_mov_b32 m0, s6
	s_nop 0
	global_load_lds_dwordx4 v3, s[22:23]
	s_waitcnt lgkmcnt(0)
	v_mfma_f32_16x16x32_f16 v[22:25], v[38:41], v[26:29], v[22:25]
	v_mfma_f32_16x16x32_f16 v[14:17], v[42:45], v[26:29], v[14:17]
	v_add_u32_e32 v59, 0x12000, v5
	v_add_u32_e32 v61, 0x16000, v8
	v_add_u32_e32 v60, 0x12800, v5
	ds_read_b128 v[26:29], v59
	ds_read_b128 v[30:33], v60
	v_add_u32_e32 v62, 0x16800, v8
	ds_read_b128 v[46:49], v61
	ds_read_b128 v[50:53], v62
	v_mfma_f32_16x16x32_f16 v[10:13], v[38:41], v[34:37], v[10:13]
	v_mfma_f32_16x16x32_f16 v[18:21], v[42:45], v[34:37], v[18:21]
	s_waitcnt lgkmcnt(0)
	v_mfma_f32_16x16x32_f16 v[22:25], v[46:49], v[26:29], v[22:25]
	v_mfma_f32_16x16x32_f16 v[14:17], v[50:53], v[26:29], v[14:17]
	s_add_i32 s20, 0, 0x12000
	v_add_u32_e32 v38, s20, v57
	v_add_u32_e32 v63, v38, v55
	v_add_u32_e32 v64, v38, v56
	ds_read_b128 v[26:29], v63
	ds_read_b128 v[34:37], v63 offset:2048
	ds_read_b128 v[38:41], v64
	ds_read_b128 v[42:45], v64 offset:2048
	v_mfma_f32_16x16x32_f16 v[10:13], v[46:49], v[30:33], v[10:13]
	v_mfma_f32_16x16x32_f16 v[18:21], v[50:53], v[30:33], v[18:21]
	v_add_u32_e32 v30, s20, v54
	s_add_u32 s24, s0, 0x480
	v_readfirstlane_b32 s22, v30
	v_add_u32_e32 v31, 0x2000, v30
	s_waitcnt vmcnt(12) lgkmcnt(0)
	s_barrier
	s_addc_u32 s25, s1, 0
	s_mov_b32 m0, s22
	v_readfirstlane_b32 s20, v31
	v_add_u32_e32 v30, 0x4000, v30
	s_add_u32 s26, s4, 0x480
	global_load_lds_dwordx4 v3, s[24:25]
	s_mov_b32 m0, s20
	v_readfirstlane_b32 s21, v30
	s_addc_u32 s27, s5, 0
	global_load_lds_dwordx4 v4, s[24:25]
	s_mov_b32 m0, s21
	s_nop 0
	global_load_lds_dwordx4 v3, s[26:27]
	s_waitcnt lgkmcnt(0)
	v_mfma_f32_16x16x32_f16 v[22:25], v[38:41], v[26:29], v[22:25]
	v_mfma_f32_16x16x32_f16 v[14:17], v[42:45], v[26:29], v[14:17]
	v_add_u32_e32 v65, 0x18000, v5
	v_add_u32_e32 v67, 0x1c000, v8
	v_add_u32_e32 v66, 0x18800, v5
	ds_read_b128 v[26:29], v65
	ds_read_b128 v[30:33], v66
	v_add_u32_e32 v68, 0x1c800, v8
	ds_read_b128 v[46:49], v67
	ds_read_b128 v[50:53], v68
	v_mfma_f32_16x16x32_f16 v[10:13], v[38:41], v[34:37], v[10:13]
	v_mfma_f32_16x16x32_f16 v[18:21], v[42:45], v[34:37], v[18:21]
	s_waitcnt lgkmcnt(0)
	v_mfma_f32_16x16x32_f16 v[22:25], v[46:49], v[26:29], v[22:25]
	v_mfma_f32_16x16x32_f16 v[14:17], v[50:53], v[26:29], v[14:17]
	s_add_i32 s23, 0, 0x18000
	v_add_u32_e32 v38, s23, v57
	v_add_u32_e32 v69, v38, v55
	v_add_u32_e32 v70, v38, v56
	ds_read_b128 v[26:29], v69
	ds_read_b128 v[34:37], v69 offset:2048
	ds_read_b128 v[38:41], v70
	ds_read_b128 v[42:45], v70 offset:2048
	v_mfma_f32_16x16x32_f16 v[10:13], v[46:49], v[30:33], v[10:13]
	v_mfma_f32_16x16x32_f16 v[18:21], v[50:53], v[30:33], v[18:21]
	v_add_u32_e32 v30, s23, v54
	s_add_u32 s24, s0, 0x500
	v_readfirstlane_b32 s23, v30
	v_add_u32_e32 v31, 0x2000, v30
	s_waitcnt vmcnt(12) lgkmcnt(0)
	s_barrier
	s_addc_u32 s25, s1, 0
	s_mov_b32 m0, s23
	v_readfirstlane_b32 s23, v31
	v_add_u32_e32 v30, 0x4000, v30
	s_add_u32 s26, s4, 0x500
	global_load_lds_dwordx4 v3, s[24:25]
	s_mov_b32 m0, s23
	v_readfirstlane_b32 s23, v30
	s_addc_u32 s27, s5, 0
	global_load_lds_dwordx4 v4, s[24:25]
	s_mov_b32 m0, s23
	s_nop 0
	global_load_lds_dwordx4 v3, s[26:27]
	s_waitcnt lgkmcnt(0)
	v_mfma_f32_16x16x32_f16 v[22:25], v[38:41], v[26:29], v[22:25]
	v_mfma_f32_16x16x32_f16 v[14:17], v[42:45], v[26:29], v[14:17]
	v_add_u32_e32 v71, 0x1e000, v5
	v_add_u32_e32 v73, 0x22000, v8
	v_add_u32_e32 v72, 0x1e800, v5
	ds_read_b128 v[26:29], v71
	ds_read_b128 v[30:33], v72
	v_add_u32_e32 v74, 0x22800, v8
	ds_read_b128 v[46:49], v73
	ds_read_b128 v[50:53], v74
	v_mfma_f32_16x16x32_f16 v[10:13], v[38:41], v[34:37], v[10:13]
	v_mfma_f32_16x16x32_f16 v[18:21], v[42:45], v[34:37], v[18:21]
	s_waitcnt lgkmcnt(0)
	v_mfma_f32_16x16x32_f16 v[22:25], v[46:49], v[26:29], v[22:25]
	v_mfma_f32_16x16x32_f16 v[14:17], v[50:53], v[26:29], v[14:17]
	s_add_i32 s23, 0, 0x1e000
	v_add_u32_e32 v38, s23, v57
	v_add_u32_e32 v55, v38, v55
	v_add_u32_e32 v56, v38, v56
	ds_read_b128 v[26:29], v55
	ds_read_b128 v[34:37], v55 offset:2048
	ds_read_b128 v[38:41], v56
	ds_read_b128 v[42:45], v56 offset:2048
	v_mfma_f32_16x16x32_f16 v[10:13], v[46:49], v[30:33], v[10:13]
	v_mfma_f32_16x16x32_f16 v[18:21], v[50:53], v[30:33], v[18:21]
	v_add_u32_e32 v30, s23, v54
	s_add_u32 s24, s0, 0x580
	v_readfirstlane_b32 s23, v30
	v_add_u32_e32 v31, 0x2000, v30
	s_waitcnt vmcnt(12) lgkmcnt(0)
	s_barrier
	s_addc_u32 s25, s1, 0
	s_mov_b32 m0, s23
	v_readfirstlane_b32 s23, v31
	v_add_u32_e32 v30, 0x4000, v30
	s_add_u32 s26, s4, 0x580
	global_load_lds_dwordx4 v3, s[24:25]
	s_mov_b32 m0, s23
	v_readfirstlane_b32 s23, v30
	s_addc_u32 s27, s5, 0
	global_load_lds_dwordx4 v4, s[24:25]
	s_mov_b32 m0, s23
	s_nop 0
	global_load_lds_dwordx4 v3, s[26:27]
	s_waitcnt lgkmcnt(0)
	v_mfma_f32_16x16x32_f16 v[22:25], v[38:41], v[26:29], v[22:25]
	v_mfma_f32_16x16x32_f16 v[14:17], v[42:45], v[26:29], v[14:17]
	ds_read_b128 v[26:29], v5
	ds_read_b128 v[30:33], v5 offset:2048
	ds_read_b128 v[46:49], v8 offset:16384
	ds_read_b128 v[50:53], v8 offset:18432
	v_mfma_f32_16x16x32_f16 v[10:13], v[38:41], v[34:37], v[10:13]
	v_mfma_f32_16x16x32_f16 v[18:21], v[42:45], v[34:37], v[18:21]
	s_waitcnt lgkmcnt(0)
	v_mfma_f32_16x16x32_f16 v[22:25], v[46:49], v[26:29], v[22:25]
	v_mfma_f32_16x16x32_f16 v[14:17], v[50:53], v[26:29], v[14:17]
	ds_read_b128 v[26:29], v6
	ds_read_b128 v[34:37], v6 offset:2048
	ds_read_b128 v[38:41], v9 offset:16384
	ds_read_b128 v[42:45], v9 offset:18432
	v_mfma_f32_16x16x32_f16 v[10:13], v[46:49], v[30:33], v[10:13]
	v_mfma_f32_16x16x32_f16 v[18:21], v[50:53], v[30:33], v[18:21]
	s_add_u32 s24, s0, 0x600
	s_mov_b32 m0, s19
	s_waitcnt vmcnt(12) lgkmcnt(0)
	s_barrier
	s_addc_u32 s25, s1, 0
	s_add_u32 s26, s4, 0x600
	global_load_lds_dwordx4 v3, s[24:25]
	s_mov_b32 m0, s17
	s_addc_u32 s27, s5, 0
	global_load_lds_dwordx4 v4, s[24:25]
	s_mov_b32 m0, s18
	s_nop 0
	global_load_lds_dwordx4 v3, s[26:27]
	s_waitcnt lgkmcnt(0)
	v_mfma_f32_16x16x32_f16 v[22:25], v[38:41], v[26:29], v[22:25]
	v_mfma_f32_16x16x32_f16 v[14:17], v[42:45], v[26:29], v[14:17]
	ds_read_b128 v[26:29], v5 offset:24576
	ds_read_b128 v[30:33], v5 offset:26624
	ds_read_b128 v[46:49], v8 offset:40960
	ds_read_b128 v[50:53], v8 offset:43008
	v_mfma_f32_16x16x32_f16 v[10:13], v[38:41], v[34:37], v[10:13]
	v_mfma_f32_16x16x32_f16 v[18:21], v[42:45], v[34:37], v[18:21]
	s_waitcnt lgkmcnt(0)
	v_mfma_f32_16x16x32_f16 v[22:25], v[46:49], v[26:29], v[22:25]
	v_mfma_f32_16x16x32_f16 v[14:17], v[50:53], v[26:29], v[14:17]
	ds_read_b128 v[26:29], v6 offset:24576
	ds_read_b128 v[34:37], v6 offset:26624
	ds_read_b128 v[38:41], v9 offset:40960
	ds_read_b128 v[42:45], v9 offset:43008
	v_mfma_f32_16x16x32_f16 v[10:13], v[46:49], v[30:33], v[10:13]
	v_mfma_f32_16x16x32_f16 v[18:21], v[50:53], v[30:33], v[18:21]
	s_mov_b32 m0, s16
	s_add_u32 s16, s0, 0x680
	s_waitcnt vmcnt(12) lgkmcnt(0)
	s_barrier
	s_addc_u32 s17, s1, 0
	s_add_u32 s18, s4, 0x680
	global_load_lds_dwordx4 v3, s[16:17]
	s_mov_b32 m0, s14
	s_addc_u32 s19, s5, 0
	global_load_lds_dwordx4 v4, s[16:17]
	s_mov_b32 m0, s15
	s_nop 0
	global_load_lds_dwordx4 v3, s[18:19]
	s_waitcnt lgkmcnt(0)
	v_mfma_f32_16x16x32_f16 v[22:25], v[38:41], v[26:29], v[22:25]
	v_mfma_f32_16x16x32_f16 v[14:17], v[42:45], v[26:29], v[14:17]
	ds_read_b128 v[26:29], v5 offset:49152
	ds_read_b128 v[30:33], v5 offset:51200
	ds_read_b128 v[46:49], v7 offset:49152
	ds_read_b128 v[50:53], v7 offset:51200
	v_mfma_f32_16x16x32_f16 v[10:13], v[38:41], v[34:37], v[10:13]
	v_mfma_f32_16x16x32_f16 v[18:21], v[42:45], v[34:37], v[18:21]
	s_waitcnt lgkmcnt(0)
	v_mfma_f32_16x16x32_f16 v[22:25], v[46:49], v[26:29], v[22:25]
	v_mfma_f32_16x16x32_f16 v[14:17], v[50:53], v[26:29], v[14:17]
	ds_read_b128 v[26:29], v6 offset:49152
	ds_read_b128 v[34:37], v6 offset:51200
	ds_read_b128 v[38:41], v58
	ds_read_b128 v[42:45], v58 offset:2048
	v_mfma_f32_16x16x32_f16 v[10:13], v[46:49], v[30:33], v[10:13]
	v_mfma_f32_16x16x32_f16 v[18:21], v[50:53], v[30:33], v[18:21]
	s_add_u32 s14, s0, 0x700
	s_mov_b32 m0, s7
	s_waitcnt vmcnt(12) lgkmcnt(0)
	s_barrier
	s_addc_u32 s15, s1, 0
	s_add_u32 s16, s4, 0x700
	global_load_lds_dwordx4 v3, s[14:15]
	s_mov_b32 m0, s3
	s_addc_u32 s17, s5, 0
	global_load_lds_dwordx4 v4, s[14:15]
	s_mov_b32 m0, s6
	s_nop 0
	global_load_lds_dwordx4 v3, s[16:17]
	s_waitcnt lgkmcnt(0)
	v_mfma_f32_16x16x32_f16 v[22:25], v[38:41], v[26:29], v[22:25]
	v_mfma_f32_16x16x32_f16 v[14:17], v[42:45], v[26:29], v[14:17]
	ds_read_b128 v[26:29], v59
	ds_read_b128 v[30:33], v60
	ds_read_b128 v[46:49], v61
	ds_read_b128 v[50:53], v62
	v_mfma_f32_16x16x32_f16 v[10:13], v[38:41], v[34:37], v[10:13]
	v_mfma_f32_16x16x32_f16 v[18:21], v[42:45], v[34:37], v[18:21]
	s_waitcnt lgkmcnt(0)
	v_mfma_f32_16x16x32_f16 v[22:25], v[46:49], v[26:29], v[22:25]
	v_mfma_f32_16x16x32_f16 v[14:17], v[50:53], v[26:29], v[14:17]
	ds_read_b128 v[26:29], v63
	ds_read_b128 v[34:37], v63 offset:2048
	ds_read_b128 v[38:41], v64
	ds_read_b128 v[42:45], v64 offset:2048
	v_mfma_f32_16x16x32_f16 v[10:13], v[46:49], v[30:33], v[10:13]
	v_mfma_f32_16x16x32_f16 v[18:21], v[50:53], v[30:33], v[18:21]
	s_add_u32 s0, s0, 0x780
	s_mov_b32 m0, s22
	s_waitcnt vmcnt(12) lgkmcnt(0)
	s_barrier
	s_addc_u32 s1, s1, 0
	s_add_u32 s4, s4, 0x780
	global_load_lds_dwordx4 v3, s[0:1]
	s_mov_b32 m0, s20
	s_addc_u32 s5, s5, 0
	global_load_lds_dwordx4 v4, s[0:1]
	s_mov_b32 m0, s21
	s_nop 0
	global_load_lds_dwordx4 v3, s[4:5]
	s_waitcnt lgkmcnt(0)
	v_mfma_f32_16x16x32_f16 v[22:25], v[38:41], v[26:29], v[22:25]
	v_mfma_f32_16x16x32_f16 v[14:17], v[42:45], v[26:29], v[14:17]
	ds_read_b128 v[26:29], v65
	ds_read_b128 v[30:33], v66
	ds_read_b128 v[46:49], v67
	ds_read_b128 v[50:53], v68
	v_mfma_f32_16x16x32_f16 v[10:13], v[38:41], v[34:37], v[10:13]
	v_mfma_f32_16x16x32_f16 v[18:21], v[42:45], v[34:37], v[18:21]
	s_waitcnt lgkmcnt(0)
	v_mfma_f32_16x16x32_f16 v[22:25], v[46:49], v[26:29], v[22:25]
	v_mfma_f32_16x16x32_f16 v[14:17], v[50:53], v[26:29], v[14:17]
	ds_read_b128 v[26:29], v69
	ds_read_b128 v[34:37], v69 offset:2048
	ds_read_b128 v[38:41], v70
	ds_read_b128 v[42:45], v70 offset:2048
	v_mfma_f32_16x16x32_f16 v[10:13], v[46:49], v[30:33], v[10:13]
	v_mfma_f32_16x16x32_f16 v[18:21], v[50:53], v[30:33], v[18:21]
	s_waitcnt vmcnt(12) lgkmcnt(0)
	s_barrier
	s_waitcnt lgkmcnt(0)
	v_mfma_f32_16x16x32_f16 v[22:25], v[38:41], v[26:29], v[22:25]
	v_mfma_f32_16x16x32_f16 v[14:17], v[42:45], v[26:29], v[14:17]
	ds_read_b128 v[26:29], v71
	ds_read_b128 v[30:33], v72
	ds_read_b128 v[46:49], v73
	ds_read_b128 v[50:53], v74
	v_mfma_f32_16x16x32_f16 v[10:13], v[38:41], v[34:37], v[10:13]
	v_mfma_f32_16x16x32_f16 v[18:21], v[42:45], v[34:37], v[18:21]
	s_waitcnt lgkmcnt(0)
	v_mfma_f32_16x16x32_f16 v[22:25], v[46:49], v[26:29], v[22:25]
	v_mfma_f32_16x16x32_f16 v[14:17], v[50:53], v[26:29], v[14:17]
	ds_read_b128 v[26:29], v55
	ds_read_b128 v[34:37], v55 offset:2048
	ds_read_b128 v[38:41], v56
	ds_read_b128 v[42:45], v56 offset:2048
	v_mfma_f32_16x16x32_f16 v[10:13], v[46:49], v[30:33], v[10:13]
	v_mfma_f32_16x16x32_f16 v[18:21], v[50:53], v[30:33], v[18:21]
	s_waitcnt vmcnt(0) lgkmcnt(0)
	s_barrier
	s_waitcnt lgkmcnt(0)
	v_mfma_f32_16x16x32_f16 v[22:25], v[38:41], v[26:29], v[22:25]
	v_mfma_f32_16x16x32_f16 v[14:17], v[42:45], v[26:29], v[14:17]
	ds_read_b128 v[26:29], v5
	ds_read_b128 v[30:33], v5 offset:2048
	ds_read_b128 v[46:49], v8 offset:16384
	ds_read_b128 v[50:53], v8 offset:18432
	v_mfma_f32_16x16x32_f16 v[10:13], v[38:41], v[34:37], v[10:13]
	v_mfma_f32_16x16x32_f16 v[18:21], v[42:45], v[34:37], v[18:21]
	s_waitcnt lgkmcnt(0)
	v_mfma_f32_16x16x32_f16 v[22:25], v[46:49], v[26:29], v[22:25]
	v_mfma_f32_16x16x32_f16 v[14:17], v[50:53], v[26:29], v[14:17]
	ds_read_b128 v[26:29], v6
	ds_read_b128 v[34:37], v6 offset:2048
	ds_read_b128 v[38:41], v9 offset:16384
	ds_read_b128 v[42:45], v9 offset:18432
	v_mfma_f32_16x16x32_f16 v[10:13], v[46:49], v[30:33], v[10:13]
	v_mfma_f32_16x16x32_f16 v[18:21], v[50:53], v[30:33], v[18:21]
	s_waitcnt vmcnt(0) lgkmcnt(0)
	s_barrier
	s_waitcnt lgkmcnt(0)
	v_mfma_f32_16x16x32_f16 v[22:25], v[38:41], v[26:29], v[22:25]
	v_mfma_f32_16x16x32_f16 v[14:17], v[42:45], v[26:29], v[14:17]
	ds_read_b128 v[26:29], v5 offset:24576
	ds_read_b128 v[30:33], v5 offset:26624
	ds_read_b128 v[46:49], v8 offset:40960
	ds_read_b128 v[50:53], v8 offset:43008
	v_mfma_f32_16x16x32_f16 v[10:13], v[38:41], v[34:37], v[10:13]
	v_mfma_f32_16x16x32_f16 v[18:21], v[42:45], v[34:37], v[18:21]
	s_waitcnt lgkmcnt(0)
	v_mfma_f32_16x16x32_f16 v[22:25], v[46:49], v[26:29], v[22:25]
	v_mfma_f32_16x16x32_f16 v[14:17], v[50:53], v[26:29], v[14:17]
	ds_read_b128 v[26:29], v6 offset:24576
	ds_read_b128 v[34:37], v6 offset:26624
	ds_read_b128 v[38:41], v9 offset:40960
	ds_read_b128 v[42:45], v9 offset:43008
	v_mfma_f32_16x16x32_f16 v[8:11], v[46:49], v[30:33], v[10:13]
	v_mfma_f32_16x16x32_f16 v[18:21], v[50:53], v[30:33], v[18:21]
	s_waitcnt vmcnt(0) lgkmcnt(0)
	s_barrier
	s_waitcnt lgkmcnt(0)
	v_mfma_f32_16x16x32_f16 v[22:25], v[38:41], v[26:29], v[22:25]
	v_mfma_f32_16x16x32_f16 v[12:15], v[42:45], v[26:29], v[14:17]
	ds_read_b128 v[26:29], v5 offset:49152
	ds_read_b128 v[30:33], v5 offset:51200
	ds_read_b128 v[46:49], v7 offset:49152
	ds_read_b128 v[50:53], v7 offset:51200
	v_mfma_f32_16x16x32_f16 v[8:11], v[38:41], v[34:37], v[8:11]
	v_mfma_f32_16x16x32_f16 v[16:19], v[42:45], v[34:37], v[18:21]
	s_waitcnt lgkmcnt(0)
	v_mfma_f32_16x16x32_f16 v[20:23], v[46:49], v[26:29], v[22:25]
	v_mfma_f32_16x16x32_f16 v[12:15], v[50:53], v[26:29], v[12:15]
	s_nop 1
	ds_read_b128 v[24:27], v6 offset:49152
	ds_read_b128 v[4:7], v6 offset:51200
	ds_read_b128 v[34:37], v58
	ds_read_b128 v[38:41], v58 offset:2048
	v_mfma_f32_16x16x32_f16 v[8:11], v[46:49], v[30:33], v[8:11]
	v_mfma_f32_16x16x32_f16 v[16:19], v[50:53], v[30:33], v[16:19]
	s_waitcnt vmcnt(0) lgkmcnt(0)
	s_barrier
	s_waitcnt lgkmcnt(0)
	v_mfma_f32_16x16x32_f16 v[20:23], v[34:37], v[24:27], v[20:23]
	v_mfma_f32_16x16x32_f16 v[12:15], v[38:41], v[24:27], v[12:15]
	ds_read_b128 v[24:27], v59
	ds_read_b128 v[28:31], v60
	ds_read_b128 v[42:45], v61
	ds_read_b128 v[46:49], v62
	v_mfma_f32_16x16x32_f16 v[8:11], v[34:37], v[4:7], v[8:11]
	v_mfma_f32_16x16x32_f16 v[4:7], v[38:41], v[4:7], v[16:19]
	s_waitcnt lgkmcnt(0)
	v_mfma_f32_16x16x32_f16 v[16:19], v[42:45], v[24:27], v[20:23]
	v_mfma_f32_16x16x32_f16 v[12:15], v[46:49], v[24:27], v[12:15]
	s_nop 1
	ds_read_b128 v[20:23], v63
	ds_read_b128 v[24:27], v63 offset:2048
	ds_read_b128 v[32:35], v64
	ds_read_b128 v[36:39], v64 offset:2048
	v_mfma_f32_16x16x32_f16 v[8:11], v[42:45], v[28:31], v[8:11]
	v_mfma_f32_16x16x32_f16 v[4:7], v[46:49], v[28:31], v[4:7]
	s_waitcnt lgkmcnt(0)
	v_mfma_f32_16x16x32_f16 v[16:19], v[32:35], v[20:23], v[16:19]
	v_mfma_f32_16x16x32_f16 v[12:15], v[36:39], v[20:23], v[12:15]
	v_mfma_f32_16x16x32_f16 v[8:11], v[32:35], v[24:27], v[8:11]
	v_mfma_f32_16x16x32_f16 v[4:7], v[36:39], v[24:27], v[4:7]
	v_or_b32_e32 v38, s12, v1
	v_lshlrev_b32_e32 v0, 2, v0
	v_or3_b32 v0, v0, v2, s13
	v_mad_u64_u32 v[2:3], s[0:1], v38, s2, 0
	s_ashr_i32 s3, s2, 31
	v_mov_b32_e32 v20, v3
	v_mad_u64_u32 v[20:21], s[0:1], v38, s3, v[20:21]
	v_mov_b32_e32 v3, v20
	v_mov_b32_e32 v1, 0
	v_lshl_add_u64 v[2:3], v[2:3], 2, s[8:9]
	v_lshlrev_b64 v[32:33], 2, v[0:1]
	v_lshl_add_u64 v[34:35], v[2:3], 0, v[32:33]
	v_lshl_add_u64 v[36:37], s[10:11], 0, v[32:33]
	v_or_b32_e32 v39, 16, v38
	v_mad_u64_u32 v[36:37], s[0:1], v39, s2, 0
	v_mov_b32_e32 v38, v37
	v_mad_u64_u32 v[38:39], s[0:1], v39, s3, v[38:39]
	v_mov_b32_e32 v37, v38
	v_lshl_add_u64 v[36:37], v[36:37], 2, s[8:9]
	v_lshl_add_u64 v[32:33], v[36:37], 0, v[32:33]
	s_waitcnt vmcnt(0)
	v_pk_add_f32 v[2:3], v[18:19], v[82:83]
	v_pk_add_f32 v[0:1], v[16:17], v[80:81]
	v_pk_add_f32 v[14:15], v[14:15], v[86:87]
	v_pk_add_f32 v[12:13], v[12:13], v[84:85]
	v_pk_add_f32 v[2:3], v[90:91], v[2:3]
	v_pk_add_f32 v[0:1], v[88:89], v[0:1]
	v_pk_add_f32 v[14:15], v[94:95], v[14:15]
	v_pk_add_f32 v[12:13], v[92:93], v[12:13]
	global_store_dwordx4 v[34:35], v[0:3], off
	global_store_dwordx4 v[34:35], v[12:15], off offset:64
	v_pk_add_f32 v[42:43], v[10:11], v[98:99]
	v_pk_add_f32 v[40:41], v[8:9], v[96:97]
	v_pk_add_f32 v[6:7], v[6:7], v[102:103]
	v_pk_add_f32 v[4:5], v[4:5], v[100:101]
	v_pk_add_f32 v[42:43], v[90:91], v[42:43]
	v_pk_add_f32 v[40:41], v[88:89], v[40:41]
	v_pk_add_f32 v[6:7], v[94:95], v[6:7]
	v_pk_add_f32 v[4:5], v[92:93], v[4:5]
	global_store_dwordx4 v[32:33], v[40:43], off
	global_store_dwordx4 v[32:33], v[4:7], off offset:64
	s_endpgm
	s_endpgm
	s_endpgm
	s_endpgm
	s_endpgm
	s_endpgm
	s_endpgm
	s_endpgm
	s_endpgm
	s_endpgm
	s_endpgm
	s_endpgm
	s_endpgm
	s_endpgm
	s_endpgm
	s_endpgm
	s_endpgm
	s_endpgm
	s_endpgm
	s_endpgm
	s_endpgm
	s_endpgm
	s_endpgm
	s_endpgm
	s_endpgm
	s_endpgm
	s_endpgm
	s_endpgm
	s_endpgm
	s_endpgm
	s_endpgm
	s_endpgm
	s_endpgm
	s_endpgm
	s_endpgm
	s_endpgm
	s_endpgm
	s_endpgm
	s_endpgm
	s_endpgm
	s_endpgm
	s_endpgm
	s_endpgm
	s_endpgm
	s_endpgm
	s_endpgm
	s_endpgm
	s_endpgm
	s_endpgm
	s_endpgm
	s_endpgm
	s_endpgm
	s_endpgm
	s_endpgm
	s_endpgm
	s_endpgm
	s_endpgm
	s_endpgm
	s_endpgm
	s_endpgm
	s_endpgm
	s_endpgm
	.section	.rodata,"a",@progbits
	.p2align	6, 0x0

_Z5gemm8ILi128ELi2ELi4ELi4ELi2ELi32EEvPKDF16_S1_iiiPDF16_PfPKf:
	v_readfirstlane_b32 s32, v0
	s_nop 3
	s_nop 0
	s_bitcmp1_b32 s32, 8
	s_cbranch_scc0 .Lprio_skip3
	s_setprio 1
.Lprio_skip3:
	s_load_dwordx8 s[4:11], s[0:1], 0x0
	s_lshl_b32 s3, s2, 2
	s_waitcnt lgkmcnt(0)
	s_and_b32 s11, s2, 4
	s_lshr_b32 s12, s2, 6
	s_bfe_u32 s13, s2, 0x30003
	s_add_i32 s11, s11, s12
	s_and_b32 s12, s2, 1
	s_and_b32 s2, s3, 8
	s_or_b32 s2, s2, s13
	s_lshl_b32 s13, s2, 7
	s_lshr_b32 s2, s10, 31
	s_add_i32 s2, s10, s2
	s_ashr_i32 s14, s2, 1
	s_mul_hi_i32 s3, s10, s13
	s_mul_i32 s2, s10, s13
	s_lshl_b32 s11, s11, 7
	s_lshl_b64 s[2:3], s[2:3], 1
	v_lshrrev_b32_e32 v2, 4, v0
	s_add_u32 s15, s4, s2
	s_mul_i32 s2, s14, s12
	v_xor_b32_e32 v1, v2, v0
	v_or_b32_e32 v4, 0x200, v0
	s_addc_u32 s16, s5, s3
	s_ashr_i32 s3, s2, 31
	v_lshlrev_b32_e32 v1, 3, v1
	v_lshrrev_b32_e32 v3, 3, v0
	v_lshrrev_b32_e32 v4, 3, v4
	s_lshl_b64 s[4:5], s[2:3], 1
	v_and_b32_e32 v1, 56, v1
	v_mul_lo_u32 v3, v3, s10
	v_mul_lo_u32 v4, v4, s10
	s_add_u32 s2, s15, s4
	s_mul_hi_i32 s15, s10, s11
	s_mul_i32 s14, s10, s11
	v_lshlrev_b32_e32 v106, 4, v0
	v_add_lshl_u32 v3, v3, v1, 1
	v_add_lshl_u32 v4, v4, v1, 1
	s_addc_u32 s3, s16, s5
	s_lshl_b64 s[14:15], s[14:15], 1
	v_add_u32_e32 v1, 0, v106
	s_add_u32 s6, s6, s14
	v_readfirstlane_b32 s18, v1
	v_add_u32_e32 v5, 0x2000, v1
	s_addc_u32 s7, s7, s15
	s_mov_b32 m0, s18
	v_readfirstlane_b32 s15, v5
	v_add_u32_e32 v5, 0x4000, v1
	s_add_u32 s4, s6, s4
	global_load_lds_dwordx4 v3, s[2:3]
	s_mov_b32 m0, s15
	v_readfirstlane_b32 s16, v5
	v_add_u32_e32 v5, 0x6000, v1
	s_addc_u32 s5, s7, s5
	global_load_lds_dwordx4 v4, s[2:3]
	s_mov_b32 m0, s16
	v_readfirstlane_b32 s17, v5
	v_add_u32_e32 v5, 0x8000, v1
	global_load_lds_dwordx4 v3, s[4:5]
	s_mov_b32 m0, s17
	s_add_u32 s20, s2, 0x80
	v_readfirstlane_b32 s14, v5
	v_add_u32_e32 v5, 0xa000, v1
	global_load_lds_dwordx4 v4, s[4:5]
	s_addc_u32 s21, s3, 0
	s_mov_b32 m0, s14
	v_readfirstlane_b32 s6, v5
	v_add_u32_e32 v5, 0xc000, v1
	s_add_u32 s22, s4, 0x80
	global_load_lds_dwordx4 v3, s[20:21]
	s_mov_b32 m0, s6
	v_readfirstlane_b32 s7, v5
	v_add_u32_e32 v5, 0xe000, v1
	s_addc_u32 s23, s5, 0
	global_load_lds_dwordx4 v4, s[20:21]
	s_mov_b32 m0, s7
	v_readfirstlane_b32 s10, v5
	v_add_u32_e32 v5, 0x10000, v1
	global_load_lds_dwordx4 v3, s[22:23]
	s_mov_b32 m0, s10
	s_add_u32 s20, s2, 0x100
	v_readfirstlane_b32 s19, v5
	v_add_u32_e32 v5, 0x12000, v1
	global_load_lds_dwordx4 v4, s[22:23]
	s_addc_u32 s21, s3, 0
	s_mov_b32 m0, s19
	v_readfirstlane_b32 s19, v5
	v_add_u32_e32 v5, 0x14000, v1
	s_add_u32 s22, s4, 0x100
	global_load_lds_dwordx4 v3, s[20:21]
	s_mov_b32 m0, s19
	v_readfirstlane_b32 s19, v5
	v_add_u32_e32 v5, 0x16000, v1
	s_addc_u32 s23, s5, 0
	global_load_lds_dwordx4 v4, s[20:21]
	s_mov_b32 m0, s19
	v_readfirstlane_b32 s19, v5
	v_add_u32_e32 v5, 0x18000, v1
	global_load_lds_dwordx4 v3, s[22:23]
	s_mov_b32 m0, s19
	s_add_u32 s20, s2, 0x180
	v_readfirstlane_b32 s19, v5
	v_add_u32_e32 v5, 0x1a000, v1
	global_load_lds_dwordx4 v4, s[22:23]
	s_addc_u32 s21, s3, 0
	s_mov_b32 m0, s19
	v_readfirstlane_b32 s19, v5
	v_add_u32_e32 v5, 0x1c000, v1
	s_add_u32 s22, s4, 0x180
	global_load_lds_dwordx4 v3, s[20:21]
	s_mov_b32 m0, s19
	v_readfirstlane_b32 s19, v5
	v_add_u32_e32 v1, 0x1e000, v1
	s_addc_u32 s23, s5, 0
	global_load_lds_dwordx4 v4, s[20:21]
	s_mov_b32 m0, s19
	v_readfirstlane_b32 s19, v1
	global_load_lds_dwordx4 v3, s[22:23]
	s_mov_b32 m0, s19
	v_bfe_u32 v8, v0, 1, 3
	global_load_lds_dwordx4 v4, s[22:23]
	v_lshrrev_b32_e32 v6, 1, v0
	v_bitop3_b32 v2, v2, v8, 3 bitop3:0x6c
	v_and_b32_e32 v5, 15, v0
	v_lshrrev_b32_e32 v1, 2, v0
	v_lshlrev_b32_e32 v7, 4, v2
	v_and_b32_e32 v2, 0x60, v6
	v_and_or_b32 v1, v1, 64, v5
	v_or_b32_e32 v5, v2, v5
	v_lshlrev_b32_e32 v6, 7, v5
	v_lshlrev_b32_e32 v102, 7, v1
	v_add_u32_e32 v9, 0, v6
	v_add_u32_e32 v38, 0, v102
	s_waitcnt vmcnt(12)
	s_barrier
	v_add_u32_e32 v5, v9, v7
	v_add_u32_e32 v7, v38, v7
	ds_read_b128 v[10:13], v5 offset:18432
	ds_read_b128 v[14:17], v5 offset:16384
	ds_read_b128 v[18:21], v7
	ds_read_b128 v[22:25], v7 offset:2048
	ds_read_b128 v[30:33], v7 offset:4096
	ds_read_b128 v[34:37], v7 offset:6144
	s_load_dwordx2 s[0:1], s[0:1], 0x20
	v_bfe_u32 v0, v0, 4, 2
	v_bitop3_b32 v8, v0, v8, 4 bitop3:0x36
	v_or_b32_e32 v103, 0x4000, v6
	s_waitcnt lgkmcnt(0)
	v_mfma_f32_16x16x32_f16 v[26:29], v[14:17], v[18:21], 0
	v_lshlrev_b32_e32 v104, 4, v8
	v_mfma_f32_16x16x32_f16 v[18:21], v[10:13], v[18:21], 0
	v_add_u32_e32 v6, v38, v104
	ds_read_b128 v[38:41], v6
	ds_read_b128 v[42:45], v6 offset:2048
	ds_read_b128 v[46:49], v6 offset:4096
	ds_read_b128 v[50:53], v6 offset:6144
	v_add_u32_e32 v8, v9, v104
	ds_read_b128 v[54:57], v8 offset:16384
	ds_read_b128 v[58:61], v8 offset:18432
	v_mfma_f32_16x16x32_f16 v[62:65], v[14:17], v[22:25], 0
	v_mfma_f32_16x16x32_f16 v[22:25], v[10:13], v[22:25], 0
	v_mfma_f32_16x16x32_f16 v[66:69], v[14:17], v[30:33], 0
	v_mfma_f32_16x16x32_f16 v[30:33], v[10:13], v[30:33], 0
	v_mfma_f32_16x16x32_f16 v[14:17], v[14:17], v[34:37], 0
	v_mfma_f32_16x16x32_f16 v[10:13], v[10:13], v[34:37], 0
	s_add_u32 s20, s2, 0x200
	s_mov_b32 m0, s18
	s_waitcnt vmcnt(8) lgkmcnt(0)
	s_barrier
	s_addc_u32 s21, s3, 0
	s_add_u32 s22, s4, 0x200
	global_load_lds_dwordx4 v3, s[20:21]
	s_mov_b32 m0, s15
	s_addc_u32 s23, s5, 0
	global_load_lds_dwordx4 v4, s[20:21]
	s_mov_b32 m0, s16
	s_nop 0
	global_load_lds_dwordx4 v3, s[22:23]
	s_mov_b32 m0, s17
	s_nop 0
	global_load_lds_dwordx4 v4, s[22:23]
	s_waitcnt lgkmcnt(0)
	v_mfma_f32_16x16x32_f16 v[26:29], v[54:57], v[38:41], v[26:29]
	v_mfma_f32_16x16x32_f16 v[18:21], v[58:61], v[38:41], v[18:21]
	ds_read_b128 v[34:37], v7 offset:32768
	ds_read_b128 v[38:41], v7 offset:34816
	ds_read_b128 v[70:73], v7 offset:36864
	ds_read_b128 v[74:77], v7 offset:38912
	ds_read_b128 v[78:81], v5 offset:49152
	ds_read_b128 v[82:85], v5 offset:51200
	v_mfma_f32_16x16x32_f16 v[62:65], v[54:57], v[42:45], v[62:65]
	v_mfma_f32_16x16x32_f16 v[22:25], v[58:61], v[42:45], v[22:25]
	v_mfma_f32_16x16x32_f16 v[42:45], v[54:57], v[46:49], v[66:69]
	v_mfma_f32_16x16x32_f16 v[30:33], v[58:61], v[46:49], v[30:33]
	v_mfma_f32_16x16x32_f16 v[14:17], v[54:57], v[50:53], v[14:17]
	v_mfma_f32_16x16x32_f16 v[10:13], v[58:61], v[50:53], v[10:13]
	s_waitcnt lgkmcnt(0)
	v_mfma_f32_16x16x32_f16 v[26:29], v[78:81], v[34:37], v[26:29]
	v_mfma_f32_16x16x32_f16 v[18:21], v[82:85], v[34:37], v[18:21]
	ds_read_b128 v[34:37], v6 offset:32768
	ds_read_b128 v[46:49], v6 offset:34816
	ds_read_b128 v[50:53], v6 offset:36864
	ds_read_b128 v[54:57], v6 offset:38912
	ds_read_b128 v[58:61], v8 offset:49152
	ds_read_b128 v[66:69], v8 offset:51200
	v_mfma_f32_16x16x32_f16 v[62:65], v[78:81], v[38:41], v[62:65]
	v_mfma_f32_16x16x32_f16 v[22:25], v[82:85], v[38:41], v[22:25]
	v_mfma_f32_16x16x32_f16 v[38:41], v[78:81], v[70:73], v[42:45]
	v_mfma_f32_16x16x32_f16 v[30:33], v[82:85], v[70:73], v[30:33]
	v_mfma_f32_16x16x32_f16 v[42:45], v[78:81], v[74:77], v[14:17]
	v_mfma_f32_16x16x32_f16 v[70:73], v[82:85], v[74:77], v[10:13]
	s_add_u32 s20, s2, 0x280
	s_mov_b32 m0, s14
	s_waitcnt vmcnt(8) lgkmcnt(0)
	s_barrier
	s_addc_u32 s21, s3, 0
	s_add_u32 s22, s4, 0x280
	global_load_lds_dwordx4 v3, s[20:21]
	s_mov_b32 m0, s6
	s_addc_u32 s23, s5, 0
	global_load_lds_dwordx4 v4, s[20:21]
	s_mov_b32 m0, s7
	s_nop 0
	global_load_lds_dwordx4 v3, s[22:23]
	s_mov_b32 m0, s10
	s_nop 0
	global_load_lds_dwordx4 v4, s[22:23]
	s_waitcnt lgkmcnt(0)
	v_mfma_f32_16x16x32_f16 v[26:29], v[58:61], v[34:37], v[26:29]
	v_mfma_f32_16x16x32_f16 v[16:19], v[66:69], v[34:37], v[18:21]
	v_add_u32_e32 v9, 0x10000, v7
	v_add_u32_e32 v11, 0x11000, v7
	v_add_u32_e32 v13, 0x14000, v5
	v_add_u32_e32 v10, 0x10800, v7
	ds_read_b128 v[34:37], v9
	ds_read_b128 v[74:77], v10
	v_add_u32_e32 v12, 0x11800, v7
	ds_read_b128 v[78:81], v11
	ds_read_b128 v[82:85], v12
	v_add_u32_e32 v14, 0x14800, v5
	ds_read_b128 v[86:89], v13
	ds_read_b128 v[90:93], v14
	v_mfma_f32_16x16x32_f16 v[62:65], v[58:61], v[46:49], v[62:65]
	v_mfma_f32_16x16x32_f16 v[20:23], v[66:69], v[46:49], v[22:25]
	v_mfma_f32_16x16x32_f16 v[38:41], v[58:61], v[50:53], v[38:41]
	v_mfma_f32_16x16x32_f16 v[30:33], v[66:69], v[50:53], v[30:33]
	v_mfma_f32_16x16x32_f16 v[42:45], v[58:61], v[54:57], v[42:45]
	v_mfma_f32_16x16x32_f16 v[46:49], v[66:69], v[54:57], v[70:73]
	s_waitcnt lgkmcnt(0)
	v_mfma_f32_16x16x32_f16 v[24:27], v[86:89], v[34:37], v[26:29]
	v_mfma_f32_16x16x32_f16 v[34:37], v[90:93], v[34:37], v[16:19]
	s_add_i32 s19, 0, 0x10000
	s_nop 1
	v_add_u32_e32 v16, s19, v104
	v_add_u32_e32 v15, v16, v102
	ds_read_b128 v[50:53], v15
	ds_read_b128 v[54:57], v15 offset:2048
	ds_read_b128 v[58:61], v15 offset:4096
	ds_read_b128 v[66:69], v15 offset:6144
	v_add_u32_e32 v16, v16, v103
	ds_read_b128 v[70:73], v16
	ds_read_b128 v[94:97], v16 offset:2048
	v_mfma_f32_16x16x32_f16 v[62:65], v[86:89], v[74:77], v[62:65]
	v_mfma_f32_16x16x32_f16 v[74:77], v[90:93], v[74:77], v[20:23]
	v_mfma_f32_16x16x32_f16 v[38:41], v[86:89], v[78:81], v[38:41]
	v_mfma_f32_16x16x32_f16 v[28:31], v[90:93], v[78:81], v[30:33]
	v_mfma_f32_16x16x32_f16 v[42:45], v[86:89], v[82:85], v[42:45]
	v_mfma_f32_16x16x32_f16 v[46:49], v[90:93], v[82:85], v[46:49]
	v_add_u32_e32 v17, s19, v106
	s_add_u32 s20, s2, 0x300
	v_readfirstlane_b32 s22, v17
	v_add_u32_e32 v18, 0x2000, v17
	s_waitcnt vmcnt(8) lgkmcnt(0)
	s_barrier
	s_addc_u32 s21, s3, 0
	s_mov_b32 m0, s22
	v_readfirstlane_b32 s19, v18
	global_load_lds_dwordx4 v3, s[20:21]
	s_mov_b32 m0, s19
	v_add_u32_e32 v18, 0x4000, v17
	s_add_u32 s24, s4, 0x300
	global_load_lds_dwordx4 v4, s[20:21]
	v_readfirstlane_b32 s20, v18
	v_add_u32_e32 v17, 0x6000, v17
	s_addc_u32 s25, s5, 0
	s_mov_b32 m0, s20
	v_readfirstlane_b32 s21, v17
	global_load_lds_dwordx4 v3, s[24:25]
	s_mov_b32 m0, s21
	s_nop 0
	global_load_lds_dwordx4 v4, s[24:25]
	s_waitcnt lgkmcnt(0)
	v_mfma_f32_16x16x32_f16 v[24:27], v[70:73], v[50:53], v[24:27]
	v_mfma_f32_16x16x32_f16 v[32:35], v[94:97], v[50:53], v[34:37]
	v_add_u32_e32 v17, 0x18000, v7
	v_add_u32_e32 v19, 0x19000, v7
	v_add_u32_e32 v21, 0x1c000, v5
	v_add_u32_e32 v18, 0x18800, v7
	ds_read_b128 v[50:53], v17
	ds_read_b128 v[78:81], v18
	v_add_u32_e32 v20, 0x19800, v7
	ds_read_b128 v[82:85], v19
	ds_read_b128 v[86:89], v20
	v_add_u32_e32 v22, 0x1c800, v5
	ds_read_b128 v[90:93], v21
	ds_read_b128 v[98:101], v22
	v_mfma_f32_16x16x32_f16 v[62:65], v[70:73], v[54:57], v[62:65]
	v_mfma_f32_16x16x32_f16 v[54:57], v[94:97], v[54:57], v[74:77]
	v_mfma_f32_16x16x32_f16 v[36:39], v[70:73], v[58:61], v[38:41]
	v_mfma_f32_16x16x32_f16 v[28:31], v[94:97], v[58:61], v[28:31]
	v_mfma_f32_16x16x32_f16 v[40:43], v[70:73], v[66:69], v[42:45]
	v_mfma_f32_16x16x32_f16 v[44:47], v[94:97], v[66:69], v[46:49]
	s_waitcnt lgkmcnt(0)
	v_mfma_f32_16x16x32_f16 v[58:61], v[90:93], v[50:53], v[24:27]
	v_mfma_f32_16x16x32_f16 v[32:35], v[98:101], v[50:53], v[32:35]
	s_add_i32 s23, 0, 0x18000
	s_nop 0
	v_add_u32_e32 v24, s23, v104
	v_add_u32_e32 v23, v24, v102
	ds_read_b128 v[48:51], v23
	ds_read_b128 v[66:69], v23 offset:2048
	ds_read_b128 v[70:73], v23 offset:4096
	ds_read_b128 v[74:77], v23 offset:6144
	v_add_u32_e32 v24, v24, v103
	ds_read_b128 v[94:97], v24
	ds_read_b128 v[102:105], v24 offset:2048
	v_mfma_f32_16x16x32_f16 v[62:65], v[90:93], v[78:81], v[62:65]
	v_mfma_f32_16x16x32_f16 v[52:55], v[98:101], v[78:81], v[54:57]
	v_mfma_f32_16x16x32_f16 v[36:39], v[90:93], v[82:85], v[36:39]
	v_mfma_f32_16x16x32_f16 v[26:29], v[98:101], v[82:85], v[28:31]
	v_mfma_f32_16x16x32_f16 v[40:43], v[90:93], v[86:89], v[40:43]
	v_mfma_f32_16x16x32_f16 v[44:47], v[98:101], v[86:89], v[44:47]
	v_add_u32_e32 v25, s23, v106
	s_add_u32 s24, s2, 0x380
	v_readfirstlane_b32 s26, v25
	v_add_u32_e32 v30, 0x2000, v25
	s_waitcnt vmcnt(8) lgkmcnt(0)
	s_barrier
	s_addc_u32 s25, s3, 0
	s_mov_b32 m0, s26
	v_readfirstlane_b32 s23, v30
	global_load_lds_dwordx4 v3, s[24:25]
	s_mov_b32 m0, s23
	v_add_u32_e32 v30, 0x4000, v25
	s_add_u32 s28, s4, 0x380
	global_load_lds_dwordx4 v4, s[24:25]
	v_readfirstlane_b32 s24, v30
	v_add_u32_e32 v25, 0x6000, v25
	s_addc_u32 s29, s5, 0
	s_mov_b32 m0, s24
	v_readfirstlane_b32 s25, v25
	global_load_lds_dwordx4 v3, s[28:29]
	s_mov_b32 m0, s25
	s_nop 0
	global_load_lds_dwordx4 v4, s[28:29]
	s_waitcnt lgkmcnt(0)
	v_mfma_f32_16x16x32_f16 v[56:59], v[94:97], v[48:51], v[58:61]
	v_mfma_f32_16x16x32_f16 v[30:33], v[102:105], v[48:51], v[32:35]
	ds_read_b128 v[48:51], v7
	ds_read_b128 v[78:81], v7 offset:2048
	ds_read_b128 v[82:85], v7 offset:4096
	ds_read_b128 v[86:89], v7 offset:6144
	ds_read_b128 v[90:93], v5 offset:16384
	ds_read_b128 v[98:101], v5 offset:18432
	v_mfma_f32_16x16x32_f16 v[60:63], v[94:97], v[66:69], v[62:65]
	v_mfma_f32_16x16x32_f16 v[52:55], v[102:105], v[66:69], v[52:55]
	v_mfma_f32_16x16x32_f16 v[34:37], v[94:97], v[70:73], v[36:39]
	v_mfma_f32_16x16x32_f16 v[26:29], v[102:105], v[70:73], v[26:29]
	v_mfma_f32_16x16x32_f16 v[38:41], v[94:97], v[74:77], v[40:43]
	v_mfma_f32_16x16x32_f16 v[42:45], v[102:105], v[74:77], v[44:47]
	s_waitcnt lgkmcnt(0)
	v_mfma_f32_16x16x32_f16 v[56:59], v[90:93], v[48:51], v[56:59]
	v_mfma_f32_16x16x32_f16 v[30:33], v[98:101], v[48:51], v[30:33]
	ds_read_b128 v[46:49], v6
	ds_read_b128 v[64:67], v6 offset:2048
	ds_read_b128 v[68:71], v6 offset:4096
	ds_read_b128 v[72:75], v6 offset:6144
	ds_read_b128 v[94:97], v8 offset:16384
	ds_read_b128 v[102:105], v8 offset:18432
	v_mfma_f32_16x16x32_f16 v[60:63], v[90:93], v[78:81], v[60:63]
	v_mfma_f32_16x16x32_f16 v[50:53], v[98:101], v[78:81], v[52:55]
	v_mfma_f32_16x16x32_f16 v[34:37], v[90:93], v[82:85], v[34:37]
	v_mfma_f32_16x16x32_f16 v[26:29], v[98:101], v[82:85], v[26:29]
	v_mfma_f32_16x16x32_f16 v[38:41], v[90:93], v[86:89], v[38:41]
	v_mfma_f32_16x16x32_f16 v[42:45], v[98:101], v[86:89], v[42:45]
	s_add_u32 s28, s2, 0x400
	s_mov_b32 m0, s18
	s_waitcnt vmcnt(8) lgkmcnt(0)
	s_barrier
	s_addc_u32 s29, s3, 0
	s_add_u32 s30, s4, 0x400
	global_load_lds_dwordx4 v3, s[28:29]
	s_mov_b32 m0, s15
	s_addc_u32 s31, s5, 0
	global_load_lds_dwordx4 v4, s[28:29]
	s_mov_b32 m0, s16
	s_nop 0
	global_load_lds_dwordx4 v3, s[30:31]
	s_mov_b32 m0, s17
	s_nop 0
	global_load_lds_dwordx4 v4, s[30:31]
	s_waitcnt lgkmcnt(0)
	v_mfma_f32_16x16x32_f16 v[54:57], v[94:97], v[46:49], v[56:59]
	v_mfma_f32_16x16x32_f16 v[30:33], v[102:105], v[46:49], v[30:33]
	ds_read_b128 v[46:49], v7 offset:32768
	ds_read_b128 v[76:79], v7 offset:34816
	ds_read_b128 v[80:83], v7 offset:36864
	ds_read_b128 v[84:87], v7 offset:38912
	ds_read_b128 v[88:91], v5 offset:49152
	ds_read_b128 v[98:101], v5 offset:51200
	v_mfma_f32_16x16x32_f16 v[58:61], v[94:97], v[64:67], v[60:63]
	v_mfma_f32_16x16x32_f16 v[50:53], v[102:105], v[64:67], v[50:53]
	v_mfma_f32_16x16x32_f16 v[34:37], v[94:97], v[68:71], v[34:37]
	v_mfma_f32_16x16x32_f16 v[26:29], v[102:105], v[68:71], v[26:29]
	v_mfma_f32_16x16x32_f16 v[38:41], v[94:97], v[72:75], v[38:41]
	v_mfma_f32_16x16x32_f16 v[42:45], v[102:105], v[72:75], v[42:45]
	s_waitcnt lgkmcnt(0)
	v_mfma_f32_16x16x32_f16 v[54:57], v[88:91], v[46:49], v[54:57]
	v_mfma_f32_16x16x32_f16 v[30:33], v[98:101], v[46:49], v[30:33]
	ds_read_b128 v[46:49], v6 offset:32768
	ds_read_b128 v[62:65], v6 offset:34816
	ds_read_b128 v[66:69], v6 offset:36864
	ds_read_b128 v[70:73], v6 offset:38912
	ds_read_b128 v[92:95], v8 offset:49152
	ds_read_b128 v[102:105], v8 offset:51200
	v_mfma_f32_16x16x32_f16 v[58:61], v[88:91], v[76:79], v[58:61]
	v_mfma_f32_16x16x32_f16 v[50:53], v[98:101], v[76:79], v[50:53]
	v_mfma_f32_16x16x32_f16 v[34:37], v[88:91], v[80:83], v[34:37]
	v_mfma_f32_16x16x32_f16 v[26:29], v[98:101], v[80:83], v[26:29]
	v_mfma_f32_16x16x32_f16 v[38:41], v[88:91], v[84:87], v[38:41]
	v_mfma_f32_16x16x32_f16 v[42:45], v[98:101], v[84:87], v[42:45]
	s_add_u32 s28, s2, 0x480
	s_mov_b32 m0, s14
	s_waitcnt vmcnt(8) lgkmcnt(0)
	s_barrier
	s_addc_u32 s29, s3, 0
	s_add_u32 s30, s4, 0x480
	global_load_lds_dwordx4 v3, s[28:29]
	s_mov_b32 m0, s6
	s_addc_u32 s31, s5, 0
	global_load_lds_dwordx4 v4, s[28:29]
	s_mov_b32 m0, s7
	s_nop 0
	global_load_lds_dwordx4 v3, s[30:31]
	s_mov_b32 m0, s10
	s_nop 0
	global_load_lds_dwordx4 v4, s[30:31]
	s_waitcnt lgkmcnt(0)
	v_mfma_f32_16x16x32_f16 v[54:57], v[92:95], v[46:49], v[54:57]
	v_mfma_f32_16x16x32_f16 v[30:33], v[102:105], v[46:49], v[30:33]
	ds_read_b128 v[46:49], v9
	ds_read_b128 v[74:77], v10
	ds_read_b128 v[78:81], v11
	ds_read_b128 v[82:85], v12
	ds_read_b128 v[86:89], v13
	ds_read_b128 v[96:99], v14
	v_mfma_f32_16x16x32_f16 v[58:61], v[92:95], v[62:65], v[58:61]
	v_mfma_f32_16x16x32_f16 v[50:53], v[102:105], v[62:65], v[50:53]
	v_mfma_f32_16x16x32_f16 v[34:37], v[92:95], v[66:69], v[34:37]
	v_mfma_f32_16x16x32_f16 v[26:29], v[102:105], v[66:69], v[26:29]
	v_mfma_f32_16x16x32_f16 v[38:41], v[92:95], v[70:73], v[38:41]
	v_mfma_f32_16x16x32_f16 v[42:45], v[102:105], v[70:73], v[42:45]
	s_waitcnt lgkmcnt(0)
	v_mfma_f32_16x16x32_f16 v[54:57], v[86:89], v[46:49], v[54:57]
	v_mfma_f32_16x16x32_f16 v[30:33], v[96:99], v[46:49], v[30:33]
	ds_read_b128 v[46:49], v15
	ds_read_b128 v[62:65], v15 offset:2048
	ds_read_b128 v[66:69], v15 offset:4096
	ds_read_b128 v[70:73], v15 offset:6144
	ds_read_b128 v[90:93], v16
	ds_read_b128 v[100:103], v16 offset:2048
	v_mfma_f32_16x16x32_f16 v[58:61], v[86:89], v[74:77], v[58:61]
	v_mfma_f32_16x16x32_f16 v[50:53], v[96:99], v[74:77], v[50:53]
	v_mfma_f32_16x16x32_f16 v[34:37], v[86:89], v[78:81], v[34:37]
	v_mfma_f32_16x16x32_f16 v[26:29], v[96:99], v[78:81], v[26:29]
	v_mfma_f32_16x16x32_f16 v[38:41], v[86:89], v[82:85], v[38:41]
	v_mfma_f32_16x16x32_f16 v[42:45], v[96:99], v[82:85], v[42:45]
	s_add_u32 s28, s2, 0x500
	s_mov_b32 m0, s22
	s_waitcnt vmcnt(8) lgkmcnt(0)
	s_barrier
	s_addc_u32 s29, s3, 0
	s_add_u32 s30, s4, 0x500
	global_load_lds_dwordx4 v3, s[28:29]
	s_mov_b32 m0, s19
	s_addc_u32 s31, s5, 0
	global_load_lds_dwordx4 v4, s[28:29]
	s_mov_b32 m0, s20
	s_nop 0
	global_load_lds_dwordx4 v3, s[30:31]
	s_mov_b32 m0, s21
	s_nop 0
	global_load_lds_dwordx4 v4, s[30:31]
	s_waitcnt lgkmcnt(0)
	v_mfma_f32_16x16x32_f16 v[54:57], v[90:93], v[46:49], v[54:57]
	v_mfma_f32_16x16x32_f16 v[30:33], v[100:103], v[46:49], v[30:33]
	ds_read_b128 v[46:49], v17
	ds_read_b128 v[74:77], v18
	ds_read_b128 v[78:81], v19
	ds_read_b128 v[82:85], v20
	ds_read_b128 v[86:89], v21
	ds_read_b128 v[94:97], v22
	v_mfma_f32_16x16x32_f16 v[58:61], v[90:93], v[62:65], v[58:61]
	v_mfma_f32_16x16x32_f16 v[50:53], v[100:103], v[62:65], v[50:53]
	v_mfma_f32_16x16x32_f16 v[34:37], v[90:93], v[66:69], v[34:37]
	v_mfma_f32_16x16x32_f16 v[26:29], v[100:103], v[66:69], v[26:29]
	v_mfma_f32_16x16x32_f16 v[38:41], v[90:93], v[70:73], v[38:41]
	v_mfma_f32_16x16x32_f16 v[42:45], v[100:103], v[70:73], v[42:45]
	s_waitcnt lgkmcnt(0)
	v_mfma_f32_16x16x32_f16 v[54:57], v[86:89], v[46:49], v[54:57]
	v_mfma_f32_16x16x32_f16 v[30:33], v[94:97], v[46:49], v[30:33]
	ds_read_b128 v[46:49], v23
	ds_read_b128 v[62:65], v23 offset:2048
	ds_read_b128 v[66:69], v23 offset:4096
	ds_read_b128 v[70:73], v23 offset:6144
	ds_read_b128 v[90:93], v24
	ds_read_b128 v[98:101], v24 offset:2048
	v_mfma_f32_16x16x32_f16 v[58:61], v[86:89], v[74:77], v[58:61]
	v_mfma_f32_16x16x32_f16 v[50:53], v[94:97], v[74:77], v[50:53]
	v_mfma_f32_16x16x32_f16 v[34:37], v[86:89], v[78:81], v[34:37]
	v_mfma_f32_16x16x32_f16 v[26:29], v[94:97], v[78:81], v[26:29]
	v_mfma_f32_16x16x32_f16 v[38:41], v[86:89], v[82:85], v[38:41]
	v_mfma_f32_16x16x32_f16 v[42:45], v[94:97], v[82:85], v[42:45]
	s_add_u32 s28, s2, 0x580
	s_mov_b32 m0, s26
	s_waitcnt vmcnt(8) lgkmcnt(0)
	s_barrier
	s_addc_u32 s29, s3, 0
	s_add_u32 s30, s4, 0x580
	global_load_lds_dwordx4 v3, s[28:29]
	s_mov_b32 m0, s23
	s_addc_u32 s31, s5, 0
	global_load_lds_dwordx4 v4, s[28:29]
	s_mov_b32 m0, s24
	s_nop 0
	global_load_lds_dwordx4 v3, s[30:31]
	s_mov_b32 m0, s25
	s_nop 0
	global_load_lds_dwordx4 v4, s[30:31]
	s_waitcnt lgkmcnt(0)
	v_mfma_f32_16x16x32_f16 v[54:57], v[90:93], v[46:49], v[54:57]
	v_mfma_f32_16x16x32_f16 v[30:33], v[98:101], v[46:49], v[30:33]
	ds_read_b128 v[46:49], v7
	ds_read_b128 v[74:77], v7 offset:2048
	ds_read_b128 v[78:81], v7 offset:4096
	ds_read_b128 v[82:85], v7 offset:6144
	ds_read_b128 v[86:89], v5 offset:16384
	ds_read_b128 v[94:97], v5 offset:18432
	v_mfma_f32_16x16x32_f16 v[58:61], v[90:93], v[62:65], v[58:61]
	v_mfma_f32_16x16x32_f16 v[50:53], v[98:101], v[62:65], v[50:53]
	v_mfma_f32_16x16x32_f16 v[34:37], v[90:93], v[66:69], v[34:37]
	v_mfma_f32_16x16x32_f16 v[26:29], v[98:101], v[66:69], v[26:29]
	v_mfma_f32_16x16x32_f16 v[38:41], v[90:93], v[70:73], v[38:41]
	v_mfma_f32_16x16x32_f16 v[42:45], v[98:101], v[70:73], v[42:45]
	s_waitcnt lgkmcnt(0)
	v_mfma_f32_16x16x32_f16 v[54:57], v[86:89], v[46:49], v[54:57]
	v_mfma_f32_16x16x32_f16 v[30:33], v[94:97], v[46:49], v[30:33]
	ds_read_b128 v[46:49], v6
	ds_read_b128 v[62:65], v6 offset:2048
	ds_read_b128 v[66:69], v6 offset:4096
	ds_read_b128 v[70:73], v6 offset:6144
	ds_read_b128 v[90:93], v8 offset:16384
	ds_read_b128 v[98:101], v8 offset:18432
	v_mfma_f32_16x16x32_f16 v[58:61], v[86:89], v[74:77], v[58:61]
	v_mfma_f32_16x16x32_f16 v[50:53], v[94:97], v[74:77], v[50:53]
	v_mfma_f32_16x16x32_f16 v[34:37], v[86:89], v[78:81], v[34:37]
	v_mfma_f32_16x16x32_f16 v[26:29], v[94:97], v[78:81], v[26:29]
	v_mfma_f32_16x16x32_f16 v[38:41], v[86:89], v[82:85], v[38:41]
	v_mfma_f32_16x16x32_f16 v[42:45], v[94:97], v[82:85], v[42:45]
	s_add_u32 s28, s2, 0x600
	s_mov_b32 m0, s18
	s_waitcnt vmcnt(8) lgkmcnt(0)
	s_barrier
	s_addc_u32 s29, s3, 0
	s_add_u32 s30, s4, 0x600
	global_load_lds_dwordx4 v3, s[28:29]
	s_mov_b32 m0, s15
	s_addc_u32 s31, s5, 0
	global_load_lds_dwordx4 v4, s[28:29]
	s_mov_b32 m0, s16
	s_nop 0
	global_load_lds_dwordx4 v3, s[30:31]
	s_mov_b32 m0, s17
	s_nop 0
	global_load_lds_dwordx4 v4, s[30:31]
	s_waitcnt lgkmcnt(0)
	v_mfma_f32_16x16x32_f16 v[54:57], v[90:93], v[46:49], v[54:57]
	v_mfma_f32_16x16x32_f16 v[30:33], v[98:101], v[46:49], v[30:33]
	ds_read_b128 v[46:49], v7 offset:32768
	ds_read_b128 v[74:77], v7 offset:34816
	ds_read_b128 v[78:81], v7 offset:36864
	ds_read_b128 v[82:85], v7 offset:38912
	ds_read_b128 v[86:89], v5 offset:49152
	ds_read_b128 v[94:97], v5 offset:51200
	v_mfma_f32_16x16x32_f16 v[58:61], v[90:93], v[62:65], v[58:61]
	v_mfma_f32_16x16x32_f16 v[50:53], v[98:101], v[62:65], v[50:53]
	v_mfma_f32_16x16x32_f16 v[34:37], v[90:93], v[66:69], v[34:37]
	v_mfma_f32_16x16x32_f16 v[26:29], v[98:101], v[66:69], v[26:29]
	v_mfma_f32_16x16x32_f16 v[38:41], v[90:93], v[70:73], v[38:41]
	v_mfma_f32_16x16x32_f16 v[42:45], v[98:101], v[70:73], v[42:45]
	s_waitcnt lgkmcnt(0)
	v_mfma_f32_16x16x32_f16 v[54:57], v[86:89], v[46:49], v[54:57]
	v_mfma_f32_16x16x32_f16 v[30:33], v[94:97], v[46:49], v[30:33]
	ds_read_b128 v[46:49], v6 offset:32768
	ds_read_b128 v[62:65], v6 offset:34816
	ds_read_b128 v[66:69], v6 offset:36864
	ds_read_b128 v[70:73], v6 offset:38912
	ds_read_b128 v[90:93], v8 offset:49152
	ds_read_b128 v[98:101], v8 offset:51200
	v_mfma_f32_16x16x32_f16 v[58:61], v[86:89], v[74:77], v[58:61]
	v_mfma_f32_16x16x32_f16 v[50:53], v[94:97], v[74:77], v[50:53]
	v_mfma_f32_16x16x32_f16 v[34:37], v[86:89], v[78:81], v[34:37]
	v_mfma_f32_16x16x32_f16 v[26:29], v[94:97], v[78:81], v[26:29]
	v_mfma_f32_16x16x32_f16 v[38:41], v[86:89], v[82:85], v[38:41]
	v_mfma_f32_16x16x32_f16 v[42:45], v[94:97], v[82:85], v[42:45]
	s_add_u32 s28, s2, 0x680
	s_mov_b32 m0, s14
	s_waitcnt vmcnt(8) lgkmcnt(0)
	s_barrier
	s_addc_u32 s29, s3, 0
	s_add_u32 s30, s4, 0x680
	global_load_lds_dwordx4 v3, s[28:29]
	s_mov_b32 m0, s6
	s_addc_u32 s31, s5, 0
	global_load_lds_dwordx4 v4, s[28:29]
	s_mov_b32 m0, s7
	s_nop 0
	global_load_lds_dwordx4 v3, s[30:31]
	s_mov_b32 m0, s10
	s_nop 0
	global_load_lds_dwordx4 v4, s[30:31]
	s_waitcnt lgkmcnt(0)
	v_mfma_f32_16x16x32_f16 v[54:57], v[90:93], v[46:49], v[54:57]
	v_mfma_f32_16x16x32_f16 v[30:33], v[98:101], v[46:49], v[30:33]
	ds_read_b128 v[46:49], v9
	ds_read_b128 v[74:77], v10
	ds_read_b128 v[78:81], v11
	ds_read_b128 v[82:85], v12
	ds_read_b128 v[86:89], v13
	ds_read_b128 v[94:97], v14
	v_mfma_f32_16x16x32_f16 v[58:61], v[90:93], v[62:65], v[58:61]
	v_mfma_f32_16x16x32_f16 v[50:53], v[98:101], v[62:65], v[50:53]
	v_mfma_f32_16x16x32_f16 v[34:37], v[90:93], v[66:69], v[34:37]
	v_mfma_f32_16x16x32_f16 v[26:29], v[98:101], v[66:69], v[26:29]
	v_mfma_f32_16x16x32_f16 v[38:41], v[90:93], v[70:73], v[38:41]
	v_mfma_f32_16x16x32_f16 v[42:45], v[98:101], v[70:73], v[42:45]
	s_waitcnt lgkmcnt(0)
	v_mfma_f32_16x16x32_f16 v[54:57], v[86:89], v[46:49], v[54:57]
	v_mfma_f32_16x16x32_f16 v[30:33], v[94:97], v[46:49], v[30:33]
	ds_read_b128 v[46:49], v15
	ds_read_b128 v[62:65], v15 offset:2048
	ds_read_b128 v[66:69], v15 offset:4096
	ds_read_b128 v[70:73], v15 offset:6144
	ds_read_b128 v[90:93], v16
	ds_read_b128 v[98:101], v16 offset:2048
	v_mfma_f32_16x16x32_f16 v[58:61], v[86:89], v[74:77], v[58:61]
	v_mfma_f32_16x16x32_f16 v[50:53], v[94:97], v[74:77], v[50:53]
	v_mfma_f32_16x16x32_f16 v[34:37], v[86:89], v[78:81], v[34:37]
	v_mfma_f32_16x16x32_f16 v[26:29], v[94:97], v[78:81], v[26:29]
	v_mfma_f32_16x16x32_f16 v[38:41], v[86:89], v[82:85], v[38:41]
	v_mfma_f32_16x16x32_f16 v[42:45], v[94:97], v[82:85], v[42:45]
	s_add_u32 s28, s2, 0x700
	s_mov_b32 m0, s22
	s_waitcnt vmcnt(8) lgkmcnt(0)
	s_barrier
	s_addc_u32 s29, s3, 0
	s_add_u32 s30, s4, 0x700
	global_load_lds_dwordx4 v3, s[28:29]
	s_mov_b32 m0, s19
	s_addc_u32 s31, s5, 0
	global_load_lds_dwordx4 v4, s[28:29]
	s_mov_b32 m0, s20
	s_nop 0
	global_load_lds_dwordx4 v3, s[30:31]
	s_mov_b32 m0, s21
	s_nop 0
	global_load_lds_dwordx4 v4, s[30:31]
	s_waitcnt lgkmcnt(0)
	v_mfma_f32_16x16x32_f16 v[54:57], v[90:93], v[46:49], v[54:57]
	v_mfma_f32_16x16x32_f16 v[30:33], v[98:101], v[46:49], v[30:33]
	ds_read_b128 v[46:49], v17
	ds_read_b128 v[74:77], v18
	ds_read_b128 v[78:81], v19
	ds_read_b128 v[82:85], v20
	ds_read_b128 v[86:89], v21
	ds_read_b128 v[94:97], v22
	v_mfma_f32_16x16x32_f16 v[58:61], v[90:93], v[62:65], v[58:61]
	v_mfma_f32_16x16x32_f16 v[50:53], v[98:101], v[62:65], v[50:53]
	v_mfma_f32_16x16x32_f16 v[34:37], v[90:93], v[66:69], v[34:37]
	v_mfma_f32_16x16x32_f16 v[26:29], v[98:101], v[66:69], v[26:29]
	v_mfma_f32_16x16x32_f16 v[38:41], v[90:93], v[70:73], v[38:41]
	v_mfma_f32_16x16x32_f16 v[42:45], v[98:101], v[70:73], v[42:45]
	s_waitcnt lgkmcnt(0)
	v_mfma_f32_16x16x32_f16 v[54:57], v[86:89], v[46:49], v[54:57]
	v_mfma_f32_16x16x32_f16 v[30:33], v[94:97], v[46:49], v[30:33]
	ds_read_b128 v[46:49], v23
	ds_read_b128 v[62:65], v23 offset:2048
	ds_read_b128 v[66:69], v23 offset:4096
	ds_read_b128 v[70:73], v23 offset:6144
	ds_read_b128 v[90:93], v24
	ds_read_b128 v[98:101], v24 offset:2048
	v_mfma_f32_16x16x32_f16 v[58:61], v[86:89], v[74:77], v[58:61]
	v_mfma_f32_16x16x32_f16 v[50:53], v[94:97], v[74:77], v[50:53]
	v_mfma_f32_16x16x32_f16 v[34:37], v[86:89], v[78:81], v[34:37]
	v_mfma_f32_16x16x32_f16 v[26:29], v[94:97], v[78:81], v[26:29]
	v_mfma_f32_16x16x32_f16 v[38:41], v[86:89], v[82:85], v[38:41]
	v_mfma_f32_16x16x32_f16 v[42:45], v[94:97], v[82:85], v[42:45]
	s_add_u32 s28, s2, 0x780
	s_mov_b32 m0, s26
	s_waitcnt vmcnt(8) lgkmcnt(0)
	s_barrier
	s_addc_u32 s29, s3, 0
	s_add_u32 s30, s4, 0x780
	global_load_lds_dwordx4 v3, s[28:29]
	s_mov_b32 m0, s23
	s_addc_u32 s31, s5, 0
	global_load_lds_dwordx4 v4, s[28:29]
	s_mov_b32 m0, s24
	s_nop 0
	global_load_lds_dwordx4 v3, s[30:31]
	s_mov_b32 m0, s25
	s_nop 0
	global_load_lds_dwordx4 v4, s[30:31]
	s_waitcnt lgkmcnt(0)
	v_mfma_f32_16x16x32_f16 v[54:57], v[90:93], v[46:49], v[54:57]
	v_mfma_f32_16x16x32_f16 v[30:33], v[98:101], v[46:49], v[30:33]
	ds_read_b128 v[46:49], v7
	ds_read_b128 v[74:77], v7 offset:2048
	ds_read_b128 v[78:81], v7 offset:4096
	ds_read_b128 v[82:85], v7 offset:6144
	ds_read_b128 v[86:89], v5 offset:16384
	ds_read_b128 v[94:97], v5 offset:18432
	v_mfma_f32_16x16x32_f16 v[58:61], v[90:93], v[62:65], v[58:61]
	v_mfma_f32_16x16x32_f16 v[50:53], v[98:101], v[62:65], v[50:53]
	v_mfma_f32_16x16x32_f16 v[34:37], v[90:93], v[66:69], v[34:37]
	v_mfma_f32_16x16x32_f16 v[26:29], v[98:101], v[66:69], v[26:29]
	v_mfma_f32_16x16x32_f16 v[38:41], v[90:93], v[70:73], v[38:41]
	v_mfma_f32_16x16x32_f16 v[42:45], v[98:101], v[70:73], v[42:45]
	s_waitcnt lgkmcnt(0)
	v_mfma_f32_16x16x32_f16 v[54:57], v[86:89], v[46:49], v[54:57]
	v_mfma_f32_16x16x32_f16 v[30:33], v[94:97], v[46:49], v[30:33]
	ds_read_b128 v[46:49], v6
	ds_read_b128 v[62:65], v6 offset:2048
	ds_read_b128 v[66:69], v6 offset:4096
	ds_read_b128 v[70:73], v6 offset:6144
	ds_read_b128 v[90:93], v8 offset:16384
	ds_read_b128 v[98:101], v8 offset:18432
	v_mfma_f32_16x16x32_f16 v[58:61], v[86:89], v[74:77], v[58:61]
	v_mfma_f32_16x16x32_f16 v[50:53], v[94:97], v[74:77], v[50:53]
	v_mfma_f32_16x16x32_f16 v[34:37], v[86:89], v[78:81], v[34:37]
	v_mfma_f32_16x16x32_f16 v[26:29], v[94:97], v[78:81], v[26:29]
	v_mfma_f32_16x16x32_f16 v[38:41], v[86:89], v[82:85], v[38:41]
	v_mfma_f32_16x16x32_f16 v[42:45], v[94:97], v[82:85], v[42:45]
	s_add_u32 s28, s2, 0x800
	s_mov_b32 m0, s18
	s_waitcnt vmcnt(8) lgkmcnt(0)
	s_barrier
	s_addc_u32 s29, s3, 0
	s_add_u32 s30, s4, 0x800
	global_load_lds_dwordx4 v3, s[28:29]
	s_mov_b32 m0, s15
	s_addc_u32 s31, s5, 0
	global_load_lds_dwordx4 v4, s[28:29]
	s_mov_b32 m0, s16
	s_nop 0
	global_load_lds_dwordx4 v3, s[30:31]
	s_mov_b32 m0, s17
	s_nop 0
	global_load_lds_dwordx4 v4, s[30:31]
	s_waitcnt lgkmcnt(0)
	v_mfma_f32_16x16x32_f16 v[54:57], v[90:93], v[46:49], v[54:57]
	v_mfma_f32_16x16x32_f16 v[30:33], v[98:101], v[46:49], v[30:33]
	ds_read_b128 v[46:49], v7 offset:32768
	ds_read_b128 v[74:77], v7 offset:34816
	ds_read_b128 v[78:81], v7 offset:36864
	ds_read_b128 v[82:85], v7 offset:38912
	ds_read_b128 v[86:89], v5 offset:49152
	ds_read_b128 v[94:97], v5 offset:51200
	v_mfma_f32_16x16x32_f16 v[58:61], v[90:93], v[62:65], v[58:61]
	v_mfma_f32_16x16x32_f16 v[50:53], v[98:101], v[62:65], v[50:53]
	v_mfma_f32_16x16x32_f16 v[34:37], v[90:93], v[66:69], v[34:37]
	v_mfma_f32_16x16x32_f16 v[26:29], v[98:101], v[66:69], v[26:29]
	v_mfma_f32_16x16x32_f16 v[38:41], v[90:93], v[70:73], v[38:41]
	v_mfma_f32_16x16x32_f16 v[42:45], v[98:101], v[70:73], v[42:45]
	s_waitcnt lgkmcnt(0)
	v_mfma_f32_16x16x32_f16 v[54:57], v[86:89], v[46:49], v[54:57]
	v_mfma_f32_16x16x32_f16 v[30:33], v[94:97], v[46:49], v[30:33]
	ds_read_b128 v[46:49], v6 offset:32768
	ds_read_b128 v[62:65], v6 offset:34816
	ds_read_b128 v[66:69], v6 offset:36864
	ds_read_b128 v[70:73], v6 offset:38912
	ds_read_b128 v[90:93], v8 offset:49152
	ds_read_b128 v[98:101], v8 offset:51200
	v_mfma_f32_16x16x32_f16 v[58:61], v[86:89], v[74:77], v[58:61]
	v_mfma_f32_16x16x32_f16 v[50:53], v[94:97], v[74:77], v[50:53]
	v_mfma_f32_16x16x32_f16 v[34:37], v[86:89], v[78:81], v[34:37]
	v_mfma_f32_16x16x32_f16 v[26:29], v[94:97], v[78:81], v[26:29]
	v_mfma_f32_16x16x32_f16 v[38:41], v[86:89], v[82:85], v[38:41]
	v_mfma_f32_16x16x32_f16 v[42:45], v[94:97], v[82:85], v[42:45]
	s_add_u32 s28, s2, 0x880
	s_mov_b32 m0, s14
	s_waitcnt vmcnt(8) lgkmcnt(0)
	s_barrier
	s_addc_u32 s29, s3, 0
	s_add_u32 s30, s4, 0x880
	global_load_lds_dwordx4 v3, s[28:29]
	s_mov_b32 m0, s6
	s_addc_u32 s31, s5, 0
	global_load_lds_dwordx4 v4, s[28:29]
	s_mov_b32 m0, s7
	s_nop 0
	global_load_lds_dwordx4 v3, s[30:31]
	s_mov_b32 m0, s10
	s_nop 0
	global_load_lds_dwordx4 v4, s[30:31]
	s_waitcnt lgkmcnt(0)
	v_mfma_f32_16x16x32_f16 v[54:57], v[90:93], v[46:49], v[54:57]
	v_mfma_f32_16x16x32_f16 v[30:33], v[98:101], v[46:49], v[30:33]
	ds_read_b128 v[46:49], v9
	ds_read_b128 v[74:77], v10
	ds_read_b128 v[78:81], v11
	ds_read_b128 v[82:85], v12
	ds_read_b128 v[86:89], v13
	ds_read_b128 v[94:97], v14
	v_mfma_f32_16x16x32_f16 v[58:61], v[90:93], v[62:65], v[58:61]
	v_mfma_f32_16x16x32_f16 v[50:53], v[98:101], v[62:65], v[50:53]
	v_mfma_f32_16x16x32_f16 v[34:37], v[90:93], v[66:69], v[34:37]
	v_mfma_f32_16x16x32_f16 v[26:29], v[98:101], v[66:69], v[26:29]
	v_mfma_f32_16x16x32_f16 v[38:41], v[90:93], v[70:73], v[38:41]
	v_mfma_f32_16x16x32_f16 v[42:45], v[98:101], v[70:73], v[42:45]
	s_waitcnt lgkmcnt(0)
	v_mfma_f32_16x16x32_f16 v[54:57], v[86:89], v[46:49], v[54:57]
	v_mfma_f32_16x16x32_f16 v[30:33], v[94:97], v[46:49], v[30:33]
	ds_read_b128 v[46:49], v15
	ds_read_b128 v[62:65], v15 offset:2048
	ds_read_b128 v[66:69], v15 offset:4096
	ds_read_b128 v[70:73], v15 offset:6144
	ds_read_b128 v[90:93], v16
	ds_read_b128 v[98:101], v16 offset:2048
	v_mfma_f32_16x16x32_f16 v[58:61], v[86:89], v[74:77], v[58:61]
	v_mfma_f32_16x16x32_f16 v[50:53], v[94:97], v[74:77], v[50:53]
	v_mfma_f32_16x16x32_f16 v[34:37], v[86:89], v[78:81], v[34:37]
	v_mfma_f32_16x16x32_f16 v[26:29], v[94:97], v[78:81], v[26:29]
	v_mfma_f32_16x16x32_f16 v[38:41], v[86:89], v[82:85], v[38:41]
	v_mfma_f32_16x16x32_f16 v[42:45], v[94:97], v[82:85], v[42:45]
	s_add_u32 s28, s2, 0x900
	s_mov_b32 m0, s22
	s_waitcnt vmcnt(8) lgkmcnt(0)
	s_barrier
	s_addc_u32 s29, s3, 0
	s_add_u32 s30, s4, 0x900
	global_load_lds_dwordx4 v3, s[28:29]
	s_mov_b32 m0, s19
	s_addc_u32 s31, s5, 0
	global_load_lds_dwordx4 v4, s[28:29]
	s_mov_b32 m0, s20
	s_nop 0
	global_load_lds_dwordx4 v3, s[30:31]
	s_mov_b32 m0, s21
	s_nop 0
	global_load_lds_dwordx4 v4, s[30:31]
	s_waitcnt lgkmcnt(0)
	v_mfma_f32_16x16x32_f16 v[54:57], v[90:93], v[46:49], v[54:57]
	v_mfma_f32_16x16x32_f16 v[30:33], v[98:101], v[46:49], v[30:33]
	ds_read_b128 v[46:49], v17
	ds_read_b128 v[74:77], v18
	ds_read_b128 v[78:81], v19
	ds_read_b128 v[82:85], v20
	ds_read_b128 v[86:89], v21
	ds_read_b128 v[94:97], v22
	v_mfma_f32_16x16x32_f16 v[58:61], v[90:93], v[62:65], v[58:61]
	v_mfma_f32_16x16x32_f16 v[50:53], v[98:101], v[62:65], v[50:53]
	v_mfma_f32_16x16x32_f16 v[34:37], v[90:93], v[66:69], v[34:37]
	v_mfma_f32_16x16x32_f16 v[26:29], v[98:101], v[66:69], v[26:29]
	v_mfma_f32_16x16x32_f16 v[38:41], v[90:93], v[70:73], v[38:41]
	v_mfma_f32_16x16x32_f16 v[42:45], v[98:101], v[70:73], v[42:45]
	s_waitcnt lgkmcnt(0)
	v_mfma_f32_16x16x32_f16 v[54:57], v[86:89], v[46:49], v[54:57]
	v_mfma_f32_16x16x32_f16 v[30:33], v[94:97], v[46:49], v[30:33]
	ds_read_b128 v[46:49], v23
	ds_read_b128 v[62:65], v23 offset:2048
	ds_read_b128 v[66:69], v23 offset:4096
	ds_read_b128 v[70:73], v23 offset:6144
	ds_read_b128 v[90:93], v24
	ds_read_b128 v[98:101], v24 offset:2048
	v_mfma_f32_16x16x32_f16 v[58:61], v[86:89], v[74:77], v[58:61]
	v_mfma_f32_16x16x32_f16 v[50:53], v[94:97], v[74:77], v[50:53]
	v_mfma_f32_16x16x32_f16 v[34:37], v[86:89], v[78:81], v[34:37]
	v_mfma_f32_16x16x32_f16 v[26:29], v[94:97], v[78:81], v[26:29]
	v_mfma_f32_16x16x32_f16 v[38:41], v[86:89], v[82:85], v[38:41]
	v_mfma_f32_16x16x32_f16 v[42:45], v[94:97], v[82:85], v[42:45]
	s_add_u32 s28, s2, 0x980
	s_mov_b32 m0, s26
	s_waitcnt vmcnt(8) lgkmcnt(0)
	s_barrier
	s_addc_u32 s29, s3, 0
	s_add_u32 s30, s4, 0x980
	global_load_lds_dwordx4 v3, s[28:29]
	s_mov_b32 m0, s23
	s_addc_u32 s31, s5, 0
	global_load_lds_dwordx4 v4, s[28:29]
	s_mov_b32 m0, s24
	s_nop 0
	global_load_lds_dwordx4 v3, s[30:31]
	s_mov_b32 m0, s25
	s_nop 0
	global_load_lds_dwordx4 v4, s[30:31]
	s_waitcnt lgkmcnt(0)
	v_mfma_f32_16x16x32_f16 v[54:57], v[90:93], v[46:49], v[54:57]
	v_mfma_f32_16x16x32_f16 v[30:33], v[98:101], v[46:49], v[30:33]
	ds_read_b128 v[46:49], v7
	ds_read_b128 v[74:77], v7 offset:2048
	ds_read_b128 v[78:81], v7 offset:4096
	ds_read_b128 v[82:85], v7 offset:6144
	ds_read_b128 v[86:89], v5 offset:16384
	ds_read_b128 v[94:97], v5 offset:18432
	v_mfma_f32_16x16x32_f16 v[58:61], v[90:93], v[62:65], v[58:61]
	v_mfma_f32_16x16x32_f16 v[50:53], v[98:101], v[62:65], v[50:53]
	v_mfma_f32_16x16x32_f16 v[34:37], v[90:93], v[66:69], v[34:37]
	v_mfma_f32_16x16x32_f16 v[26:29], v[98:101], v[66:69], v[26:29]
	v_mfma_f32_16x16x32_f16 v[38:41], v[90:93], v[70:73], v[38:41]
	v_mfma_f32_16x16x32_f16 v[42:45], v[98:101], v[70:73], v[42:45]
	s_waitcnt lgkmcnt(0)
	v_mfma_f32_16x16x32_f16 v[54:57], v[86:89], v[46:49], v[54:57]
	v_mfma_f32_16x16x32_f16 v[30:33], v[94:97], v[46:49], v[30:33]
	ds_read_b128 v[46:49], v6
	ds_read_b128 v[62:65], v6 offset:2048
	ds_read_b128 v[66:69], v6 offset:4096
	ds_read_b128 v[70:73], v6 offset:6144
	ds_read_b128 v[90:93], v8 offset:16384
	ds_read_b128 v[98:101], v8 offset:18432
	v_mfma_f32_16x16x32_f16 v[58:61], v[86:89], v[74:77], v[58:61]
	v_mfma_f32_16x16x32_f16 v[50:53], v[94:97], v[74:77], v[50:53]
	v_mfma_f32_16x16x32_f16 v[34:37], v[86:89], v[78:81], v[34:37]
	v_mfma_f32_16x16x32_f16 v[26:29], v[94:97], v[78:81], v[26:29]
	v_mfma_f32_16x16x32_f16 v[38:41], v[86:89], v[82:85], v[38:41]
	v_mfma_f32_16x16x32_f16 v[42:45], v[94:97], v[82:85], v[42:45]
	s_add_u32 s28, s2, 0xa00
	s_mov_b32 m0, s18
	s_waitcnt vmcnt(8) lgkmcnt(0)
	s_barrier
	s_addc_u32 s29, s3, 0
	s_add_u32 s30, s4, 0xa00
	global_load_lds_dwordx4 v3, s[28:29]
	s_mov_b32 m0, s15
	s_addc_u32 s31, s5, 0
	global_load_lds_dwordx4 v4, s[28:29]
	s_mov_b32 m0, s16
	s_nop 0
	global_load_lds_dwordx4 v3, s[30:31]
	s_mov_b32 m0, s17
	s_nop 0
	global_load_lds_dwordx4 v4, s[30:31]
	s_waitcnt lgkmcnt(0)
	v_mfma_f32_16x16x32_f16 v[54:57], v[90:93], v[46:49], v[54:57]
	v_mfma_f32_16x16x32_f16 v[30:33], v[98:101], v[46:49], v[30:33]
	ds_read_b128 v[46:49], v7 offset:32768
	ds_read_b128 v[74:77], v7 offset:34816
	ds_read_b128 v[78:81], v7 offset:36864
	ds_read_b128 v[82:85], v7 offset:38912
	ds_read_b128 v[86:89], v5 offset:49152
	ds_read_b128 v[94:97], v5 offset:51200
	v_mfma_f32_16x16x32_f16 v[58:61], v[90:93], v[62:65], v[58:61]
	v_mfma_f32_16x16x32_f16 v[50:53], v[98:101], v[62:65], v[50:53]
	v_mfma_f32_16x16x32_f16 v[34:37], v[90:93], v[66:69], v[34:37]
	v_mfma_f32_16x16x32_f16 v[26:29], v[98:101], v[66:69], v[26:29]
	v_mfma_f32_16x16x32_f16 v[38:41], v[90:93], v[70:73], v[38:41]
	v_mfma_f32_16x16x32_f16 v[42:45], v[98:101], v[70:73], v[42:45]
	s_waitcnt lgkmcnt(0)
	v_mfma_f32_16x16x32_f16 v[54:57], v[86:89], v[46:49], v[54:57]
	v_mfma_f32_16x16x32_f16 v[30:33], v[94:97], v[46:49], v[30:33]
	ds_read_b128 v[46:49], v6 offset:32768
	ds_read_b128 v[62:65], v6 offset:34816
	ds_read_b128 v[66:69], v6 offset:36864
	ds_read_b128 v[70:73], v6 offset:38912
	ds_read_b128 v[90:93], v8 offset:49152
	ds_read_b128 v[98:101], v8 offset:51200
	v_mfma_f32_16x16x32_f16 v[58:61], v[86:89], v[74:77], v[58:61]
	v_mfma_f32_16x16x32_f16 v[50:53], v[94:97], v[74:77], v[50:53]
	v_mfma_f32_16x16x32_f16 v[34:37], v[86:89], v[78:81], v[34:37]
	v_mfma_f32_16x16x32_f16 v[26:29], v[94:97], v[78:81], v[26:29]
	v_mfma_f32_16x16x32_f16 v[38:41], v[86:89], v[82:85], v[38:41]
	v_mfma_f32_16x16x32_f16 v[42:45], v[94:97], v[82:85], v[42:45]
	s_add_u32 s28, s2, 0xa80
	s_mov_b32 m0, s14
	s_waitcnt vmcnt(8) lgkmcnt(0)
	s_barrier
	s_addc_u32 s29, s3, 0
	s_add_u32 s30, s4, 0xa80
	global_load_lds_dwordx4 v3, s[28:29]
	s_mov_b32 m0, s6
	s_addc_u32 s31, s5, 0
	global_load_lds_dwordx4 v4, s[28:29]
	s_mov_b32 m0, s7
	s_nop 0
	global_load_lds_dwordx4 v3, s[30:31]
	s_mov_b32 m0, s10
	s_nop 0
	global_load_lds_dwordx4 v4, s[30:31]
	s_waitcnt lgkmcnt(0)
	v_mfma_f32_16x16x32_f16 v[54:57], v[90:93], v[46:49], v[54:57]
	v_mfma_f32_16x16x32_f16 v[30:33], v[98:101], v[46:49], v[30:33]
	ds_read_b128 v[46:49], v9
	ds_read_b128 v[74:77], v10
	ds_read_b128 v[78:81], v11
	ds_read_b128 v[82:85], v12
	ds_read_b128 v[86:89], v13
	ds_read_b128 v[94:97], v14
	v_mfma_f32_16x16x32_f16 v[58:61], v[90:93], v[62:65], v[58:61]
	v_mfma_f32_16x16x32_f16 v[50:53], v[98:101], v[62:65], v[50:53]
	v_mfma_f32_16x16x32_f16 v[34:37], v[90:93], v[66:69], v[34:37]
	v_mfma_f32_16x16x32_f16 v[26:29], v[98:101], v[66:69], v[26:29]
	v_mfma_f32_16x16x32_f16 v[38:41], v[90:93], v[70:73], v[38:41]
	v_mfma_f32_16x16x32_f16 v[42:45], v[98:101], v[70:73], v[42:45]
	s_waitcnt lgkmcnt(0)
	v_mfma_f32_16x16x32_f16 v[54:57], v[86:89], v[46:49], v[54:57]
	v_mfma_f32_16x16x32_f16 v[30:33], v[94:97], v[46:49], v[30:33]
	ds_read_b128 v[46:49], v15
	ds_read_b128 v[62:65], v15 offset:2048
	ds_read_b128 v[66:69], v15 offset:4096
	ds_read_b128 v[70:73], v15 offset:6144
	ds_read_b128 v[90:93], v16
	ds_read_b128 v[98:101], v16 offset:2048
	v_mfma_f32_16x16x32_f16 v[58:61], v[86:89], v[74:77], v[58:61]
	v_mfma_f32_16x16x32_f16 v[50:53], v[94:97], v[74:77], v[50:53]
	v_mfma_f32_16x16x32_f16 v[34:37], v[86:89], v[78:81], v[34:37]
	v_mfma_f32_16x16x32_f16 v[26:29], v[94:97], v[78:81], v[26:29]
	v_mfma_f32_16x16x32_f16 v[38:41], v[86:89], v[82:85], v[38:41]
	v_mfma_f32_16x16x32_f16 v[42:45], v[94:97], v[82:85], v[42:45]
	s_add_u32 s28, s2, 0xb00
	s_mov_b32 m0, s22
	s_waitcnt vmcnt(8) lgkmcnt(0)
	s_barrier
	s_addc_u32 s29, s3, 0
	s_add_u32 s30, s4, 0xb00
	global_load_lds_dwordx4 v3, s[28:29]
	s_mov_b32 m0, s19
	s_addc_u32 s31, s5, 0
	global_load_lds_dwordx4 v4, s[28:29]
	s_mov_b32 m0, s20
	s_nop 0
	global_load_lds_dwordx4 v3, s[30:31]
	s_mov_b32 m0, s21
	s_nop 0
	global_load_lds_dwordx4 v4, s[30:31]
	s_waitcnt lgkmcnt(0)
	v_mfma_f32_16x16x32_f16 v[54:57], v[90:93], v[46:49], v[54:57]
	v_mfma_f32_16x16x32_f16 v[30:33], v[98:101], v[46:49], v[30:33]
	ds_read_b128 v[46:49], v17
	ds_read_b128 v[74:77], v18
	ds_read_b128 v[78:81], v19
	ds_read_b128 v[82:85], v20
	ds_read_b128 v[86:89], v21
	ds_read_b128 v[94:97], v22
	v_mfma_f32_16x16x32_f16 v[58:61], v[90:93], v[62:65], v[58:61]
	v_mfma_f32_16x16x32_f16 v[50:53], v[98:101], v[62:65], v[50:53]
	v_mfma_f32_16x16x32_f16 v[34:37], v[90:93], v[66:69], v[34:37]
	v_mfma_f32_16x16x32_f16 v[26:29], v[98:101], v[66:69], v[26:29]
	v_mfma_f32_16x16x32_f16 v[38:41], v[90:93], v[70:73], v[38:41]
	v_mfma_f32_16x16x32_f16 v[42:45], v[98:101], v[70:73], v[42:45]
	s_waitcnt lgkmcnt(0)
	v_mfma_f32_16x16x32_f16 v[54:57], v[86:89], v[46:49], v[54:57]
	v_mfma_f32_16x16x32_f16 v[30:33], v[94:97], v[46:49], v[30:33]
	ds_read_b128 v[46:49], v23
	ds_read_b128 v[62:65], v23 offset:2048
	ds_read_b128 v[66:69], v23 offset:4096
	ds_read_b128 v[70:73], v23 offset:6144
	ds_read_b128 v[90:93], v24
	ds_read_b128 v[98:101], v24 offset:2048
	v_mfma_f32_16x16x32_f16 v[58:61], v[86:89], v[74:77], v[58:61]
	v_mfma_f32_16x16x32_f16 v[50:53], v[94:97], v[74:77], v[50:53]
	v_mfma_f32_16x16x32_f16 v[34:37], v[86:89], v[78:81], v[34:37]
	v_mfma_f32_16x16x32_f16 v[26:29], v[94:97], v[78:81], v[26:29]
	v_mfma_f32_16x16x32_f16 v[38:41], v[86:89], v[82:85], v[38:41]
	v_mfma_f32_16x16x32_f16 v[42:45], v[94:97], v[82:85], v[42:45]
	s_add_u32 s28, s2, 0xb80
	s_mov_b32 m0, s26
	s_waitcnt vmcnt(8) lgkmcnt(0)
	s_barrier
	s_addc_u32 s29, s3, 0
	s_add_u32 s30, s4, 0xb80
	global_load_lds_dwordx4 v3, s[28:29]
	s_mov_b32 m0, s23
	s_addc_u32 s31, s5, 0
	global_load_lds_dwordx4 v4, s[28:29]
	s_mov_b32 m0, s24
	s_nop 0
	global_load_lds_dwordx4 v3, s[30:31]
	s_mov_b32 m0, s25
	s_nop 0
	global_load_lds_dwordx4 v4, s[30:31]
	s_waitcnt lgkmcnt(0)
	v_mfma_f32_16x16x32_f16 v[54:57], v[90:93], v[46:49], v[54:57]
	v_mfma_f32_16x16x32_f16 v[30:33], v[98:101], v[46:49], v[30:33]
	ds_read_b128 v[46:49], v7
	ds_read_b128 v[74:77], v7 offset:2048
	ds_read_b128 v[78:81], v7 offset:4096
	ds_read_b128 v[82:85], v7 offset:6144
	ds_read_b128 v[86:89], v5 offset:16384
	ds_read_b128 v[94:97], v5 offset:18432
	v_mfma_f32_16x16x32_f16 v[58:61], v[90:93], v[62:65], v[58:61]
	v_mfma_f32_16x16x32_f16 v[50:53], v[98:101], v[62:65], v[50:53]
	v_mfma_f32_16x16x32_f16 v[34:37], v[90:93], v[66:69], v[34:37]
	v_mfma_f32_16x16x32_f16 v[26:29], v[98:101], v[66:69], v[26:29]
	v_mfma_f32_16x16x32_f16 v[38:41], v[90:93], v[70:73], v[38:41]
	v_mfma_f32_16x16x32_f16 v[42:45], v[98:101], v[70:73], v[42:45]
	s_waitcnt lgkmcnt(0)
	v_mfma_f32_16x16x32_f16 v[54:57], v[86:89], v[46:49], v[54:57]
	v_mfma_f32_16x16x32_f16 v[30:33], v[94:97], v[46:49], v[30:33]
	ds_read_b128 v[46:49], v6
	ds_read_b128 v[62:65], v6 offset:2048
	ds_read_b128 v[66:69], v6 offset:4096
	ds_read_b128 v[70:73], v6 offset:6144
	ds_read_b128 v[90:93], v8 offset:16384
	ds_read_b128 v[98:101], v8 offset:18432
	v_mfma_f32_16x16x32_f16 v[58:61], v[86:89], v[74:77], v[58:61]
	v_mfma_f32_16x16x32_f16 v[50:53], v[94:97], v[74:77], v[50:53]
	v_mfma_f32_16x16x32_f16 v[34:37], v[86:89], v[78:81], v[34:37]
	v_mfma_f32_16x16x32_f16 v[26:29], v[94:97], v[78:81], v[26:29]
	v_mfma_f32_16x16x32_f16 v[38:41], v[86:89], v[82:85], v[38:41]
	v_mfma_f32_16x16x32_f16 v[42:45], v[94:97], v[82:85], v[42:45]
	s_add_u32 s28, s2, 0xc00
	s_mov_b32 m0, s18
	s_waitcnt vmcnt(8) lgkmcnt(0)
	s_barrier
	s_addc_u32 s29, s3, 0
	s_add_u32 s30, s4, 0xc00
	global_load_lds_dwordx4 v3, s[28:29]
	s_mov_b32 m0, s15
	s_addc_u32 s31, s5, 0
	global_load_lds_dwordx4 v4, s[28:29]
	s_mov_b32 m0, s16
	s_nop 0
	global_load_lds_dwordx4 v3, s[30:31]
	s_mov_b32 m0, s17
	s_nop 0
	global_load_lds_dwordx4 v4, s[30:31]
	s_waitcnt lgkmcnt(0)
	v_mfma_f32_16x16x32_f16 v[54:57], v[90:93], v[46:49], v[54:57]
	v_mfma_f32_16x16x32_f16 v[30:33], v[98:101], v[46:49], v[30:33]
	ds_read_b128 v[46:49], v7 offset:32768
	ds_read_b128 v[74:77], v7 offset:34816
	ds_read_b128 v[78:81], v7 offset:36864
	ds_read_b128 v[82:85], v7 offset:38912
	ds_read_b128 v[86:89], v5 offset:49152
	ds_read_b128 v[94:97], v5 offset:51200
	v_mfma_f32_16x16x32_f16 v[58:61], v[90:93], v[62:65], v[58:61]
	v_mfma_f32_16x16x32_f16 v[50:53], v[98:101], v[62:65], v[50:53]
	v_mfma_f32_16x16x32_f16 v[34:37], v[90:93], v[66:69], v[34:37]
	v_mfma_f32_16x16x32_f16 v[26:29], v[98:101], v[66:69], v[26:29]
	v_mfma_f32_16x16x32_f16 v[38:41], v[90:93], v[70:73], v[38:41]
	v_mfma_f32_16x16x32_f16 v[42:45], v[98:101], v[70:73], v[42:45]
	s_waitcnt lgkmcnt(0)
	v_mfma_f32_16x16x32_f16 v[54:57], v[86:89], v[46:49], v[54:57]
	v_mfma_f32_16x16x32_f16 v[30:33], v[94:97], v[46:49], v[30:33]
	ds_read_b128 v[46:49], v6 offset:32768
	ds_read_b128 v[62:65], v6 offset:34816
	ds_read_b128 v[66:69], v6 offset:36864
	ds_read_b128 v[70:73], v6 offset:38912
	ds_read_b128 v[90:93], v8 offset:49152
	ds_read_b128 v[98:101], v8 offset:51200
	v_mfma_f32_16x16x32_f16 v[58:61], v[86:89], v[74:77], v[58:61]
	v_mfma_f32_16x16x32_f16 v[50:53], v[94:97], v[74:77], v[50:53]
	v_mfma_f32_16x16x32_f16 v[34:37], v[86:89], v[78:81], v[34:37]
	v_mfma_f32_16x16x32_f16 v[26:29], v[94:97], v[78:81], v[26:29]
	v_mfma_f32_16x16x32_f16 v[38:41], v[86:89], v[82:85], v[38:41]
	v_mfma_f32_16x16x32_f16 v[42:45], v[94:97], v[82:85], v[42:45]
	s_add_u32 s28, s2, 0xc80
	s_mov_b32 m0, s14
	s_waitcnt vmcnt(8) lgkmcnt(0)
	s_barrier
	s_addc_u32 s29, s3, 0
	s_add_u32 s30, s4, 0xc80
	global_load_lds_dwordx4 v3, s[28:29]
	s_mov_b32 m0, s6
	s_addc_u32 s31, s5, 0
	global_load_lds_dwordx4 v4, s[28:29]
	s_mov_b32 m0, s7
	s_nop 0
	global_load_lds_dwordx4 v3, s[30:31]
	s_mov_b32 m0, s10
	s_nop 0
	global_load_lds_dwordx4 v4, s[30:31]
	s_waitcnt lgkmcnt(0)
	v_mfma_f32_16x16x32_f16 v[54:57], v[90:93], v[46:49], v[54:57]
	v_mfma_f32_16x16x32_f16 v[30:33], v[98:101], v[46:49], v[30:33]
	ds_read_b128 v[46:49], v9
	ds_read_b128 v[74:77], v10
	ds_read_b128 v[78:81], v11
	ds_read_b128 v[82:85], v12
	ds_read_b128 v[86:89], v13
	ds_read_b128 v[94:97], v14
	v_mfma_f32_16x16x32_f16 v[58:61], v[90:93], v[62:65], v[58:61]
	v_mfma_f32_16x16x32_f16 v[50:53], v[98:101], v[62:65], v[50:53]
	v_mfma_f32_16x16x32_f16 v[34:37], v[90:93], v[66:69], v[34:37]
	v_mfma_f32_16x16x32_f16 v[26:29], v[98:101], v[66:69], v[26:29]
	v_mfma_f32_16x16x32_f16 v[38:41], v[90:93], v[70:73], v[38:41]
	v_mfma_f32_16x16x32_f16 v[42:45], v[98:101], v[70:73], v[42:45]
	s_waitcnt lgkmcnt(0)
	v_mfma_f32_16x16x32_f16 v[54:57], v[86:89], v[46:49], v[54:57]
	v_mfma_f32_16x16x32_f16 v[30:33], v[94:97], v[46:49], v[30:33]
	ds_read_b128 v[46:49], v15
	ds_read_b128 v[62:65], v15 offset:2048
	ds_read_b128 v[66:69], v15 offset:4096
	ds_read_b128 v[70:73], v15 offset:6144
	ds_read_b128 v[90:93], v16
	ds_read_b128 v[98:101], v16 offset:2048
	v_mfma_f32_16x16x32_f16 v[58:61], v[86:89], v[74:77], v[58:61]
	v_mfma_f32_16x16x32_f16 v[50:53], v[94:97], v[74:77], v[50:53]
	v_mfma_f32_16x16x32_f16 v[34:37], v[86:89], v[78:81], v[34:37]
	v_mfma_f32_16x16x32_f16 v[26:29], v[94:97], v[78:81], v[26:29]
	v_mfma_f32_16x16x32_f16 v[38:41], v[86:89], v[82:85], v[38:41]
	v_mfma_f32_16x16x32_f16 v[42:45], v[94:97], v[82:85], v[42:45]
	s_add_u32 s28, s2, 0xd00
	s_mov_b32 m0, s22
	s_waitcnt vmcnt(8) lgkmcnt(0)
	s_barrier
	s_addc_u32 s29, s3, 0
	s_add_u32 s30, s4, 0xd00
	global_load_lds_dwordx4 v3, s[28:29]
	s_mov_b32 m0, s19
	s_addc_u32 s31, s5, 0
	global_load_lds_dwordx4 v4, s[28:29]
	s_mov_b32 m0, s20
	s_nop 0
	global_load_lds_dwordx4 v3, s[30:31]
	s_mov_b32 m0, s21
	s_nop 0
	global_load_lds_dwordx4 v4, s[30:31]
	s_waitcnt lgkmcnt(0)
	v_mfma_f32_16x16x32_f16 v[54:57], v[90:93], v[46:49], v[54:57]
	v_mfma_f32_16x16x32_f16 v[30:33], v[98:101], v[46:49], v[30:33]
	ds_read_b128 v[46:49], v17
	ds_read_b128 v[74:77], v18
	ds_read_b128 v[78:81], v19
	ds_read_b128 v[82:85], v20
	ds_read_b128 v[86:89], v21
	ds_read_b128 v[94:97], v22
	v_mfma_f32_16x16x32_f16 v[58:61], v[90:93], v[62:65], v[58:61]
	v_mfma_f32_16x16x32_f16 v[50:53], v[98:101], v[62:65], v[50:53]
	v_mfma_f32_16x16x32_f16 v[34:37], v[90:93], v[66:69], v[34:37]
	v_mfma_f32_16x16x32_f16 v[26:29], v[98:101], v[66:69], v[26:29]
	v_mfma_f32_16x16x32_f16 v[38:41], v[90:93], v[70:73], v[38:41]
	v_mfma_f32_16x16x32_f16 v[42:45], v[98:101], v[70:73], v[42:45]
	s_waitcnt lgkmcnt(0)
	v_mfma_f32_16x16x32_f16 v[54:57], v[86:89], v[46:49], v[54:57]
	v_mfma_f32_16x16x32_f16 v[30:33], v[94:97], v[46:49], v[30:33]
	ds_read_b128 v[46:49], v23
	ds_read_b128 v[62:65], v23 offset:2048
	ds_read_b128 v[66:69], v23 offset:4096
	ds_read_b128 v[70:73], v23 offset:6144
	ds_read_b128 v[90:93], v24
	ds_read_b128 v[98:101], v24 offset:2048
	v_mfma_f32_16x16x32_f16 v[58:61], v[86:89], v[74:77], v[58:61]
	v_mfma_f32_16x16x32_f16 v[50:53], v[94:97], v[74:77], v[50:53]
	v_mfma_f32_16x16x32_f16 v[34:37], v[86:89], v[78:81], v[34:37]
	v_mfma_f32_16x16x32_f16 v[26:29], v[94:97], v[78:81], v[26:29]
	v_mfma_f32_16x16x32_f16 v[38:41], v[86:89], v[82:85], v[38:41]
	v_mfma_f32_16x16x32_f16 v[42:45], v[94:97], v[82:85], v[42:45]
	s_add_u32 s28, s2, 0xd80
	s_mov_b32 m0, s26
	s_waitcnt vmcnt(8) lgkmcnt(0)
	s_barrier
	s_addc_u32 s29, s3, 0
	s_add_u32 s30, s4, 0xd80
	global_load_lds_dwordx4 v3, s[28:29]
	s_mov_b32 m0, s23
	s_addc_u32 s31, s5, 0
	global_load_lds_dwordx4 v4, s[28:29]
	s_mov_b32 m0, s24
	s_nop 0
	global_load_lds_dwordx4 v3, s[30:31]
	s_mov_b32 m0, s25
	s_nop 0
	global_load_lds_dwordx4 v4, s[30:31]
	s_waitcnt lgkmcnt(0)
	v_mfma_f32_16x16x32_f16 v[54:57], v[90:93], v[46:49], v[54:57]
	v_mfma_f32_16x16x32_f16 v[30:33], v[98:101], v[46:49], v[30:33]
	ds_read_b128 v[46:49], v7
	ds_read_b128 v[74:77], v7 offset:2048
	ds_read_b128 v[78:81], v7 offset:4096
	ds_read_b128 v[82:85], v7 offset:6144
	ds_read_b128 v[86:89], v5 offset:16384
	ds_read_b128 v[94:97], v5 offset:18432
	v_mfma_f32_16x16x32_f16 v[58:61], v[90:93], v[62:65], v[58:61]
	v_mfma_f32_16x16x32_f16 v[50:53], v[98:101], v[62:65], v[50:53]
	v_mfma_f32_16x16x32_f16 v[34:37], v[90:93], v[66:69], v[34:37]
	v_mfma_f32_16x16x32_f16 v[26:29], v[98:101], v[66:69], v[26:29]
	v_mfma_f32_16x16x32_f16 v[38:41], v[90:93], v[70:73], v[38:41]
	v_mfma_f32_16x16x32_f16 v[42:45], v[98:101], v[70:73], v[42:45]
	s_waitcnt lgkmcnt(0)
	v_mfma_f32_16x16x32_f16 v[54:57], v[86:89], v[46:49], v[54:57]
	v_mfma_f32_16x16x32_f16 v[30:33], v[94:97], v[46:49], v[30:33]
	ds_read_b128 v[46:49], v6
	ds_read_b128 v[62:65], v6 offset:2048
	ds_read_b128 v[66:69], v6 offset:4096
	ds_read_b128 v[70:73], v6 offset:6144
	ds_read_b128 v[90:93], v8 offset:16384
	ds_read_b128 v[98:101], v8 offset:18432
	v_mfma_f32_16x16x32_f16 v[58:61], v[86:89], v[74:77], v[58:61]
	v_mfma_f32_16x16x32_f16 v[50:53], v[94:97], v[74:77], v[50:53]
	v_mfma_f32_16x16x32_f16 v[34:37], v[86:89], v[78:81], v[34:37]
	v_mfma_f32_16x16x32_f16 v[26:29], v[94:97], v[78:81], v[26:29]
	v_mfma_f32_16x16x32_f16 v[38:41], v[86:89], v[82:85], v[38:41]
	v_mfma_f32_16x16x32_f16 v[42:45], v[94:97], v[82:85], v[42:45]
	s_add_u32 s28, s2, 0xe00
	s_mov_b32 m0, s18
	s_waitcnt vmcnt(8) lgkmcnt(0)
	s_barrier
	s_addc_u32 s29, s3, 0
	s_add_u32 s30, s4, 0xe00
	global_load_lds_dwordx4 v3, s[28:29]
	s_mov_b32 m0, s15
	s_addc_u32 s31, s5, 0
	global_load_lds_dwordx4 v4, s[28:29]
	s_mov_b32 m0, s16
	s_nop 0
	global_load_lds_dwordx4 v3, s[30:31]
	s_mov_b32 m0, s17
	s_nop 0
	global_load_lds_dwordx4 v4, s[30:31]
	s_waitcnt lgkmcnt(0)
	v_mfma_f32_16x16x32_f16 v[54:57], v[90:93], v[46:49], v[54:57]
	v_mfma_f32_16x16x32_f16 v[30:33], v[98:101], v[46:49], v[30:33]
	ds_read_b128 v[46:49], v7 offset:32768
	ds_read_b128 v[74:77], v7 offset:34816
	ds_read_b128 v[78:81], v7 offset:36864
	ds_read_b128 v[82:85], v7 offset:38912
	ds_read_b128 v[86:89], v5 offset:49152
	ds_read_b128 v[94:97], v5 offset:51200
	v_mfma_f32_16x16x32_f16 v[58:61], v[90:93], v[62:65], v[58:61]
	v_mfma_f32_16x16x32_f16 v[50:53], v[98:101], v[62:65], v[50:53]
	v_mfma_f32_16x16x32_f16 v[34:37], v[90:93], v[66:69], v[34:37]
	v_mfma_f32_16x16x32_f16 v[26:29], v[98:101], v[66:69], v[26:29]
	v_mfma_f32_16x16x32_f16 v[38:41], v[90:93], v[70:73], v[38:41]
	v_mfma_f32_16x16x32_f16 v[42:45], v[98:101], v[70:73], v[42:45]
	s_waitcnt lgkmcnt(0)
	v_mfma_f32_16x16x32_f16 v[54:57], v[86:89], v[46:49], v[54:57]
	v_mfma_f32_16x16x32_f16 v[30:33], v[94:97], v[46:49], v[30:33]
	ds_read_b128 v[46:49], v6 offset:32768
	ds_read_b128 v[62:65], v6 offset:34816
	ds_read_b128 v[66:69], v6 offset:36864
	ds_read_b128 v[70:73], v6 offset:38912
	ds_read_b128 v[90:93], v8 offset:49152
	ds_read_b128 v[98:101], v8 offset:51200
	v_mfma_f32_16x16x32_f16 v[58:61], v[86:89], v[74:77], v[58:61]
	v_mfma_f32_16x16x32_f16 v[50:53], v[94:97], v[74:77], v[50:53]
	v_mfma_f32_16x16x32_f16 v[34:37], v[86:89], v[78:81], v[34:37]
	v_mfma_f32_16x16x32_f16 v[26:29], v[94:97], v[78:81], v[26:29]
	v_mfma_f32_16x16x32_f16 v[38:41], v[86:89], v[82:85], v[38:41]
	v_mfma_f32_16x16x32_f16 v[42:45], v[94:97], v[82:85], v[42:45]
	s_mov_b32 m0, s14
	s_add_u32 s14, s2, 0xe80
	s_waitcnt vmcnt(8) lgkmcnt(0)
	s_barrier
	s_addc_u32 s15, s3, 0
	s_add_u32 s16, s4, 0xe80
	global_load_lds_dwordx4 v3, s[14:15]
	s_mov_b32 m0, s6
	s_addc_u32 s17, s5, 0
	global_load_lds_dwordx4 v4, s[14:15]
	s_mov_b32 m0, s7
	s_nop 0
	global_load_lds_dwordx4 v3, s[16:17]
	s_mov_b32 m0, s10
	s_nop 0
	global_load_lds_dwordx4 v4, s[16:17]
	s_waitcnt lgkmcnt(0)
	v_mfma_f32_16x16x32_f16 v[54:57], v[90:93], v[46:49], v[54:57]
	v_mfma_f32_16x16x32_f16 v[30:33], v[98:101], v[46:49], v[30:33]
	ds_read_b128 v[46:49], v9
	ds_read_b128 v[74:77], v10
	ds_read_b128 v[78:81], v11
	ds_read_b128 v[82:85], v12
	ds_read_b128 v[86:89], v13
	ds_read_b128 v[94:97], v14
	v_mfma_f32_16x16x32_f16 v[58:61], v[90:93], v[62:65], v[58:61]
	v_mfma_f32_16x16x32_f16 v[50:53], v[98:101], v[62:65], v[50:53]
	v_mfma_f32_16x16x32_f16 v[34:37], v[90:93], v[66:69], v[34:37]
	v_mfma_f32_16x16x32_f16 v[26:29], v[98:101], v[66:69], v[26:29]
	v_mfma_f32_16x16x32_f16 v[38:41], v[90:93], v[70:73], v[38:41]
	v_mfma_f32_16x16x32_f16 v[42:45], v[98:101], v[70:73], v[42:45]
	s_waitcnt lgkmcnt(0)
	v_mfma_f32_16x16x32_f16 v[54:57], v[86:89], v[46:49], v[54:57]
	v_mfma_f32_16x16x32_f16 v[30:33], v[94:97], v[46:49], v[30:33]
	ds_read_b128 v[46:49], v15
	ds_read_b128 v[62:65], v15 offset:2048
	ds_read_b128 v[66:69], v15 offset:4096
	ds_read_b128 v[70:73], v15 offset:6144
	ds_read_b128 v[90:93], v16
	ds_read_b128 v[98:101], v16 offset:2048
	v_mfma_f32_16x16x32_f16 v[58:61], v[86:89], v[74:77], v[58:61]
	v_mfma_f32_16x16x32_f16 v[50:53], v[94:97], v[74:77], v[50:53]
	v_mfma_f32_16x16x32_f16 v[34:37], v[86:89], v[78:81], v[34:37]
	v_mfma_f32_16x16x32_f16 v[26:29], v[94:97], v[78:81], v[26:29]
	v_mfma_f32_16x16x32_f16 v[38:41], v[86:89], v[82:85], v[38:41]
	v_mfma_f32_16x16x32_f16 v[42:45], v[94:97], v[82:85], v[42:45]
	s_add_u32 s6, s2, 0xf00
	s_mov_b32 m0, s22
	s_waitcnt vmcnt(8) lgkmcnt(0)
	s_barrier
	s_addc_u32 s7, s3, 0
	s_add_u32 s14, s4, 0xf00
	global_load_lds_dwordx4 v3, s[6:7]
	s_mov_b32 m0, s19
	s_addc_u32 s15, s5, 0
	global_load_lds_dwordx4 v4, s[6:7]
	s_mov_b32 m0, s20
	s_nop 0
	global_load_lds_dwordx4 v3, s[14:15]
	s_mov_b32 m0, s21
	s_nop 0
	global_load_lds_dwordx4 v4, s[14:15]
	s_waitcnt lgkmcnt(0)
	v_mfma_f32_16x16x32_f16 v[54:57], v[90:93], v[46:49], v[54:57]
	v_mfma_f32_16x16x32_f16 v[30:33], v[98:101], v[46:49], v[30:33]
	ds_read_b128 v[46:49], v17
	ds_read_b128 v[74:77], v18
	ds_read_b128 v[78:81], v19
	ds_read_b128 v[82:85], v20
	ds_read_b128 v[86:89], v21
	ds_read_b128 v[94:97], v22
	v_mfma_f32_16x16x32_f16 v[58:61], v[90:93], v[62:65], v[58:61]
	v_mfma_f32_16x16x32_f16 v[50:53], v[98:101], v[62:65], v[50:53]
	v_mfma_f32_16x16x32_f16 v[34:37], v[90:93], v[66:69], v[34:37]
	v_mfma_f32_16x16x32_f16 v[26:29], v[98:101], v[66:69], v[26:29]
	v_mfma_f32_16x16x32_f16 v[38:41], v[90:93], v[70:73], v[38:41]
	v_mfma_f32_16x16x32_f16 v[42:45], v[98:101], v[70:73], v[42:45]
	s_waitcnt lgkmcnt(0)
	v_mfma_f32_16x16x32_f16 v[54:57], v[86:89], v[46:49], v[54:57]
	v_mfma_f32_16x16x32_f16 v[30:33], v[94:97], v[46:49], v[30:33]
	ds_read_b128 v[46:49], v23
	ds_read_b128 v[62:65], v23 offset:2048
	ds_read_b128 v[66:69], v23 offset:4096
	ds_read_b128 v[70:73], v23 offset:6144
	ds_read_b128 v[90:93], v24
	ds_read_b128 v[98:101], v24 offset:2048
	v_mfma_f32_16x16x32_f16 v[58:61], v[86:89], v[74:77], v[58:61]
	v_mfma_f32_16x16x32_f16 v[50:53], v[94:97], v[74:77], v[50:53]
	v_mfma_f32_16x16x32_f16 v[34:37], v[86:89], v[78:81], v[34:37]
	v_mfma_f32_16x16x32_f16 v[26:29], v[94:97], v[78:81], v[26:29]
	v_mfma_f32_16x16x32_f16 v[38:41], v[86:89], v[82:85], v[38:41]
	v_mfma_f32_16x16x32_f16 v[42:45], v[94:97], v[82:85], v[42:45]
	s_add_u32 s2, s2, 0xf80
	s_mov_b32 m0, s26
	s_waitcnt vmcnt(8) lgkmcnt(0)
	s_barrier
	s_addc_u32 s3, s3, 0
	s_add_u32 s4, s4, 0xf80
	global_load_lds_dwordx4 v3, s[2:3]
	s_mov_b32 m0, s23
	s_addc_u32 s5, s5, 0
	global_load_lds_dwordx4 v4, s[2:3]
	s_mov_b32 m0, s24
	s_nop 0
	global_load_lds_dwordx4 v3, s[4:5]
	s_mov_b32 m0, s25
	s_nop 0
	global_load_lds_dwordx4 v4, s[4:5]
	s_waitcnt lgkmcnt(0)
	v_mfma_f32_16x16x32_f16 v[54:57], v[90:93], v[46:49], v[54:57]
	v_mfma_f32_16x16x32_f16 v[30:33], v[98:101], v[46:49], v[30:33]
	ds_read_b128 v[46:49], v7
	ds_read_b128 v[74:77], v7 offset:2048
	ds_read_b128 v[78:81], v7 offset:4096
	ds_read_b128 v[82:85], v7 offset:6144
	ds_read_b128 v[86:89], v5 offset:16384
	ds_read_b128 v[94:97], v5 offset:18432
	v_mfma_f32_16x16x32_f16 v[58:61], v[90:93], v[62:65], v[58:61]
	v_mfma_f32_16x16x32_f16 v[50:53], v[98:101], v[62:65], v[50:53]
	v_mfma_f32_16x16x32_f16 v[34:37], v[90:93], v[66:69], v[34:37]
	v_mfma_f32_16x16x32_f16 v[26:29], v[98:101], v[66:69], v[26:29]
	v_mfma_f32_16x16x32_f16 v[38:41], v[90:93], v[70:73], v[38:41]
	v_mfma_f32_16x16x32_f16 v[42:45], v[98:101], v[70:73], v[42:45]
	s_waitcnt lgkmcnt(0)
	v_mfma_f32_16x16x32_f16 v[54:57], v[86:89], v[46:49], v[54:57]
	v_mfma_f32_16x16x32_f16 v[30:33], v[94:97], v[46:49], v[30:33]
	ds_read_b128 v[46:49], v6
	ds_read_b128 v[62:65], v6 offset:2048
	ds_read_b128 v[66:69], v6 offset:4096
	ds_read_b128 v[70:73], v6 offset:6144
	ds_read_b128 v[90:93], v8 offset:16384
	ds_read_b128 v[98:101], v8 offset:18432
	v_mfma_f32_16x16x32_f16 v[58:61], v[86:89], v[74:77], v[58:61]
	v_mfma_f32_16x16x32_f16 v[50:53], v[94:97], v[74:77], v[50:53]
	v_mfma_f32_16x16x32_f16 v[34:37], v[86:89], v[78:81], v[34:37]
	v_mfma_f32_16x16x32_f16 v[26:29], v[94:97], v[78:81], v[26:29]
	v_mfma_f32_16x16x32_f16 v[38:41], v[86:89], v[82:85], v[38:41]
	v_mfma_f32_16x16x32_f16 v[42:45], v[94:97], v[82:85], v[42:45]
	s_waitcnt vmcnt(8) lgkmcnt(0)
	s_barrier
	s_waitcnt lgkmcnt(0)
	v_mfma_f32_16x16x32_f16 v[54:57], v[90:93], v[46:49], v[54:57]
	v_mfma_f32_16x16x32_f16 v[30:33], v[98:101], v[46:49], v[30:33]
	ds_read_b128 v[46:49], v7 offset:32768
	ds_read_b128 v[74:77], v7 offset:34816
	ds_read_b128 v[78:81], v7 offset:36864
	ds_read_b128 v[82:85], v7 offset:38912
	ds_read_b128 v[86:89], v5 offset:49152
	ds_read_b128 v[94:97], v5 offset:51200
	v_mfma_f32_16x16x32_f16 v[58:61], v[90:93], v[62:65], v[58:61]
	v_mfma_f32_16x16x32_f16 v[50:53], v[98:101], v[62:65], v[50:53]
	v_mfma_f32_16x16x32_f16 v[34:37], v[90:93], v[66:69], v[34:37]
	v_mfma_f32_16x16x32_f16 v[26:29], v[98:101], v[66:69], v[26:29]
	v_mfma_f32_16x16x32_f16 v[38:41], v[90:93], v[70:73], v[38:41]
	v_mfma_f32_16x16x32_f16 v[42:45], v[98:101], v[70:73], v[42:45]
	s_waitcnt lgkmcnt(0)
	v_mfma_f32_16x16x32_f16 v[54:57], v[86:89], v[46:49], v[54:57]
	v_mfma_f32_16x16x32_f16 v[30:33], v[94:97], v[46:49], v[30:33]
	ds_read_b128 v[46:49], v6 offset:32768
	ds_read_b128 v[62:65], v6 offset:34816
	ds_read_b128 v[66:69], v6 offset:36864
	ds_read_b128 v[4:7], v6 offset:38912
	ds_read_b128 v[70:73], v8 offset:49152
	ds_read_b128 v[90:93], v8 offset:51200
	v_mfma_f32_16x16x32_f16 v[58:61], v[86:89], v[74:77], v[58:61]
	v_mfma_f32_16x16x32_f16 v[50:53], v[94:97], v[74:77], v[50:53]
	v_mfma_f32_16x16x32_f16 v[34:37], v[86:89], v[78:81], v[34:37]
	v_mfma_f32_16x16x32_f16 v[26:29], v[94:97], v[78:81], v[26:29]
	v_mfma_f32_16x16x32_f16 v[38:41], v[86:89], v[82:85], v[38:41]
	v_mfma_f32_16x16x32_f16 v[42:45], v[94:97], v[82:85], v[42:45]
	s_waitcnt vmcnt(0) lgkmcnt(0)
	s_barrier
	s_waitcnt lgkmcnt(0)
	v_mfma_f32_16x16x32_f16 v[54:57], v[70:73], v[46:49], v[54:57]
	v_mfma_f32_16x16x32_f16 v[30:33], v[90:93], v[46:49], v[30:33]
	ds_read_b128 v[46:49], v9
	ds_read_b128 v[74:77], v10
	ds_read_b128 v[8:11], v11
	ds_read_b128 v[78:81], v12
	ds_read_b128 v[82:85], v13
	ds_read_b128 v[86:89], v14
	v_mfma_f32_16x16x32_f16 v[58:61], v[70:73], v[62:65], v[58:61]
	v_mfma_f32_16x16x32_f16 v[50:53], v[90:93], v[62:65], v[50:53]
	v_mfma_f32_16x16x32_f16 v[34:37], v[70:73], v[66:69], v[34:37]
	v_mfma_f32_16x16x32_f16 v[26:29], v[90:93], v[66:69], v[26:29]
	v_mfma_f32_16x16x32_f16 v[38:41], v[70:73], v[4:7], v[38:41]
	v_mfma_f32_16x16x32_f16 v[4:7], v[90:93], v[4:7], v[42:45]
	s_waitcnt lgkmcnt(0)
	v_mfma_f32_16x16x32_f16 v[42:45], v[82:85], v[46:49], v[54:57]
	v_mfma_f32_16x16x32_f16 v[30:33], v[86:89], v[46:49], v[30:33]
	ds_read_b128 v[46:49], v15
	s_nop 0
	ds_read_b128 v[54:57], v15 offset:2048
	ds_read_b128 v[62:65], v15 offset:4096
	ds_read_b128 v[12:15], v15 offset:6144
	ds_read_b128 v[66:69], v16
	ds_read_b128 v[70:73], v16 offset:2048
	v_mfma_f32_16x16x32_f16 v[58:61], v[82:85], v[74:77], v[58:61]
	v_mfma_f32_16x16x32_f16 v[50:53], v[86:89], v[74:77], v[50:53]
	v_mfma_f32_16x16x32_f16 v[34:37], v[82:85], v[8:11], v[34:37]
	v_mfma_f32_16x16x32_f16 v[8:11], v[86:89], v[8:11], v[26:29]
	v_mfma_f32_16x16x32_f16 v[26:29], v[82:85], v[78:81], v[38:41]
	v_mfma_f32_16x16x32_f16 v[4:7], v[86:89], v[78:81], v[4:7]
	s_waitcnt vmcnt(0) lgkmcnt(0)
	s_barrier
	s_waitcnt lgkmcnt(0)
	v_mfma_f32_16x16x32_f16 v[38:41], v[66:69], v[46:49], v[42:45]
	v_mfma_f32_16x16x32_f16 v[30:33], v[70:73], v[46:49], v[30:33]
	s_nop 1
	ds_read_b128 v[42:45], v17
	ds_read_b128 v[46:49], v18
	ds_read_b128 v[16:19], v19
	ds_read_b128 v[74:77], v20
	ds_read_b128 v[78:81], v21
	ds_read_b128 v[82:85], v22
	v_mfma_f32_16x16x32_f16 v[58:61], v[66:69], v[54:57], v[58:61]
	v_mfma_f32_16x16x32_f16 v[50:53], v[70:73], v[54:57], v[50:53]
	v_mfma_f32_16x16x32_f16 v[34:37], v[66:69], v[62:65], v[34:37]
	v_mfma_f32_16x16x32_f16 v[8:11], v[70:73], v[62:65], v[8:11]
	v_mfma_f32_16x16x32_f16 v[26:29], v[66:69], v[12:15], v[26:29]
	v_mfma_f32_16x16x32_f16 v[4:7], v[70:73], v[12:15], v[4:7]
	s_waitcnt lgkmcnt(0)
	v_mfma_f32_16x16x32_f16 v[12:15], v[78:81], v[42:45], v[38:41]
	v_mfma_f32_16x16x32_f16 v[30:33], v[82:85], v[42:45], v[30:33]
	s_nop 1
	ds_read_b128 v[38:41], v23
	ds_read_b128 v[42:45], v23 offset:2048
	ds_read_b128 v[54:57], v23 offset:4096
	ds_read_b128 v[20:23], v23 offset:6144
	ds_read_b128 v[62:65], v24
	ds_read_b128 v[66:69], v24 offset:2048
	v_mfma_f32_16x16x32_f16 v[58:61], v[78:81], v[46:49], v[58:61]
	v_mfma_f32_16x16x32_f16 v[46:49], v[82:85], v[46:49], v[50:53]
	v_mfma_f32_16x16x32_f16 v[34:37], v[78:81], v[16:19], v[34:37]
	v_mfma_f32_16x16x32_f16 v[8:11], v[82:85], v[16:19], v[8:11]
	v_mfma_f32_16x16x32_f16 v[16:19], v[78:81], v[74:77], v[26:29]
	v_mfma_f32_16x16x32_f16 v[4:7], v[82:85], v[74:77], v[4:7]
	s_waitcnt lgkmcnt(0)
	v_mfma_f32_16x16x32_f16 v[12:15], v[62:65], v[38:41], v[12:15]
	v_mfma_f32_16x16x32_f16 v[24:27], v[66:69], v[38:41], v[30:33]
	v_mfma_f32_16x16x32_f16 v[28:31], v[62:65], v[42:45], v[58:61]
	v_mfma_f32_16x16x32_f16 v[38:41], v[66:69], v[42:45], v[46:49]
	v_mfma_f32_16x16x32_f16 v[32:35], v[62:65], v[54:57], v[34:37]
	v_mfma_f32_16x16x32_f16 v[8:11], v[66:69], v[54:57], v[8:11]
	v_mfma_f32_16x16x32_f16 v[16:19], v[62:65], v[20:23], v[16:19]
	v_mfma_f32_16x16x32_f16 v[4:7], v[66:69], v[20:23], v[4:7]
	s_mul_i32 s4, s8, s12
	s_ashr_i32 s3, s9, 31
	s_mul_hi_i32 s2, s8, s12
	s_mul_i32 s3, s4, s3
	s_mul_hi_u32 s5, s4, s9
	s_add_i32 s3, s5, s3
	s_mul_i32 s2, s2, s9
	s_add_i32 s3, s3, s2
	s_mul_i32 s2, s4, s9
	s_lshl_b64 s[2:3], s[2:3], 1
	v_or_b32_e32 v20, s13, v1
	v_lshlrev_b32_e32 v0, 2, v0
	s_add_u32 s0, s0, s2
	v_or3_b32 v21, v0, v2, s11
	s_addc_u32 s1, s1, s3
	v_mad_i64_i32 v[0:1], s[2:3], v20, s9, 0
	v_lshl_add_u64 v[0:1], v[0:1], 1, s[0:1]
	v_cvt_pk_f16_f32 v2, v12, v13
	v_lshlrev_b32_e32 v12, 1, v21
	v_mov_b32_e32 v13, 0
	v_cvt_pk_f16_f32 v3, v14, v15
	v_lshl_add_u64 v[0:1], v[0:1], 0, v[12:13]
	global_store_dwordx2 v[0:1], v[2:3], off
	v_cvt_pk_f16_f32 v3, v26, v27
	v_cvt_pk_f16_f32 v2, v24, v25
	global_store_dwordx2 v[0:1], v[2:3], off offset:32
	v_or_b32_e32 v0, 16, v20
	v_mad_i64_i32 v[0:1], s[2:3], v0, s9, 0
	v_lshl_add_u64 v[0:1], v[0:1], 1, s[0:1]
	v_cvt_pk_f16_f32 v3, v30, v31
	v_cvt_pk_f16_f32 v2, v28, v29
	v_lshl_add_u64 v[0:1], v[0:1], 0, v[12:13]
	global_store_dwordx2 v[0:1], v[2:3], off
	v_cvt_pk_f16_f32 v3, v40, v41
	v_cvt_pk_f16_f32 v2, v38, v39
	global_store_dwordx2 v[0:1], v[2:3], off offset:32
	v_or_b32_e32 v0, 32, v20
	v_mad_i64_i32 v[0:1], s[2:3], v0, s9, 0
	v_lshl_add_u64 v[0:1], v[0:1], 1, s[0:1]
	v_cvt_pk_f16_f32 v3, v34, v35
	v_cvt_pk_f16_f32 v2, v32, v33
	v_lshl_add_u64 v[0:1], v[0:1], 0, v[12:13]
	global_store_dwordx2 v[0:1], v[2:3], off
	v_cvt_pk_f16_f32 v3, v10, v11
	v_cvt_pk_f16_f32 v2, v8, v9
	global_store_dwordx2 v[0:1], v[2:3], off offset:32
	v_or_b32_e32 v0, 48, v20
	v_mad_i64_i32 v[0:1], s[2:3], v0, s9, 0
	v_lshl_add_u64 v[0:1], v[0:1], 1, s[0:1]
	v_cvt_pk_f16_f32 v3, v18, v19
	v_cvt_pk_f16_f32 v2, v16, v17
	v_lshl_add_u64 v[0:1], v[0:1], 0, v[12:13]
	global_store_dwordx2 v[0:1], v[2:3], off
	v_cvt_pk_f16_f32 v3, v6, v7
	v_cvt_pk_f16_f32 v2, v4, v5
	global_store_dwordx2 v[0:1], v[2:3], off offset:32
	s_endpgm
	s_endpgm
	s_endpgm
	s_endpgm
	s_endpgm
	s_endpgm
	s_endpgm
	s_endpgm
	s_endpgm
	s_endpgm
	s_endpgm
	s_endpgm
	s_endpgm
	s_endpgm
	s_endpgm
	s_endpgm
	s_endpgm
	s_endpgm
	s_endpgm
	s_endpgm
	s_endpgm
	s_endpgm
	s_endpgm
	s_endpgm
	s_endpgm
	s_endpgm
	s_endpgm
	s_endpgm
	s_endpgm
	s_endpgm
	s_endpgm
	s_endpgm
	s_endpgm
	s_endpgm
	s_endpgm
	s_endpgm
	s_endpgm
	s_endpgm
	s_endpgm
	s_endpgm
	s_endpgm
	s_endpgm
	s_endpgm
	s_endpgm
	s_endpgm
	s_endpgm
	s_endpgm
	s_endpgm
	.section	.rodata,"a",@progbits
	.p2align	6, 0x0
